# P2 output stores marked nt, plus earlier edits
# baseline (speedup 1.0000x reference)
.LBB0_217:
	v_add_u32_e32 v8, s6, v67
	v_ashrrev_i32_e32 v8, 5, v8
	v_and_b32_e32 v52, -8, v8
	v_add_u32_e32 v12, s96, v8
	v_or_b32_e32 v10, 7, v8
	v_add_u32_e32 v24, -1, v52
	v_mad_i64_i32 v[8:9], s[2:3], v52, s73, v[4:5]
	v_or_b32_e32 v25, 2, v52
	v_or_b32_e32 v26, 3, v52
	v_or_b32_e32 v27, 4, v52
	v_or_b32_e32 v28, 5, v52
	v_or_b32_e32 v29, 6, v52
	v_cmp_gt_u32_e32 vcc, s74, v12
	v_add_u32_e32 v32, s96, v24
	global_load_dword v33, v[8:9], off offset:1024
	global_load_dword v34, v[8:9], off offset:2048
	v_add_u32_e32 v30, 8, v52
	v_or_b32_e32 v13, 1, v52
	v_mad_i64_i32 v[10:11], s[2:3], v10, s73, v[4:5]
	v_cndmask_b32_e64 v31, 0, 1, vcc
	v_mad_i64_i32 v[14:15], s[2:3], v25, s73, v[4:5]
	v_mad_i64_i32 v[16:17], s[2:3], v26, s73, v[4:5]
	v_mad_i64_i32 v[18:19], s[2:3], v27, s73, v[4:5]
	v_mad_i64_i32 v[20:21], s[2:3], v28, s73, v[4:5]
	v_mad_i64_i32 v[22:23], s[2:3], v29, s73, v[4:5]
	v_cndmask_b32_e32 v25, v52, v25, vcc
	v_cndmask_b32_e32 v26, v52, v26, vcc
	v_cndmask_b32_e32 v27, v52, v27, vcc
	v_cndmask_b32_e32 v28, v52, v28, vcc
	v_cmp_gt_u32_e64 s[4:5], s74, v32
	v_add_u32_e32 v35, s96, v30
	v_mad_i64_i32 v[12:13], s[2:3], v13, s73, v[4:5]
	v_or_b32_e32 v31, v52, v31
	v_cndmask_b32_e32 v29, v52, v29, vcc
	v_cndmask_b32_e64 v36, 0, 7, vcc
	global_load_dword v37, v[18:19], off
	global_load_dword v38, v[20:21], off
	global_load_dword v39, v[22:23], off
	global_load_dword v40, v[10:11], off
	v_cndmask_b32_e64 v32, v52, v24, s[4:5]
	v_mad_i64_i32 v[10:11], s[8:9], v25, s73, v[4:5]
	v_mad_i64_i32 v[20:21], s[8:9], v26, s73, v[4:5]
	v_mad_i64_i32 v[22:23], s[8:9], v27, s73, v[4:5]
	v_mad_i64_i32 v[24:25], s[8:9], v28, s73, v[4:5]
	v_cmp_gt_u32_e64 s[2:3], s74, v35
	v_mad_i64_i32 v[18:19], s[8:9], v31, s73, v[4:5]
	v_mad_i64_i32 v[26:27], s[8:9], v29, s73, v[4:5]
	v_or_b32_e32 v35, v36, v52
	v_mad_i64_i32 v[28:29], s[8:9], v32, s73, v[4:5]
	global_load_dword v32, v[10:11], off offset:2048
	global_load_dword v36, v[18:19], off offset:1024
	global_load_dword v41, v[18:19], off offset:2048
	global_load_dword v42, v[10:11], off offset:1024
	global_load_dword v43, v[20:21], off offset:1024
	s_nop 0
	global_load_dword v20, v[20:21], off offset:2048
	s_nop 0
	global_load_dword v21, v[22:23], off offset:1024
	s_nop 0
	global_load_dword v22, v[22:23], off offset:2048
	s_nop 0
	global_load_dword v23, v[24:25], off offset:1024
	s_nop 0
	global_load_dword v24, v[24:25], off offset:2048
	s_nop 0
	global_load_dword v25, v[26:27], off offset:1024
	v_cndmask_b32_e64 v30, v52, v30, s[2:3]
	v_mad_i64_i32 v[30:31], s[8:9], v30, s73, v[4:5]
	v_mad_i64_i32 v[10:11], s[8:9], v35, s73, v[4:5]
	global_load_dword v26, v[26:27], off offset:2048
	s_nop 0
	global_load_dword v27, v[28:29], off offset:1024
	global_load_dword v35, v[8:9], off
	global_load_dword v45, v[12:13], off
	global_load_dword v47, v[14:15], off
	global_load_dword v53, v[28:29], off offset:2048
	global_load_dword v54, v[10:11], off offset:1024
	global_load_dword v55, v[10:11], off offset:2048
	global_load_dword v56, v[30:31], off offset:1024
	global_load_dword v57, v[30:31], off offset:2048
	global_load_dword v58, v[16:17], off
	global_load_dwordx2 v[50:51], v[0:1], off offset:2048
	v_add_u32_e32 v52, s97, v52
	s_addk_i32 s6, 0x200
	s_cmpk_eq_i32 s6, 0x800
	s_waitcnt vmcnt(28)
	v_cndmask_b32_e32 v9, 0, v33, vcc
	s_waitcnt vmcnt(27)
	v_cndmask_b32_e32 v11, 0, v34, vcc
	v_lshlrev_b32_e32 v8, 16, v9
	v_lshlrev_b32_e32 v10, 16, v11
	v_and_b32_e32 v9, 0xffff0000, v9
	v_and_b32_e32 v11, 0xffff0000, v11
	v_pk_mul_f32 v[8:9], v[8:9], v[10:11]
	s_waitcnt vmcnt(26)
	v_lshlrev_b32_e32 v12, 16, v37
	v_and_b32_e32 v13, 0xffff0000, v37
	s_waitcnt vmcnt(24)
	v_lshlrev_b32_e32 v16, 16, v39
	v_and_b32_e32 v17, 0xffff0000, v39
	v_lshlrev_b32_e32 v14, 16, v38
	v_and_b32_e32 v15, 0xffff0000, v38
	s_waitcnt vmcnt(23)
	v_lshlrev_b32_e32 v18, 16, v40
	v_and_b32_e32 v19, 0xffff0000, v40
	s_waitcnt vmcnt(22)
	v_cndmask_b32_e32 v11, 0, v32, vcc
	s_waitcnt vmcnt(21)
	v_cndmask_b32_e32 v28, 0, v36, vcc
	s_waitcnt vmcnt(20)
	v_cndmask_b32_e32 v29, 0, v41, vcc
	s_waitcnt vmcnt(19)
	v_cndmask_b32_e32 v30, 0, v42, vcc
	s_waitcnt vmcnt(18)
	v_cndmask_b32_e32 v31, 0, v43, vcc
	v_lshlrev_b32_e32 v10, 16, v11
	s_waitcnt vmcnt(11)
	v_cndmask_b32_e32 v43, 0, v26, vcc
	v_cndmask_b32_e32 v36, 0, v22, vcc
	v_cndmask_b32_e32 v37, 0, v23, vcc
	v_cndmask_b32_e32 v39, 0, v24, vcc
	v_cndmask_b32_e32 v41, 0, v25, vcc
	s_waitcnt vmcnt(10)
	v_cndmask_b32_e64 v49, 0, v27, s[4:5]
	v_and_b32_e32 v11, 0xffff0000, v11
	v_lshlrev_b32_e32 v22, 16, v28
	v_lshlrev_b32_e32 v24, 16, v29
	v_and_b32_e32 v23, 0xffff0000, v28
	v_and_b32_e32 v25, 0xffff0000, v29
	v_lshlrev_b32_e32 v26, 16, v30
	v_and_b32_e32 v27, 0xffff0000, v30
	v_pk_mul_f32 v[22:23], v[22:23], v[24:25]
	v_pk_mul_f32 v[10:11], v[26:27], v[10:11]
	global_load_dwordx2 v[26:27], v[2:3], off
	global_load_dwordx2 v[24:25], v[0:1], off
	v_cndmask_b32_e32 v32, 0, v20, vcc
	v_cndmask_b32_e32 v33, 0, v21, vcc
	s_waitcnt vmcnt(11)
	v_lshlrev_b32_e32 v20, 16, v35
	v_and_b32_e32 v21, 0xffff0000, v35
	v_lshlrev_b32_e32 v28, 16, v31
	v_lshlrev_b32_e32 v30, 16, v32
	v_and_b32_e32 v29, 0xffff0000, v31
	v_and_b32_e32 v31, 0xffff0000, v32
	v_lshlrev_b32_e32 v32, 16, v33
	v_lshlrev_b32_e32 v34, 16, v36
	v_and_b32_e32 v33, 0xffff0000, v33
	v_and_b32_e32 v35, 0xffff0000, v36
	v_lshlrev_b32_e32 v36, 16, v37
	v_lshlrev_b32_e32 v38, 16, v39
	v_and_b32_e32 v37, 0xffff0000, v37
	v_and_b32_e32 v39, 0xffff0000, v39
	v_lshlrev_b32_e32 v40, 16, v41
	v_lshlrev_b32_e32 v42, 16, v43
	v_and_b32_e32 v41, 0xffff0000, v41
	v_and_b32_e32 v43, 0xffff0000, v43
	s_waitcnt vmcnt(8)
	v_cndmask_b32_e64 v53, 0, v53, s[4:5]
	s_waitcnt vmcnt(7)
	v_cndmask_b32_e32 v54, 0, v54, vcc
	s_waitcnt vmcnt(6)
	v_cndmask_b32_e32 v55, 0, v55, vcc
	s_waitcnt vmcnt(5)
	v_cndmask_b32_e64 v56, 0, v56, s[2:3]
	s_waitcnt vmcnt(4)
	v_cndmask_b32_e64 v57, 0, v57, s[2:3]
	v_lshlrev_b32_e32 v48, 16, v49
	v_and_b32_e32 v49, 0xffff0000, v49
	v_pk_mul_f32 v[28:29], v[28:29], v[30:31]
	v_lshlrev_b32_e32 v30, 16, v53
	v_and_b32_e32 v31, 0xffff0000, v53
	v_pk_mul_f32 v[32:33], v[32:33], v[34:35]
	v_pk_mul_f32 v[34:35], v[36:37], v[38:39]
	v_pk_mul_f32 v[36:37], v[40:41], v[42:43]
	v_lshlrev_b32_e32 v38, 16, v54
	v_lshlrev_b32_e32 v40, 16, v55
	v_and_b32_e32 v39, 0xffff0000, v54
	v_and_b32_e32 v41, 0xffff0000, v55
	v_lshlrev_b32_e32 v42, 16, v56
	v_lshlrev_b32_e32 v54, 16, v57
	v_and_b32_e32 v43, 0xffff0000, v56
	v_and_b32_e32 v55, 0xffff0000, v57
	v_pk_mul_f32 v[30:31], v[48:49], v[30:31]
	v_pk_mul_f32 v[42:43], v[42:43], v[54:55]
	s_waitcnt vmcnt(2)
	v_pk_mul_f32 v[54:55], v[50:51], v[8:9]
	v_pk_mul_f32 v[38:39], v[38:39], v[40:41]
	v_lshlrev_b32_e32 v44, 16, v45
	v_and_b32_e32 v45, 0xffff0000, v45
	v_ashrrev_i32_e32 v53, 31, v52
	v_or_b32_e32 v56, 1, v52
	v_or_b32_e32 v48, 2, v52
	v_or_b32_e32 v40, 3, v52
	v_lshlrev_b32_e32 v46, 16, v47
	v_and_b32_e32 v47, 0xffff0000, v47
	v_ashrrev_i32_e32 v57, 31, v56
	v_ashrrev_i32_e32 v49, 31, v48
	v_ashrrev_i32_e32 v41, 31, v40
	v_lshlrev_b64 v[56:57], 12, v[56:57]
	v_lshlrev_b64 v[48:49], 12, v[48:49]
	v_lshlrev_b64 v[40:41], 12, v[40:41]
	v_lshl_add_u64 v[56:57], v[6:7], 0, v[56:57]
	v_lshl_add_u64 v[48:49], v[6:7], 0, v[48:49]
	v_lshl_add_u64 v[40:41], v[6:7], 0, v[40:41]
	s_waitcnt vmcnt(0)
	v_pk_fma_f32 v[30:31], v[24:25], v[30:31], v[54:55]
	v_pk_mul_f32 v[54:55], v[50:51], v[22:23]
	s_nop 0
	v_pk_fma_f32 v[8:9], v[24:25], v[8:9], v[54:55]
	v_pk_mul_f32 v[54:55], v[50:51], v[10:11]
	v_pk_fma_f32 v[8:9], v[26:27], v[10:11], v[8:9]
	v_pk_fma_f32 v[54:55], v[24:25], v[22:23], v[54:55]
	v_pk_fma_f32 v[22:23], v[26:27], v[22:23], v[30:31]
	v_pk_mul_f32 v[30:31], v[50:51], v[28:29]
	v_pk_mul_f32 v[20:21], v[22:23], v[20:21]
	v_pk_fma_f32 v[30:31], v[24:25], v[10:11], v[30:31]
	v_pk_mul_f32 v[10:11], v[50:51], v[32:33]
	v_pk_fma_f32 v[30:31], v[26:27], v[32:33], v[30:31]
	v_pk_fma_f32 v[10:11], v[24:25], v[28:29], v[10:11]
	v_pk_fma_f32 v[28:29], v[26:27], v[28:29], v[54:55]
	v_pk_mul_f32 v[54:55], v[50:51], v[34:35]
	v_pk_fma_f32 v[10:11], v[26:27], v[34:35], v[10:11]
	v_pk_fma_f32 v[54:55], v[24:25], v[32:33], v[54:55]
	v_pk_mul_f32 v[32:33], v[50:51], v[36:37]
	v_pk_mul_f32 v[50:51], v[50:51], v[38:39]
	v_pk_fma_f32 v[32:33], v[24:25], v[34:35], v[32:33]
	v_pk_fma_f32 v[24:25], v[24:25], v[36:37], v[50:51]
	v_pk_fma_f32 v[36:37], v[26:27], v[36:37], v[54:55]
	v_pk_fma_f32 v[32:33], v[26:27], v[38:39], v[32:33]
	v_or_b32_e32 v38, 7, v52
	v_or_b32_e32 v34, 4, v52
	v_or_b32_e32 v50, 5, v52
	v_or_b32_e32 v54, 6, v52
	v_ashrrev_i32_e32 v39, 31, v38
	v_pk_mul_f32 v[8:9], v[8:9], v[44:45]
	v_pk_mul_f32 v[10:11], v[10:11], v[12:13]
	v_pk_mul_f32 v[12:13], v[36:37], v[14:15]
	v_pk_mul_f32 v[14:15], v[32:33], v[16:17]
	v_pk_fma_f32 v[16:17], v[26:27], v[42:43], v[24:25]
	v_lshlrev_b64 v[52:53], 12, v[52:53]
	v_ashrrev_i32_e32 v35, 31, v34
	v_ashrrev_i32_e32 v51, 31, v50
	v_ashrrev_i32_e32 v55, 31, v54
	v_lshlrev_b64 v[38:39], 12, v[38:39]
	v_lshlrev_b32_e32 v22, 16, v58
	v_and_b32_e32 v23, 0xffff0000, v58
	v_cvt_pk_bf16_f32 v20, v20, v21
	v_cvt_pk_bf16_f32 v21, v8, v9
	v_pk_mul_f32 v[8:9], v[16:17], v[18:19]
	v_lshl_add_u64 v[52:53], v[6:7], 0, v[52:53]
	v_lshlrev_b64 v[34:35], 12, v[34:35]
	v_lshlrev_b64 v[50:51], 12, v[50:51]
	v_lshlrev_b64 v[54:55], 12, v[54:55]
	v_lshl_add_u64 v[38:39], v[6:7], 0, v[38:39]
	v_pk_mul_f32 v[28:29], v[28:29], v[46:47]
	v_pk_mul_f32 v[22:23], v[30:31], v[22:23]
	v_cvt_pk_bf16_f32 v8, v8, v9
	v_lshl_add_u64 v[34:35], v[6:7], 0, v[34:35]
	v_lshl_add_u64 v[50:51], v[6:7], 0, v[50:51]
	v_lshl_add_u64 v[54:55], v[6:7], 0, v[54:55]
	v_cvt_pk_bf16_f32 v24, v28, v29
	v_cvt_pk_bf16_f32 v22, v22, v23
	v_cvt_pk_bf16_f32 v10, v10, v11
	v_cvt_pk_bf16_f32 v11, v12, v13
	v_cvt_pk_bf16_f32 v12, v14, v15
	global_store_dword v[52:53], v20, off nt
	global_store_dword v[56:57], v21, off nt
	global_store_dword v[48:49], v24, off nt
	global_store_dword v[40:41], v22, off nt
	global_store_dword v[34:35], v10, off nt
	global_store_dword v[50:51], v11, off nt
	global_store_dword v[54:55], v12, off nt
	global_store_dword v[38:39], v8, off nt
	s_cbranch_scc0 .LBB0_217
	v_mov_b32_e32 v123, v67
	s_load_dwordx2 s[2:3], s[30:31], 0x8
	s_load_dwordx4 s[8:11], s[30:31], 0x28
	v_ashrrev_i32_e32 v0, 3, v123
	v_add_u32_e32 v2, s97, v0
	v_ashrrev_i32_e32 v3, 31, v2
	v_and_b32_e32 v16, 7, v123
	s_waitcnt lgkmcnt(0)
	v_lshl_add_u64 v[2:3], v[2:3], 2, s[2:3]
	global_load_dword v1, v[2:3], off
	v_lshlrev_b32_e32 v2, 1, v16
	v_cvt_f32_ubyte0_e32 v2, v2
	v_mul_f32_e32 v17, 0xbd800000, v2
	v_cmp_eq_f32_e32 vcc, 0, v17
	v_readfirstlane_b32 s14, v123
	s_waitcnt vmcnt(0)
	v_cvt_f32_i32_e32 v1, v1
	v_cndmask_b32_e64 v12, v110, 1.0, vcc
	v_frexp_mant_f32_e32 v2, v12
	v_cmp_gt_f32_e64 s[2:3], s75, v2
	s_nop 1
	v_cndmask_b32_e64 v3, 1.0, 2.0, s[2:3]
	v_mul_f32_e32 v2, v2, v3
	v_add_f32_e32 v5, 1.0, v2
	v_rcp_f32_e32 v10, v5
	v_add_f32_e32 v3, -1.0, v5
	v_sub_f32_e32 v7, v2, v3
	v_add_f32_e32 v3, -1.0, v2
	v_mul_f32_e32 v11, v3, v10
	v_mul_f32_e32 v4, v5, v11
	v_fma_f32 v6, v11, v5, -v4
	v_fmac_f32_e32 v6, v11, v7
	v_add_f32_e32 v2, v4, v6
	v_sub_f32_e32 v5, v3, v2
	v_pk_add_f32 v[8:9], v[2:3], v[4:5] neg_lo:[0,1] neg_hi:[0,1]
	v_mov_b32_e32 v7, v2
	v_pk_add_f32 v[2:3], v[8:9], v[6:7] neg_lo:[0,1] neg_hi:[0,1]
	s_nop 0
	v_add_f32_e32 v2, v2, v3
	v_add_f32_e32 v2, v5, v2
	v_mul_f32_e32 v3, v10, v2
	v_add_f32_e32 v2, v11, v3
	v_sub_f32_e32 v4, v2, v11
	v_sub_f32_e32 v13, v3, v4
	v_mul_f32_e32 v3, v2, v2
	v_fma_f32 v5, v2, v2, -v3
	v_add_f32_e32 v4, v13, v13
	v_fmac_f32_e32 v5, v2, v4
	v_add_f32_e32 v4, v3, v5
	v_fmamk_f32 v6, v4, 0x3e76c4e1, v104
	v_fmaak_f32 v6, v4, v6, 0x3ecccdef
	v_sub_f32_e32 v3, v4, v3
	v_sub_f32_e32 v14, v5, v3
	v_mul_f32_e32 v3, v4, v6
	v_fma_f32 v5, v4, v6, -v3
	v_fmac_f32_e32 v5, v14, v6
	v_add_f32_e32 v6, v3, v5
	v_add_f32_e32 v7, 0x3f2aaaaa, v6
	v_sub_f32_e32 v3, v6, v3
	v_sub_f32_e32 v3, v5, v3
	v_add_f32_e32 v5, 0xbf2aaaaa, v7
	v_add_f32_e32 v3, 0x31739010, v3
	v_sub_f32_e32 v5, v6, v5
	v_pk_mul_f32 v[8:9], v[2:3], v[4:5]
	v_pk_add_f32 v[10:11], v[2:3], v[4:5]
	v_fma_f32 v6, v4, v2, -v8
	v_fmac_f32_e32 v6, v4, v13
	v_mov_b32_e32 v9, v11
	v_fmac_f32_e32 v6, v14, v2
	v_pk_add_f32 v[4:5], v[8:9], v[6:7]
	v_ldexp_f32 v14, v13, 1
	v_sub_f32_e32 v3, v4, v8
	v_sub_f32_e32 v3, v6, v3
	v_sub_f32_e32 v6, v7, v5
	v_add_f32_e32 v10, v11, v6
	v_pk_mul_f32 v[6:7], v[4:5], v[4:5] op_sel:[0,1] op_sel_hi:[1,0]
	v_cvt_f64_f32_e32 v[8:9], v12
	v_frexp_exp_i32_f64_e32 v7, v[8:9]
	v_subbrev_co_u32_e64 v7, s[2:3], 0, v7, s[2:3]
	v_cvt_f32_i32_e32 v7, v7
	v_fma_f32 v8, v4, v5, -v6
	v_fmac_f32_e32 v8, v4, v10
	v_fmac_f32_e32 v8, v3, v5
	v_mul_f32_e32 v4, 0x3f317218, v7
	v_fma_f32 v10, v7, s76, -v4
	v_fmac_f32_e32 v10, 0xb102e308, v7
	v_ldexp_f32 v11, v2, 1
	v_add_f32_e32 v5, v6, v8
	v_pk_add_f32 v[2:3], v[4:5], v[10:11]
	v_mov_b32_e32 v12, v5
	v_mov_b32_e32 v13, v3
	v_mov_b32_e32 v7, v11
	v_pk_add_f32 v[6:7], v[12:13], v[6:7] neg_lo:[0,1] neg_hi:[0,1]
	v_mov_b32_e32 v9, v5
	v_pk_add_f32 v[6:7], v[8:9], v[6:7] neg_lo:[0,1] neg_hi:[0,1]
	v_mov_b32_e32 v11, v2
	v_add_f32_e32 v5, v14, v6
	v_add_f32_e32 v5, v5, v7
	v_pk_add_f32 v[6:7], v[2:3], v[4:5] neg_lo:[0,1] neg_hi:[0,1]
	v_pk_add_f32 v[8:9], v[2:3], v[4:5]
	v_mov_b32_e32 v4, v5
	v_mov_b32_e32 v7, v9
	v_pk_add_f32 v[12:13], v[10:11], v[6:7] neg_lo:[0,1] neg_hi:[0,1]
	v_pk_add_f32 v[6:7], v[10:11], v[6:7]
	v_mov_b32_e32 v5, v2
	v_pk_add_f32 v[10:11], v[6:7], v[2:3] op_sel:[1,0] op_sel_hi:[0,1] neg_lo:[0,1] neg_hi:[0,1]
	v_pk_add_f32 v[14:15], v[8:9], v[10:11] op_sel_hi:[1,0] neg_lo:[0,1] neg_hi:[0,1]
	v_mov_b32_e32 v8, v9
	v_mov_b32_e32 v9, v7
	v_pk_mov_b32 v[10:11], v[2:3], v[10:11] op_sel:[1,0]
	v_mov_b32_e32 v14, v12
	v_pk_add_f32 v[8:9], v[8:9], v[10:11] neg_lo:[0,1] neg_hi:[0,1]
	v_mov_b32_e32 v13, v7
	v_pk_add_f32 v[2:3], v[4:5], v[8:9] neg_lo:[0,1] neg_hi:[0,1]
	s_nop 0
	v_pk_add_f32 v[4:5], v[14:15], v[2:3]
	s_nop 0
	v_pk_add_f32 v[8:9], v[4:5], v[4:5] op_sel:[0,1] op_sel_hi:[1,0]
	s_nop 0
	v_pk_add_f32 v[6:7], v[6:7], v[8:9] op_sel:[1,0] op_sel_hi:[0,1]
	v_mov_b32_e32 v5, v6
	v_pk_add_f32 v[10:11], v[4:5], v[12:13] neg_lo:[0,1] neg_hi:[0,1]
	v_mov_b32_e32 v3, v8
	v_sub_f32_e32 v4, v4, v10
	v_pk_add_f32 v[2:3], v[2:3], v[10:11] neg_lo:[0,1] neg_hi:[0,1]
	v_sub_f32_e32 v4, v12, v4
	v_add_f32_e32 v2, v2, v4
	v_add_f32_e32 v2, v2, v3
	v_add_f32_e32 v3, v6, v2
	v_sub_f32_e32 v4, v3, v6
	v_sub_f32_e32 v2, v2, v4
	v_mul_f32_e32 v4, v17, v3
	v_fma_f32 v3, v17, v3, -v4
	v_fmac_f32_e32 v3, v17, v2
	v_add_f32_e32 v2, v4, v3
	v_cmp_class_f32_e64 s[2:3], v4, s77
	v_sub_f32_e32 v5, v2, v4
	v_sub_f32_e32 v3, v3, v5
	v_cndmask_b32_e64 v2, v2, v4, s[2:3]
	v_cmp_eq_f32_e64 s[2:3], s79, v2
	s_nop 1
	v_cndmask_b32_e64 v4, 0, v111, s[2:3]
	v_sub_f32_e32 v5, v2, v4
	v_mul_f32_e32 v6, 0x3fb8aa3b, v5
	v_fma_f32 v7, v5, s80, -v6
	v_rndne_f32_e32 v8, v6
	v_fmac_f32_e32 v7, 0x32a5705f, v5
	v_sub_f32_e32 v6, v6, v8
	v_add_f32_e32 v6, v6, v7
	v_exp_f32_e32 v6, v6
	v_cvt_i32_f32_e32 v7, v8
	v_cmp_neq_f32_e64 s[2:3], |v2|, s78
	s_nop 1
	v_cndmask_b32_e64 v2, 0, v3, s[2:3]
	v_ldexp_f32 v3, v6, v7
	v_cmp_ngt_f32_e64 s[2:3], s81, v5
	v_add_f32_e32 v2, v4, v2
	s_nop 0
	v_cndmask_b32_e64 v3, 0, v3, s[2:3]
	v_cmp_nlt_f32_e64 s[2:3], s79, v5
	s_nop 1
	v_cndmask_b32_e64 v3, v112, v3, s[2:3]
	v_fma_f32 v2, v3, v2, v3
	v_cmp_class_f32_e64 s[2:3], v3, s77
	s_nop 1
	v_cndmask_b32_e64 v2, v2, v3, s[2:3]
	v_cmp_neq_f32_e64 s[2:3], v17, |v17|
	s_nop 1
	v_cndmask_b32_e64 v3, v112, 0, s[2:3]
	v_cndmask_b32_e64 v3, v3, 1.0, vcc
	v_cmp_class_f32_e64 s[2:3], v17, s77
	s_nop 1
	v_cndmask_b32_e64 v2, |v2|, v3, s[2:3]
	v_mul_f32_e32 v1, v2, v1
	s_brev_b32 s2, 18
	v_and_b32_e32 v2, 0x7fffffff, v1
	v_cmp_nlt_f32_e64 s[2:3], |v1|, s2
	s_and_saveexec_b64 s[4:5], s[2:3]
	s_xor_b64 s[12:13], exec, s[4:5]
	s_cbranch_execz .LBB0_220
	v_lshrrev_b32_e32 v3, 23, v2
	v_add_u32_e32 v3, 0xffffff88, v3
	v_cmp_lt_u32_e32 vcc, 63, v3
	s_mov_b32 s6, 0xfe5163ab
	s_nop 0
	v_cndmask_b32_e32 v4, 0, v113, vcc
	v_add_u32_e32 v3, v4, v3
	v_cmp_lt_u32_e64 s[2:3], 31, v3
	s_nop 1
	v_cndmask_b32_e64 v4, 0, v114, s[2:3]
	v_add_u32_e32 v3, v4, v3
	v_cmp_lt_u32_e64 s[4:5], 31, v3
	s_nop 1
	v_cndmask_b32_e64 v4, 0, v114, s[4:5]
	v_add_u32_e32 v3, v4, v3
	v_and_b32_e32 v4, 0x7fffff, v2
	v_or_b32_e32 v17, 0x800000, v4
	v_mad_u64_u32 v[4:5], s[6:7], v17, s6, 0
	v_mov_b32_e32 v64, v5
	s_mov_b32 s6, 0x3c439041
	v_mad_u64_u32 v[6:7], s[6:7], v17, s6, v[64:65]
	v_mov_b32_e32 v64, v7
	s_mov_b32 s6, 0xdb629599
	v_mad_u64_u32 v[8:9], s[6:7], v17, s6, v[64:65]
	v_mov_b32_e32 v64, v9
	s_mov_b32 s6, 0xf534ddc0
	v_mad_u64_u32 v[10:11], s[6:7], v17, s6, v[64:65]
	v_mov_b32_e32 v64, v11
	s_mov_b32 s6, 0xfc2757d1
	v_mad_u64_u32 v[12:13], s[6:7], v17, s6, v[64:65]
	v_mov_b32_e32 v64, v13
	s_mov_b32 s6, 0x4e441529
	v_mad_u64_u32 v[14:15], s[6:7], v17, s6, v[64:65]
	v_mov_b32_e32 v64, v15
	s_mov_b32 s6, 0xa2f9836e
	v_mad_u64_u32 v[18:19], s[6:7], v17, s6, v[64:65]
	v_cndmask_b32_e32 v5, v14, v10, vcc
	v_cndmask_b32_e32 v7, v18, v12, vcc
	v_cndmask_b32_e32 v11, v19, v14, vcc
	v_cndmask_b32_e64 v9, v7, v5, s[2:3]
	v_cndmask_b32_e64 v7, v11, v7, s[2:3]
	v_cndmask_b32_e32 v11, v12, v8, vcc
	v_cndmask_b32_e64 v5, v5, v11, s[2:3]
	v_sub_u32_e32 v12, 32, v3
	v_cmp_eq_u32_e64 s[6:7], 0, v3
	v_cndmask_b32_e32 v3, v10, v6, vcc
	v_cndmask_b32_e64 v7, v7, v9, s[4:5]
	v_cndmask_b32_e64 v9, v9, v5, s[4:5]
	v_cndmask_b32_e64 v6, v11, v3, s[2:3]
	v_alignbit_b32 v13, v7, v9, v12
	v_cndmask_b32_e64 v5, v5, v6, s[4:5]
	v_cndmask_b32_e64 v7, v13, v7, s[6:7]
	v_alignbit_b32 v10, v9, v5, v12
	v_cndmask_b32_e32 v4, v8, v4, vcc
	v_cndmask_b32_e64 v9, v10, v9, s[6:7]
	v_bfe_u32 v13, v7, 29, 1
	v_cndmask_b32_e64 v3, v3, v4, s[2:3]
	v_alignbit_b32 v10, v7, v9, 30
	v_sub_u32_e32 v14, 0, v13
	v_cndmask_b32_e64 v3, v6, v3, s[4:5]
	v_xor_b32_e32 v10, v10, v14
	v_alignbit_b32 v4, v5, v3, v12
	v_cndmask_b32_e64 v4, v4, v5, s[6:7]
	v_ffbh_u32_e32 v6, v10
	v_alignbit_b32 v5, v9, v4, 30
	v_min_u32_e32 v6, 32, v6
	v_alignbit_b32 v3, v4, v3, 30
	v_xor_b32_e32 v5, v5, v14
	v_sub_u32_e32 v8, 31, v6
	v_xor_b32_e32 v3, v3, v14
	v_alignbit_b32 v9, v10, v5, v8
	v_alignbit_b32 v3, v5, v3, v8
	v_alignbit_b32 v4, v9, v3, 9
	v_ffbh_u32_e32 v5, v4
	v_min_u32_e32 v5, 32, v5
	v_lshrrev_b32_e32 v11, 29, v7
	v_not_b32_e32 v8, v5
	v_alignbit_b32 v3, v4, v3, v8
	v_lshlrev_b32_e32 v4, 31, v11
	v_or_b32_e32 v8, 0x33000000, v4
	v_add_lshl_u32 v5, v5, v6, 23
	v_lshrrev_b32_e32 v3, 9, v3
	v_sub_u32_e32 v5, v8, v5
	v_or_b32_e32 v4, 0.5, v4
	v_lshlrev_b32_e32 v6, 23, v6
	v_or_b32_e32 v3, v5, v3
	v_lshrrev_b32_e32 v5, 9, v9
	v_sub_u32_e32 v4, v4, v6
	v_or_b32_e32 v4, v5, v4
	v_mul_f32_e32 v5, 0x3fc90fda, v4
	s_mov_b32 s2, 0x3fc90fda
	v_fma_f32 v6, v4, s2, -v5
	v_fmac_f32_e32 v6, 0x33a22168, v4
	v_fmac_f32_e32 v6, 0x3fc90fda, v3
	v_lshrrev_b32_e32 v4, 30, v7
	v_add_f32_e32 v3, v5, v6
	v_add_u32_e32 v4, v13, v4

.LBB0_223:
	s_or_b64 exec, exec, s[8:9]
	s_waitcnt lgkmcnt(5)
	v_cndmask_b32_e64 v26, v119, 1.0, s[6:7]
	s_waitcnt lgkmcnt(4)
	v_pk_mul_f32 v[16:17], v[26:27], v[16:17] op_sel_hi:[0,1]
	v_cvt_pk_bf16_f32 v24, v16, v17
	v_pk_mul_f32 v[16:17], v[26:27], v[18:19] op_sel_hi:[0,1]
	v_cvt_pk_bf16_f32 v25, v16, v17
	v_add_u32_e32 v18, s97, v127
	v_mov_b64_e32 v[16:17], s[38:39]
	v_mad_i64_i32 v[16:17], s[8:9], v18, s83, v[16:17]
	v_cndmask_b32_e64 v18, 0, v120, s[6:7]
	v_mov_b32_e32 v19, v65
	v_lshl_add_u64 v[16:17], v[16:17], 0, v[18:19]
	v_pk_mul_f32 v[22:23], v[26:27], v[22:23] op_sel_hi:[0,1]
	v_pk_mul_f32 v[20:21], v[26:27], v[20:21] op_sel_hi:[0,1]
	v_lshl_add_u64 v[16:17], v[60:61], 1, v[16:17]
	v_add_co_u32_e32 v125, vcc, 12, v125
	v_cvt_pk_bf16_f32 v22, v22, v23
	v_cvt_pk_bf16_f32 v23, v20, v21
	v_lshl_add_u64 v[16:17], v[16:17], 0, v[64:65]
	s_andn2_b64 vcc, exec, vcc
	v_add_u32_e32 v124, 0x300, v124
	global_store_dwordx4 v[16:17], v[22:25], off nt
	s_cbranch_vccnz .LBB0_248

.LBB0_226:
	s_or_b64 exec, exec, s[56:57]
	s_waitcnt vmcnt(10)
	v_lshlrev_b32_e32 v138, 16, v48
	v_and_b32_e32 v139, 0xffff0000, v48
	s_waitcnt lgkmcnt(2)
	v_pk_mul_f32 v[102:103], v[138:139], v[138:139]
	v_lshlrev_b32_e32 v48, 16, v49
	v_and_b32_e32 v49, 0xffff0000, v49
	v_pk_mul_f32 v[140:141], v[48:49], v[48:49]
	s_waitcnt lgkmcnt(0)
	v_add_f32_e32 v97, v102, v103
	v_lshlrev_b32_e32 v142, 16, v50
	v_and_b32_e32 v143, 0xffff0000, v50
	v_add_f32_e32 v97, v140, v97
	v_and_b32_e32 v98, 0xffff0000, v51
	v_lshlrev_b32_e32 v99, 16, v51
	v_pk_mul_f32 v[50:51], v[142:143], v[142:143]
	v_add_f32_e32 v97, v141, v97
	v_add_f32_e32 v50, v50, v97
	v_pk_mul_f32 v[100:101], v[98:99], v[98:99]
	v_add_f32_e32 v50, v51, v50
	v_add_f32_e32 v50, v101, v50
	v_add_f32_e32 v97, v100, v50
	ds_swizzle_b32 v102, v97 offset:swizzle(SWAP,1)
	v_cndmask_b32_e64 v96, v119, 1.0, s[28:29]
	v_pk_mul_f32 v[50:51], v[96:97], v[88:89] op_sel_hi:[0,1]
	v_cvt_pk_bf16_f32 v100, v50, v51
	v_pk_mul_f32 v[50:51], v[96:97], v[92:93] op_sel_hi:[0,1]
	s_waitcnt lgkmcnt(0)
	v_add_f32_e32 v88, v97, v102
	ds_swizzle_b32 v89, v88 offset:swizzle(SWAP,2)
	v_cvt_pk_bf16_f32 v101, v50, v51
	v_pk_mul_f32 v[50:51], v[96:97], v[90:91] op_sel_hi:[0,1]
	v_cvt_pk_bf16_f32 v102, v50, v51
	v_pk_mul_f32 v[50:51], v[96:97], v[94:95] op_sel_hi:[0,1]
	s_waitcnt lgkmcnt(0)
	v_add_f32_e32 v88, v88, v89
	ds_swizzle_b32 v89, v88 offset:swizzle(SWAP,4)
	v_cvt_pk_bf16_f32 v103, v50, v51
	v_add_u32_e32 v90, s97, v137
	v_mov_b64_e32 v[50:51], s[38:39]
	v_mad_i64_i32 v[140:141], s[56:57], v90, s83, v[50:51]
	s_waitcnt lgkmcnt(0)
	v_add_f32_e32 v50, v88, v89
	v_fmamk_f32 v50, v50, 0x3c800000, v107
	v_mul_f32_e32 v51, 0x4f800000, v50
	v_cmp_gt_f32_e32 vcc, s84, v50
	v_cndmask_b32_e64 v144, 0, v120, s[28:29]
	v_mov_b32_e32 v145, v65
	v_cndmask_b32_e32 v50, v50, v51, vcc
	v_sqrt_f32_e32 v88, v50
	v_cndmask_b32_e64 v51, v9, v13, s[26:27]
	v_add_u32_e32 v89, -1, v88
	v_fma_f32 v90, -v89, v88, v50
	v_cmp_ge_f32_e64 s[28:29], 0, v90
	v_add_u32_e32 v90, 1, v88
	s_nop 0
	v_cndmask_b32_e64 v89, v88, v89, s[28:29]
	v_fma_f32 v88, -v90, v88, v50
	v_cmp_lt_f32_e64 s[28:29], 0, v88
	s_nop 1
	v_cndmask_b32_e64 v88, v89, v90, s[28:29]
	v_mul_f32_e32 v89, 0x37800000, v88
	v_cndmask_b32_e32 v88, v88, v89, vcc
	v_cmp_class_f32_e32 vcc, v50, v108
	v_cndmask_b32_e64 v89, v11, v15, s[26:27]
	s_nop 0
	v_cndmask_b32_e32 v90, v88, v50, vcc
	v_div_scale_f32 v91, s[28:29], v90, v90, 1.0
	v_rcp_f32_e32 v92, v91
	v_cndmask_b32_e64 v50, v8, v12, s[26:27]
	v_cndmask_b32_e64 v88, v10, v14, s[26:27]
	v_fma_f32 v93, -v91, v92, 1.0
	v_fmac_f32_e32 v92, v93, v92
	v_div_scale_f32 v93, vcc, 1.0, v90, 1.0
	v_mul_f32_e32 v94, v93, v92
	v_fma_f32 v95, -v91, v94, v93
	v_fmac_f32_e32 v94, v95, v92
	v_fma_f32 v91, -v91, v94, v93
	v_div_fmas_f32 v91, v91, v92, v94
	v_div_fixup_f32 v90, v91, v90, 1.0
	v_pk_mul_f32 v[92:93], v[90:91], v[138:139] op_sel_hi:[0,1]
	v_pk_mul_f32 v[48:49], v[90:91], v[48:49] op_sel_hi:[0,1]
	v_pk_mul_f32 v[50:51], v[50:51], v[92:93]
	v_pk_mul_f32 v[48:49], v[88:89], v[48:49]
	v_pk_mul_f32 v[88:89], v[90:91], v[142:143] op_sel_hi:[0,1]
	v_cndmask_b32_e64 v93, v1, v5, s[26:27]
	v_cndmask_b32_e64 v92, v0, v4, s[26:27]
	v_pk_mul_f32 v[88:89], v[92:93], v[88:89]
	v_pk_mul_f32 v[90:91], v[90:91], v[98:99] op_sel_hi:[0,1]
	v_cndmask_b32_e64 v93, v3, v7, s[26:27]
	v_cndmask_b32_e64 v92, v2, v6, s[26:27]
	v_pk_mul_f32 v[90:91], v[92:93], v[90:91] op_sel:[0,1] op_sel_hi:[1,0]
	ds_swizzle_b32 v92, v50 offset:swizzle(SWAP,1)
	ds_swizzle_b32 v93, v51 offset:swizzle(SWAP,1)
	ds_swizzle_b32 v94, v48 offset:swizzle(SWAP,1)
	ds_swizzle_b32 v95, v49 offset:swizzle(SWAP,1)
	ds_swizzle_b32 v98, v88 offset:swizzle(SWAP,1)
	ds_swizzle_b32 v99, v89 offset:swizzle(SWAP,1)
	ds_swizzle_b32 v96, v90 offset:swizzle(SWAP,1)
	ds_swizzle_b32 v97, v91 offset:swizzle(SWAP,1)
	v_lshl_add_u64 v[138:139], v[140:141], 0, v[144:145]
	v_lshl_add_u64 v[86:87], v[86:87], 1, v[138:139]
	v_lshl_add_u64 v[86:87], v[86:87], 0, v[64:65]
	global_store_dwordx4 v[86:87], v[100:103], off nt
	s_and_saveexec_b64 s[28:29], s[2:3]
	s_cbranch_execz .LBB0_228
	v_lshl_add_u32 v137, v136, 6, s60
	ds_read2_b32 v[86:87], v137 offset0:8 offset1:9
	ds_read2_b32 v[100:101], v137 offset0:10 offset1:11
	ds_read2_b32 v[102:103], v137 offset0:12 offset1:13
	ds_read2_b32 v[138:139], v137 offset0:14 offset1:15
	s_waitcnt lgkmcnt(3)
	v_pk_mul_f32 v[86:87], v[86:87], v[92:93]
	s_waitcnt lgkmcnt(2)
	v_pk_mul_f32 v[92:93], v[100:101], v[94:95]
	s_waitcnt lgkmcnt(1)
	v_pk_mul_f32 v[94:95], v[102:103], v[98:99]
	ds_read2_b32 v[98:99], v137 offset1:1
	ds_read2_b32 v[100:101], v137 offset0:2 offset1:3
	ds_read2_b32 v[102:103], v137 offset0:4 offset1:5
	ds_read2_b32 v[140:141], v137 offset0:6 offset1:7
	s_waitcnt lgkmcnt(4)
	v_pk_mul_f32 v[96:97], v[138:139], v[96:97]
	v_cndmask_b32_e64 v87, v87, -v87, s[4:5]
	v_cndmask_b32_e64 v86, v86, -v86, s[4:5]
	v_cndmask_b32_e64 v93, v93, -v93, s[4:5]
	v_cndmask_b32_e64 v92, v92, -v92, s[4:5]
	v_cndmask_b32_e64 v94, v94, -v94, s[4:5]
	v_cndmask_b32_e64 v95, v95, -v95, s[4:5]
	v_cndmask_b32_e64 v96, v96, -v96, s[4:5]
	v_cndmask_b32_e64 v97, v97, -v97, s[4:5]
	s_waitcnt lgkmcnt(0)
	v_pk_fma_f32 v[90:91], v[90:91], v[140:141], v[96:97]
	v_pk_fma_f32 v[88:89], v[88:89], v[102:103], v[94:95]
	v_pk_fma_f32 v[48:49], v[48:49], v[100:101], v[92:93]
	v_pk_fma_f32 v[50:51], v[50:51], v[98:99], v[86:87]
.LBB0_228:
	s_or_b64 exec, exec, s[28:29]
	s_waitcnt vmcnt(10) lgkmcnt(3)
	v_lshlrev_b32_e32 v98, 16, v56
	s_waitcnt lgkmcnt(2)
	v_and_b32_e32 v99, 0xffff0000, v56
	s_waitcnt lgkmcnt(0)
	v_pk_mul_f32 v[96:97], v[98:99], v[98:99]
	v_lshlrev_b32_e32 v56, 16, v57
	v_and_b32_e32 v57, 0xffff0000, v57
	v_pk_mul_f32 v[100:101], v[56:57], v[56:57]
	v_add_f32_e32 v87, v96, v97
	v_lshlrev_b32_e32 v102, 16, v58
	v_and_b32_e32 v103, 0xffff0000, v58
	v_add_f32_e32 v87, v100, v87
	v_and_b32_e32 v92, 0xffff0000, v59
	v_lshlrev_b32_e32 v93, 16, v59
	v_pk_mul_f32 v[58:59], v[102:103], v[102:103]
	v_add_f32_e32 v87, v101, v87
	v_add_f32_e32 v58, v58, v87
	v_pk_mul_f32 v[94:95], v[92:93], v[92:93]
	v_add_f32_e32 v58, v59, v58
	v_add_f32_e32 v58, v95, v58
	v_add_f32_e32 v58, v94, v58
	ds_swizzle_b32 v59, v58 offset:swizzle(SWAP,1)
	v_cndmask_b32_e64 v86, v119, 1.0, s[26:27]
	v_pk_mul_f32 v[50:51], v[86:87], v[50:51] op_sel_hi:[0,1]
	v_cvt_pk_bf16_f32 v94, v50, v51
	v_pk_mul_f32 v[48:49], v[86:87], v[48:49] op_sel_hi:[0,1]
	s_waitcnt lgkmcnt(0)
	v_add_f32_e32 v50, v58, v59
	ds_swizzle_b32 v51, v50 offset:swizzle(SWAP,2)
	v_cvt_pk_bf16_f32 v95, v48, v49
	v_pk_mul_f32 v[48:49], v[86:87], v[88:89] op_sel_hi:[0,1]
	v_cvt_pk_bf16_f32 v96, v48, v49
	v_pk_mul_f32 v[48:49], v[86:87], v[90:91] op_sel_hi:[0,1]
	s_waitcnt lgkmcnt(0)
	v_add_f32_e32 v50, v50, v51
	ds_swizzle_b32 v51, v50 offset:swizzle(SWAP,4)
	v_cvt_pk_bf16_f32 v97, v48, v49
	v_add_u32_e32 v58, s97, v136
	v_mov_b64_e32 v[48:49], s[38:39]
	v_mad_i64_i32 v[100:101], s[28:29], v58, s83, v[48:49]
	s_waitcnt lgkmcnt(0)
	v_add_f32_e32 v48, v50, v51
	v_fmamk_f32 v48, v48, 0x3c800000, v107
	v_mul_f32_e32 v49, 0x4f800000, v48
	v_cmp_gt_f32_e32 vcc, s84, v48
	v_cndmask_b32_e64 v136, 0, v120, s[26:27]
	v_cndmask_b32_e64 v59, v11, v15, s[24:25]
	v_cndmask_b32_e32 v48, v48, v49, vcc
	v_sqrt_f32_e32 v50, v48
	v_cndmask_b32_e64 v49, v9, v13, s[24:25]
	v_mov_b32_e32 v137, v65
	v_add_u32_e32 v51, -1, v50
	v_fma_f32 v58, -v51, v50, v48
	v_cmp_ge_f32_e64 s[26:27], 0, v58
	v_add_u32_e32 v58, 1, v50
	s_nop 0
	v_cndmask_b32_e64 v51, v50, v51, s[26:27]
	v_fma_f32 v50, -v58, v50, v48
	v_cmp_lt_f32_e64 s[26:27], 0, v50
	s_nop 1
	v_cndmask_b32_e64 v50, v51, v58, s[26:27]
	v_mul_f32_e32 v51, 0x37800000, v50
	v_cndmask_b32_e32 v50, v50, v51, vcc
	v_cmp_class_f32_e32 vcc, v48, v108
	v_cndmask_b32_e64 v58, v10, v14, s[24:25]
	s_nop 0
	v_cndmask_b32_e32 v50, v50, v48, vcc
	v_div_scale_f32 v51, s[26:27], v50, v50, 1.0
	v_rcp_f32_e32 v86, v51
	v_cndmask_b32_e64 v48, v8, v12, s[24:25]
	v_fma_f32 v87, -v51, v86, 1.0
	v_fmac_f32_e32 v86, v87, v86
	v_div_scale_f32 v87, vcc, 1.0, v50, 1.0
	v_mul_f32_e32 v88, v87, v86
	v_fma_f32 v89, -v51, v88, v87
	v_fmac_f32_e32 v88, v89, v86
	v_fma_f32 v51, -v51, v88, v87
	v_div_fmas_f32 v51, v51, v86, v88
	v_div_fixup_f32 v86, v51, v50, 1.0
	v_pk_mul_f32 v[50:51], v[86:87], v[98:99] op_sel_hi:[0,1]
	v_pk_mul_f32 v[50:51], v[48:49], v[50:51]
	v_pk_mul_f32 v[48:49], v[86:87], v[56:57] op_sel_hi:[0,1]
	v_pk_mul_f32 v[48:49], v[58:59], v[48:49]
	v_pk_mul_f32 v[56:57], v[86:87], v[102:103] op_sel_hi:[0,1]
	v_cndmask_b32_e64 v59, v1, v5, s[24:25]
	v_cndmask_b32_e64 v58, v0, v4, s[24:25]
	v_pk_mul_f32 v[56:57], v[58:59], v[56:57]
	v_pk_mul_f32 v[58:59], v[86:87], v[92:93] op_sel_hi:[0,1]
	v_cndmask_b32_e64 v87, v3, v7, s[24:25]
	v_cndmask_b32_e64 v86, v2, v6, s[24:25]
	v_pk_mul_f32 v[58:59], v[86:87], v[58:59] op_sel:[0,1] op_sel_hi:[1,0]
	ds_swizzle_b32 v86, v50 offset:swizzle(SWAP,1)
	ds_swizzle_b32 v87, v51 offset:swizzle(SWAP,1)
	ds_swizzle_b32 v88, v48 offset:swizzle(SWAP,1)
	ds_swizzle_b32 v89, v49 offset:swizzle(SWAP,1)
	ds_swizzle_b32 v92, v56 offset:swizzle(SWAP,1)
	ds_swizzle_b32 v93, v57 offset:swizzle(SWAP,1)
	ds_swizzle_b32 v90, v58 offset:swizzle(SWAP,1)
	ds_swizzle_b32 v91, v59 offset:swizzle(SWAP,1)
	v_lshl_add_u64 v[98:99], v[100:101], 0, v[136:137]
	v_lshl_add_u64 v[84:85], v[84:85], 1, v[98:99]
	v_lshl_add_u64 v[84:85], v[84:85], 0, v[64:65]
	global_store_dwordx4 v[84:85], v[94:97], off nt
	s_and_saveexec_b64 s[26:27], s[2:3]
	s_cbranch_execz .LBB0_230
	v_lshl_add_u32 v100, v135, 6, s60
	ds_read2_b32 v[84:85], v100 offset0:8 offset1:9
	ds_read2_b32 v[94:95], v100 offset0:10 offset1:11
	ds_read2_b32 v[96:97], v100 offset0:12 offset1:13
	ds_read2_b32 v[98:99], v100 offset0:14 offset1:15
	s_waitcnt lgkmcnt(3)
	v_pk_mul_f32 v[84:85], v[84:85], v[86:87]
	s_waitcnt lgkmcnt(2)
	v_pk_mul_f32 v[86:87], v[94:95], v[88:89]
	s_waitcnt lgkmcnt(1)
	v_pk_mul_f32 v[88:89], v[96:97], v[92:93]
	ds_read2_b32 v[92:93], v100 offset1:1
	ds_read2_b32 v[94:95], v100 offset0:2 offset1:3
	ds_read2_b32 v[96:97], v100 offset0:4 offset1:5
	ds_read2_b32 v[100:101], v100 offset0:6 offset1:7
	s_waitcnt lgkmcnt(4)
	v_pk_mul_f32 v[90:91], v[98:99], v[90:91]
	v_cndmask_b32_e64 v85, v85, -v85, s[4:5]
	v_cndmask_b32_e64 v84, v84, -v84, s[4:5]
	v_cndmask_b32_e64 v87, v87, -v87, s[4:5]
	v_cndmask_b32_e64 v86, v86, -v86, s[4:5]
	v_cndmask_b32_e64 v88, v88, -v88, s[4:5]
	v_cndmask_b32_e64 v89, v89, -v89, s[4:5]
	v_cndmask_b32_e64 v90, v90, -v90, s[4:5]
	v_cndmask_b32_e64 v91, v91, -v91, s[4:5]
	s_waitcnt lgkmcnt(0)
	v_pk_fma_f32 v[58:59], v[58:59], v[100:101], v[90:91]
	v_pk_fma_f32 v[56:57], v[56:57], v[96:97], v[88:89]
	v_pk_fma_f32 v[48:49], v[48:49], v[94:95], v[86:87]
	v_pk_fma_f32 v[50:51], v[50:51], v[92:93], v[84:85]
.LBB0_230:
	s_or_b64 exec, exec, s[26:27]
	s_waitcnt vmcnt(10) lgkmcnt(3)
	v_lshlrev_b32_e32 v92, 16, v52
	s_waitcnt lgkmcnt(2)
	v_and_b32_e32 v93, 0xffff0000, v52
	s_waitcnt lgkmcnt(0)
	v_pk_mul_f32 v[90:91], v[92:93], v[92:93]
	v_lshlrev_b32_e32 v52, 16, v53
	v_and_b32_e32 v53, 0xffff0000, v53
	v_pk_mul_f32 v[94:95], v[52:53], v[52:53]
	v_add_f32_e32 v85, v90, v91
	v_lshlrev_b32_e32 v96, 16, v54
	v_and_b32_e32 v97, 0xffff0000, v54
	v_add_f32_e32 v85, v94, v85
	v_and_b32_e32 v86, 0xffff0000, v55
	v_lshlrev_b32_e32 v87, 16, v55
	v_pk_mul_f32 v[54:55], v[96:97], v[96:97]
	v_add_f32_e32 v85, v95, v85
	v_add_f32_e32 v54, v54, v85
	v_pk_mul_f32 v[88:89], v[86:87], v[86:87]
	v_add_f32_e32 v54, v55, v54
	v_add_f32_e32 v54, v89, v54
	v_add_f32_e32 v54, v88, v54
	ds_swizzle_b32 v55, v54 offset:swizzle(SWAP,1)
	v_cndmask_b32_e64 v84, v119, 1.0, s[24:25]
	v_pk_mul_f32 v[50:51], v[84:85], v[50:51] op_sel_hi:[0,1]
	v_cvt_pk_bf16_f32 v88, v50, v51
	v_pk_mul_f32 v[48:49], v[84:85], v[48:49] op_sel_hi:[0,1]
	s_waitcnt lgkmcnt(0)
	v_add_f32_e32 v50, v54, v55
	ds_swizzle_b32 v51, v50 offset:swizzle(SWAP,2)
	v_cvt_pk_bf16_f32 v89, v48, v49
	v_pk_mul_f32 v[48:49], v[84:85], v[56:57] op_sel_hi:[0,1]
	v_cvt_pk_bf16_f32 v90, v48, v49
	v_pk_mul_f32 v[48:49], v[84:85], v[58:59] op_sel_hi:[0,1]
	s_waitcnt lgkmcnt(0)
	v_add_f32_e32 v50, v50, v51
	ds_swizzle_b32 v51, v50 offset:swizzle(SWAP,4)
	v_cvt_pk_bf16_f32 v91, v48, v49
	v_add_u32_e32 v54, s97, v135
	v_mov_b64_e32 v[48:49], s[38:39]
	v_mad_i64_i32 v[94:95], s[26:27], v54, s83, v[48:49]
	s_waitcnt lgkmcnt(0)
	v_add_f32_e32 v48, v50, v51
	v_fmamk_f32 v48, v48, 0x3c800000, v107
	v_mul_f32_e32 v49, 0x4f800000, v48
	v_cmp_gt_f32_e32 vcc, s84, v48
	v_cndmask_b32_e64 v98, 0, v120, s[24:25]
	v_cndmask_b32_e64 v55, v11, v15, s[22:23]
	v_cndmask_b32_e32 v48, v48, v49, vcc
	v_sqrt_f32_e32 v50, v48
	v_cndmask_b32_e64 v49, v9, v13, s[22:23]
	v_mov_b32_e32 v99, v65
	v_add_u32_e32 v51, -1, v50
	v_fma_f32 v54, -v51, v50, v48
	v_cmp_ge_f32_e64 s[24:25], 0, v54
	v_add_u32_e32 v54, 1, v50
	s_nop 0
	v_cndmask_b32_e64 v51, v50, v51, s[24:25]
	v_fma_f32 v50, -v54, v50, v48
	v_cmp_lt_f32_e64 s[24:25], 0, v50
	s_nop 1
	v_cndmask_b32_e64 v50, v51, v54, s[24:25]
	v_mul_f32_e32 v51, 0x37800000, v50
	v_cndmask_b32_e32 v50, v50, v51, vcc
	v_cmp_class_f32_e32 vcc, v48, v108
	v_cndmask_b32_e64 v54, v10, v14, s[22:23]
	s_nop 0
	v_cndmask_b32_e32 v50, v50, v48, vcc
	v_div_scale_f32 v51, s[24:25], v50, v50, 1.0
	v_rcp_f32_e32 v56, v51
	v_cndmask_b32_e64 v48, v8, v12, s[22:23]
	v_fma_f32 v57, -v51, v56, 1.0
	v_fmac_f32_e32 v56, v57, v56
	v_div_scale_f32 v57, vcc, 1.0, v50, 1.0
	v_mul_f32_e32 v58, v57, v56
	v_fma_f32 v59, -v51, v58, v57
	v_fmac_f32_e32 v58, v59, v56
	v_fma_f32 v51, -v51, v58, v57
	v_div_fmas_f32 v51, v51, v56, v58
	v_div_fixup_f32 v56, v51, v50, 1.0
	v_pk_mul_f32 v[50:51], v[56:57], v[92:93] op_sel_hi:[0,1]
	v_pk_mul_f32 v[50:51], v[48:49], v[50:51]
	v_pk_mul_f32 v[48:49], v[56:57], v[52:53] op_sel_hi:[0,1]
	v_pk_mul_f32 v[48:49], v[54:55], v[48:49]
	v_pk_mul_f32 v[52:53], v[56:57], v[96:97] op_sel_hi:[0,1]
	v_cndmask_b32_e64 v55, v1, v5, s[22:23]
	v_cndmask_b32_e64 v54, v0, v4, s[22:23]
	v_pk_mul_f32 v[52:53], v[54:55], v[52:53]
	v_pk_mul_f32 v[54:55], v[56:57], v[86:87] op_sel_hi:[0,1]
	v_cndmask_b32_e64 v57, v3, v7, s[22:23]
	v_cndmask_b32_e64 v56, v2, v6, s[22:23]
	v_pk_mul_f32 v[54:55], v[56:57], v[54:55] op_sel:[0,1] op_sel_hi:[1,0]
	ds_swizzle_b32 v56, v50 offset:swizzle(SWAP,1)
	ds_swizzle_b32 v57, v51 offset:swizzle(SWAP,1)
	ds_swizzle_b32 v58, v48 offset:swizzle(SWAP,1)
	ds_swizzle_b32 v59, v49 offset:swizzle(SWAP,1)
	ds_swizzle_b32 v86, v52 offset:swizzle(SWAP,1)
	ds_swizzle_b32 v87, v53 offset:swizzle(SWAP,1)
	ds_swizzle_b32 v84, v54 offset:swizzle(SWAP,1)
	ds_swizzle_b32 v85, v55 offset:swizzle(SWAP,1)
	v_lshl_add_u64 v[92:93], v[94:95], 0, v[98:99]
	v_lshl_add_u64 v[82:83], v[82:83], 1, v[92:93]
	v_lshl_add_u64 v[82:83], v[82:83], 0, v[64:65]
	global_store_dwordx4 v[82:83], v[88:91], off nt
	s_and_saveexec_b64 s[24:25], s[2:3]
	s_cbranch_execz .LBB0_232
	v_lshl_add_u32 v94, v134, 6, s60
	ds_read2_b32 v[82:83], v94 offset0:8 offset1:9
	ds_read2_b32 v[88:89], v94 offset0:10 offset1:11
	ds_read2_b32 v[90:91], v94 offset0:12 offset1:13
	ds_read2_b32 v[92:93], v94 offset0:14 offset1:15
	s_waitcnt lgkmcnt(3)
	v_pk_mul_f32 v[56:57], v[82:83], v[56:57]
	s_waitcnt lgkmcnt(2)
	v_pk_mul_f32 v[58:59], v[88:89], v[58:59]
	s_waitcnt lgkmcnt(1)
	v_pk_mul_f32 v[82:83], v[90:91], v[86:87]
	ds_read2_b32 v[86:87], v94 offset1:1
	ds_read2_b32 v[88:89], v94 offset0:2 offset1:3
	ds_read2_b32 v[90:91], v94 offset0:4 offset1:5
	ds_read2_b32 v[94:95], v94 offset0:6 offset1:7
	s_waitcnt lgkmcnt(4)
	v_pk_mul_f32 v[84:85], v[92:93], v[84:85]
	v_cndmask_b32_e64 v57, v57, -v57, s[4:5]
	v_cndmask_b32_e64 v56, v56, -v56, s[4:5]
	v_cndmask_b32_e64 v59, v59, -v59, s[4:5]
	v_cndmask_b32_e64 v58, v58, -v58, s[4:5]
	v_cndmask_b32_e64 v82, v82, -v82, s[4:5]
	v_cndmask_b32_e64 v83, v83, -v83, s[4:5]
	v_cndmask_b32_e64 v84, v84, -v84, s[4:5]
	v_cndmask_b32_e64 v85, v85, -v85, s[4:5]
	s_waitcnt lgkmcnt(0)
	v_pk_fma_f32 v[54:55], v[54:55], v[94:95], v[84:85]
	v_pk_fma_f32 v[52:53], v[52:53], v[90:91], v[82:83]
	v_pk_fma_f32 v[48:49], v[48:49], v[88:89], v[58:59]
	v_pk_fma_f32 v[50:51], v[50:51], v[86:87], v[56:57]
.LBB0_232:
	s_or_b64 exec, exec, s[24:25]
	s_waitcnt vmcnt(10) lgkmcnt(3)
	v_lshlrev_b32_e32 v86, 16, v44
	s_waitcnt lgkmcnt(2)
	v_and_b32_e32 v87, 0xffff0000, v44
	s_waitcnt lgkmcnt(0)
	v_pk_mul_f32 v[84:85], v[86:87], v[86:87]
	v_lshlrev_b32_e32 v44, 16, v45
	v_and_b32_e32 v45, 0xffff0000, v45
	v_pk_mul_f32 v[88:89], v[44:45], v[44:45]
	v_add_f32_e32 v57, v84, v85
	v_lshlrev_b32_e32 v90, 16, v46
	v_and_b32_e32 v91, 0xffff0000, v46
	v_add_f32_e32 v57, v88, v57
	v_and_b32_e32 v58, 0xffff0000, v47
	v_lshlrev_b32_e32 v59, 16, v47
	v_pk_mul_f32 v[46:47], v[90:91], v[90:91]
	v_add_f32_e32 v57, v89, v57
	v_add_f32_e32 v46, v46, v57
	v_pk_mul_f32 v[82:83], v[58:59], v[58:59]
	v_add_f32_e32 v46, v47, v46
	v_add_f32_e32 v46, v83, v46
	v_add_f32_e32 v57, v82, v46
	ds_swizzle_b32 v84, v57 offset:swizzle(SWAP,1)
	v_cndmask_b32_e64 v56, v119, 1.0, s[22:23]
	v_pk_mul_f32 v[46:47], v[56:57], v[50:51] op_sel_hi:[0,1]
	v_cvt_pk_bf16_f32 v82, v46, v47
	v_pk_mul_f32 v[46:47], v[56:57], v[48:49] op_sel_hi:[0,1]
	s_waitcnt lgkmcnt(0)
	v_add_f32_e32 v48, v57, v84
	ds_swizzle_b32 v49, v48 offset:swizzle(SWAP,2)
	v_cvt_pk_bf16_f32 v83, v46, v47
	v_pk_mul_f32 v[46:47], v[56:57], v[52:53] op_sel_hi:[0,1]
	v_cvt_pk_bf16_f32 v84, v46, v47
	v_pk_mul_f32 v[46:47], v[56:57], v[54:55] op_sel_hi:[0,1]
	s_waitcnt lgkmcnt(0)
	v_add_f32_e32 v48, v48, v49
	ds_swizzle_b32 v49, v48 offset:swizzle(SWAP,4)
	v_cvt_pk_bf16_f32 v85, v46, v47
	v_add_u32_e32 v50, s97, v134
	v_mov_b64_e32 v[46:47], s[38:39]
	v_mad_i64_i32 v[88:89], s[24:25], v50, s83, v[46:47]
	s_waitcnt lgkmcnt(0)
	v_add_f32_e32 v46, v48, v49
	v_fmamk_f32 v46, v46, 0x3c800000, v107
	v_mul_f32_e32 v47, 0x4f800000, v46
	v_cmp_gt_f32_e32 vcc, s84, v46
	v_cndmask_b32_e64 v92, 0, v120, s[22:23]
	v_mov_b32_e32 v93, v65
	v_cndmask_b32_e32 v46, v46, v47, vcc
	v_sqrt_f32_e32 v48, v46
	v_cndmask_b32_e64 v47, v9, v13, s[20:21]
	v_add_u32_e32 v49, -1, v48
	v_fma_f32 v50, -v49, v48, v46
	v_cmp_ge_f32_e64 s[22:23], 0, v50
	v_add_u32_e32 v50, 1, v48
	s_nop 0
	v_cndmask_b32_e64 v49, v48, v49, s[22:23]
	v_fma_f32 v48, -v50, v48, v46
	v_cmp_lt_f32_e64 s[22:23], 0, v48
	s_nop 1
	v_cndmask_b32_e64 v48, v49, v50, s[22:23]
	v_mul_f32_e32 v49, 0x37800000, v48
	v_cndmask_b32_e32 v48, v48, v49, vcc
	v_cmp_class_f32_e32 vcc, v46, v108
	v_cndmask_b32_e64 v49, v11, v15, s[20:21]
	s_nop 0
	v_cndmask_b32_e32 v50, v48, v46, vcc
	v_div_scale_f32 v51, s[22:23], v50, v50, 1.0
	v_rcp_f32_e32 v52, v51
	v_cndmask_b32_e64 v46, v8, v12, s[20:21]
	v_cndmask_b32_e64 v48, v10, v14, s[20:21]
	v_fma_f32 v53, -v51, v52, 1.0
	v_fmac_f32_e32 v52, v53, v52
	v_div_scale_f32 v53, vcc, 1.0, v50, 1.0
	v_mul_f32_e32 v54, v53, v52
	v_fma_f32 v55, -v51, v54, v53
	v_fmac_f32_e32 v54, v55, v52
	v_fma_f32 v51, -v51, v54, v53
	v_div_fmas_f32 v51, v51, v52, v54
	v_div_fixup_f32 v50, v51, v50, 1.0
	v_pk_mul_f32 v[52:53], v[50:51], v[86:87] op_sel_hi:[0,1]
	v_pk_mul_f32 v[44:45], v[50:51], v[44:45] op_sel_hi:[0,1]
	v_pk_mul_f32 v[46:47], v[46:47], v[52:53]
	v_pk_mul_f32 v[44:45], v[48:49], v[44:45]
	v_pk_mul_f32 v[48:49], v[50:51], v[90:91] op_sel_hi:[0,1]
	v_cndmask_b32_e64 v53, v1, v5, s[20:21]
	v_cndmask_b32_e64 v52, v0, v4, s[20:21]
	v_pk_mul_f32 v[48:49], v[52:53], v[48:49]
	v_pk_mul_f32 v[50:51], v[50:51], v[58:59] op_sel_hi:[0,1]
	v_cndmask_b32_e64 v53, v3, v7, s[20:21]
	v_cndmask_b32_e64 v52, v2, v6, s[20:21]
	v_pk_mul_f32 v[50:51], v[52:53], v[50:51] op_sel:[0,1] op_sel_hi:[1,0]
	ds_swizzle_b32 v52, v46 offset:swizzle(SWAP,1)
	ds_swizzle_b32 v53, v47 offset:swizzle(SWAP,1)
	ds_swizzle_b32 v54, v44 offset:swizzle(SWAP,1)
	ds_swizzle_b32 v55, v45 offset:swizzle(SWAP,1)
	ds_swizzle_b32 v58, v48 offset:swizzle(SWAP,1)
	ds_swizzle_b32 v59, v49 offset:swizzle(SWAP,1)
	ds_swizzle_b32 v56, v50 offset:swizzle(SWAP,1)
	ds_swizzle_b32 v57, v51 offset:swizzle(SWAP,1)
	v_lshl_add_u64 v[86:87], v[88:89], 0, v[92:93]
	v_lshl_add_u64 v[80:81], v[80:81], 1, v[86:87]
	v_lshl_add_u64 v[80:81], v[80:81], 0, v[64:65]
	global_store_dwordx4 v[80:81], v[82:85], off nt
	s_and_saveexec_b64 s[22:23], s[2:3]
	s_cbranch_execz .LBB0_234
	v_lshl_add_u32 v88, v133, 6, s60
	ds_read2_b32 v[80:81], v88 offset0:8 offset1:9
	ds_read2_b32 v[82:83], v88 offset0:10 offset1:11
	ds_read2_b32 v[84:85], v88 offset0:12 offset1:13
	ds_read2_b32 v[86:87], v88 offset0:14 offset1:15
	s_waitcnt lgkmcnt(3)
	v_pk_mul_f32 v[52:53], v[80:81], v[52:53]
	s_waitcnt lgkmcnt(2)
	v_pk_mul_f32 v[54:55], v[82:83], v[54:55]
	s_waitcnt lgkmcnt(1)
	v_pk_mul_f32 v[58:59], v[84:85], v[58:59]
	ds_read2_b32 v[80:81], v88 offset1:1
	ds_read2_b32 v[82:83], v88 offset0:2 offset1:3
	ds_read2_b32 v[84:85], v88 offset0:4 offset1:5
	ds_read2_b32 v[88:89], v88 offset0:6 offset1:7
	s_waitcnt lgkmcnt(4)
	v_pk_mul_f32 v[56:57], v[86:87], v[56:57]
	v_cndmask_b32_e64 v53, v53, -v53, s[4:5]
	v_cndmask_b32_e64 v52, v52, -v52, s[4:5]
	v_cndmask_b32_e64 v55, v55, -v55, s[4:5]
	v_cndmask_b32_e64 v54, v54, -v54, s[4:5]
	v_cndmask_b32_e64 v58, v58, -v58, s[4:5]
	v_cndmask_b32_e64 v59, v59, -v59, s[4:5]
	v_cndmask_b32_e64 v56, v56, -v56, s[4:5]
	v_cndmask_b32_e64 v57, v57, -v57, s[4:5]
	s_waitcnt lgkmcnt(0)
	v_pk_fma_f32 v[50:51], v[50:51], v[88:89], v[56:57]
	v_pk_fma_f32 v[48:49], v[48:49], v[84:85], v[58:59]
	v_pk_fma_f32 v[44:45], v[44:45], v[82:83], v[54:55]
	v_pk_fma_f32 v[46:47], v[46:47], v[80:81], v[52:53]
.LBB0_234:
	s_or_b64 exec, exec, s[22:23]
	s_waitcnt vmcnt(10)
	v_lshlrev_b32_e32 v80, 16, v40
	v_and_b32_e32 v81, 0xffff0000, v40
	s_waitcnt lgkmcnt(2)
	v_pk_mul_f32 v[58:59], v[80:81], v[80:81]
	v_lshlrev_b32_e32 v40, 16, v41
	v_and_b32_e32 v41, 0xffff0000, v41
	v_pk_mul_f32 v[82:83], v[40:41], v[40:41]
	v_add_f32_e32 v53, v58, v59
	v_lshlrev_b32_e32 v84, 16, v42
	v_and_b32_e32 v85, 0xffff0000, v42
	v_add_f32_e32 v53, v82, v53
	v_and_b32_e32 v54, 0xffff0000, v43
	v_lshlrev_b32_e32 v55, 16, v43
	v_pk_mul_f32 v[42:43], v[84:85], v[84:85]
	v_add_f32_e32 v53, v83, v53
	v_add_f32_e32 v42, v42, v53
	s_waitcnt lgkmcnt(0)
	v_pk_mul_f32 v[56:57], v[54:55], v[54:55]
	v_add_f32_e32 v42, v43, v42
	v_add_f32_e32 v42, v57, v42
	v_add_f32_e32 v53, v56, v42
	ds_swizzle_b32 v58, v53 offset:swizzle(SWAP,1)
	v_cndmask_b32_e64 v52, v119, 1.0, s[20:21]
	v_pk_mul_f32 v[42:43], v[52:53], v[46:47] op_sel_hi:[0,1]
	v_cvt_pk_bf16_f32 v56, v42, v43
	v_pk_mul_f32 v[42:43], v[52:53], v[44:45] op_sel_hi:[0,1]
	s_waitcnt lgkmcnt(0)
	v_add_f32_e32 v44, v53, v58
	ds_swizzle_b32 v45, v44 offset:swizzle(SWAP,2)
	v_cvt_pk_bf16_f32 v57, v42, v43
	v_pk_mul_f32 v[42:43], v[52:53], v[48:49] op_sel_hi:[0,1]
	v_cvt_pk_bf16_f32 v58, v42, v43
	v_pk_mul_f32 v[42:43], v[52:53], v[50:51] op_sel_hi:[0,1]
	s_waitcnt lgkmcnt(0)
	v_add_f32_e32 v44, v44, v45
	ds_swizzle_b32 v45, v44 offset:swizzle(SWAP,4)
	v_cvt_pk_bf16_f32 v59, v42, v43
	v_add_u32_e32 v46, s97, v133
	v_mov_b64_e32 v[42:43], s[38:39]
	v_mad_i64_i32 v[82:83], s[22:23], v46, s83, v[42:43]
	s_waitcnt lgkmcnt(0)
	v_add_f32_e32 v42, v44, v45
	v_fmamk_f32 v42, v42, 0x3c800000, v107
	v_mul_f32_e32 v43, 0x4f800000, v42
	v_cmp_gt_f32_e32 vcc, s84, v42
	v_cndmask_b32_e64 v86, 0, v120, s[20:21]
	v_mov_b32_e32 v87, v65
	v_cndmask_b32_e32 v42, v42, v43, vcc
	v_sqrt_f32_e32 v44, v42
	v_cndmask_b32_e64 v43, v9, v13, s[18:19]
	v_add_u32_e32 v45, -1, v44
	v_fma_f32 v46, -v45, v44, v42
	v_cmp_ge_f32_e64 s[20:21], 0, v46
	v_add_u32_e32 v46, 1, v44
	s_nop 0
	v_cndmask_b32_e64 v45, v44, v45, s[20:21]
	v_fma_f32 v44, -v46, v44, v42
	v_cmp_lt_f32_e64 s[20:21], 0, v44
	s_nop 1
	v_cndmask_b32_e64 v44, v45, v46, s[20:21]
	v_mul_f32_e32 v45, 0x37800000, v44
	v_cndmask_b32_e32 v44, v44, v45, vcc
	v_cmp_class_f32_e32 vcc, v42, v108
	v_cndmask_b32_e64 v45, v11, v15, s[18:19]
	s_nop 0
	v_cndmask_b32_e32 v46, v44, v42, vcc
	v_div_scale_f32 v47, s[20:21], v46, v46, 1.0
	v_rcp_f32_e32 v48, v47
	v_cndmask_b32_e64 v42, v8, v12, s[18:19]
	v_cndmask_b32_e64 v44, v10, v14, s[18:19]
	v_fma_f32 v49, -v47, v48, 1.0
	v_fmac_f32_e32 v48, v49, v48
	v_div_scale_f32 v49, vcc, 1.0, v46, 1.0
	v_mul_f32_e32 v50, v49, v48
	v_fma_f32 v51, -v47, v50, v49
	v_fmac_f32_e32 v50, v51, v48
	v_fma_f32 v47, -v47, v50, v49
	v_div_fmas_f32 v47, v47, v48, v50
	v_div_fixup_f32 v46, v47, v46, 1.0
	v_pk_mul_f32 v[48:49], v[46:47], v[80:81] op_sel_hi:[0,1]
	v_pk_mul_f32 v[40:41], v[46:47], v[40:41] op_sel_hi:[0,1]
	v_pk_mul_f32 v[42:43], v[42:43], v[48:49]
	v_pk_mul_f32 v[40:41], v[44:45], v[40:41]
	v_pk_mul_f32 v[44:45], v[46:47], v[84:85] op_sel_hi:[0,1]
	v_cndmask_b32_e64 v49, v1, v5, s[18:19]
	v_cndmask_b32_e64 v48, v0, v4, s[18:19]
	v_pk_mul_f32 v[44:45], v[48:49], v[44:45]
	v_pk_mul_f32 v[46:47], v[46:47], v[54:55] op_sel_hi:[0,1]
	v_cndmask_b32_e64 v49, v3, v7, s[18:19]
	v_cndmask_b32_e64 v48, v2, v6, s[18:19]
	v_pk_mul_f32 v[46:47], v[48:49], v[46:47] op_sel:[0,1] op_sel_hi:[1,0]
	ds_swizzle_b32 v48, v42 offset:swizzle(SWAP,1)
	ds_swizzle_b32 v49, v43 offset:swizzle(SWAP,1)
	ds_swizzle_b32 v50, v40 offset:swizzle(SWAP,1)
	ds_swizzle_b32 v51, v41 offset:swizzle(SWAP,1)
	ds_swizzle_b32 v54, v44 offset:swizzle(SWAP,1)
	ds_swizzle_b32 v55, v45 offset:swizzle(SWAP,1)
	ds_swizzle_b32 v52, v46 offset:swizzle(SWAP,1)
	ds_swizzle_b32 v53, v47 offset:swizzle(SWAP,1)
	v_lshl_add_u64 v[80:81], v[82:83], 0, v[86:87]
	v_lshl_add_u64 v[78:79], v[78:79], 1, v[80:81]
	v_lshl_add_u64 v[78:79], v[78:79], 0, v[64:65]
	global_store_dwordx4 v[78:79], v[56:59], off nt
	s_and_saveexec_b64 s[20:21], s[2:3]
	s_cbranch_execz .LBB0_236
	v_lshl_add_u32 v82, v132, 6, s60
	ds_read2_b32 v[56:57], v82 offset0:8 offset1:9
	ds_read2_b32 v[58:59], v82 offset0:10 offset1:11
	ds_read2_b32 v[78:79], v82 offset0:12 offset1:13
	ds_read2_b32 v[80:81], v82 offset0:14 offset1:15
	s_waitcnt lgkmcnt(3)
	v_pk_mul_f32 v[48:49], v[56:57], v[48:49]
	s_waitcnt lgkmcnt(2)
	v_pk_mul_f32 v[50:51], v[58:59], v[50:51]
	s_waitcnt lgkmcnt(1)
	v_pk_mul_f32 v[54:55], v[78:79], v[54:55]
	ds_read2_b32 v[56:57], v82 offset1:1
	ds_read2_b32 v[58:59], v82 offset0:2 offset1:3
	ds_read2_b32 v[78:79], v82 offset0:4 offset1:5
	ds_read2_b32 v[82:83], v82 offset0:6 offset1:7
	s_waitcnt lgkmcnt(4)
	v_pk_mul_f32 v[52:53], v[80:81], v[52:53]
	v_cndmask_b32_e64 v49, v49, -v49, s[4:5]
	v_cndmask_b32_e64 v48, v48, -v48, s[4:5]
	v_cndmask_b32_e64 v51, v51, -v51, s[4:5]
	v_cndmask_b32_e64 v50, v50, -v50, s[4:5]
	v_cndmask_b32_e64 v54, v54, -v54, s[4:5]
	v_cndmask_b32_e64 v55, v55, -v55, s[4:5]
	v_cndmask_b32_e64 v52, v52, -v52, s[4:5]
	v_cndmask_b32_e64 v53, v53, -v53, s[4:5]
	s_waitcnt lgkmcnt(0)
	v_pk_fma_f32 v[46:47], v[46:47], v[82:83], v[52:53]
	v_pk_fma_f32 v[44:45], v[44:45], v[78:79], v[54:55]
	v_pk_fma_f32 v[40:41], v[40:41], v[58:59], v[50:51]
	v_pk_fma_f32 v[42:43], v[42:43], v[56:57], v[48:49]
.LBB0_236:
	s_or_b64 exec, exec, s[20:21]
	s_waitcnt vmcnt(10)
	v_lshlrev_b32_e32 v56, 16, v36
	v_and_b32_e32 v57, 0xffff0000, v36
	s_waitcnt lgkmcnt(2)
	v_pk_mul_f32 v[54:55], v[56:57], v[56:57]
	v_lshlrev_b32_e32 v36, 16, v37
	v_and_b32_e32 v37, 0xffff0000, v37
	v_pk_mul_f32 v[58:59], v[36:37], v[36:37]
	v_add_f32_e32 v49, v54, v55
	v_lshlrev_b32_e32 v78, 16, v38
	v_and_b32_e32 v79, 0xffff0000, v38
	v_add_f32_e32 v49, v58, v49
	v_and_b32_e32 v50, 0xffff0000, v39
	v_lshlrev_b32_e32 v51, 16, v39
	v_pk_mul_f32 v[38:39], v[78:79], v[78:79]
	v_add_f32_e32 v49, v59, v49
	v_add_f32_e32 v38, v38, v49
	s_waitcnt lgkmcnt(0)
	v_pk_mul_f32 v[52:53], v[50:51], v[50:51]
	v_add_f32_e32 v38, v39, v38
	v_add_f32_e32 v38, v53, v38
	v_add_f32_e32 v49, v52, v38
	ds_swizzle_b32 v54, v49 offset:swizzle(SWAP,1)
	v_cndmask_b32_e64 v48, v119, 1.0, s[18:19]
	v_pk_mul_f32 v[38:39], v[48:49], v[42:43] op_sel_hi:[0,1]
	v_cvt_pk_bf16_f32 v52, v38, v39
	v_pk_mul_f32 v[38:39], v[48:49], v[40:41] op_sel_hi:[0,1]
	s_waitcnt lgkmcnt(0)
	v_add_f32_e32 v40, v49, v54
	ds_swizzle_b32 v41, v40 offset:swizzle(SWAP,2)
	v_cvt_pk_bf16_f32 v53, v38, v39
	v_pk_mul_f32 v[38:39], v[48:49], v[44:45] op_sel_hi:[0,1]
	v_cvt_pk_bf16_f32 v54, v38, v39
	v_pk_mul_f32 v[38:39], v[48:49], v[46:47] op_sel_hi:[0,1]
	s_waitcnt lgkmcnt(0)
	v_add_f32_e32 v40, v40, v41
	ds_swizzle_b32 v41, v40 offset:swizzle(SWAP,4)
	v_cvt_pk_bf16_f32 v55, v38, v39
	v_add_u32_e32 v42, s97, v132
	v_mov_b64_e32 v[38:39], s[38:39]
	v_mad_i64_i32 v[58:59], s[20:21], v42, s83, v[38:39]
	s_waitcnt lgkmcnt(0)
	v_add_f32_e32 v38, v40, v41
	v_fmamk_f32 v38, v38, 0x3c800000, v107
	v_mul_f32_e32 v39, 0x4f800000, v38
	v_cmp_gt_f32_e32 vcc, s84, v38
	v_cndmask_b32_e64 v80, 0, v120, s[18:19]
	v_mov_b32_e32 v81, v65
	v_cndmask_b32_e32 v38, v38, v39, vcc
	v_sqrt_f32_e32 v40, v38
	v_cndmask_b32_e64 v39, v9, v13, s[16:17]
	v_add_u32_e32 v41, -1, v40
	v_fma_f32 v42, -v41, v40, v38
	v_cmp_ge_f32_e64 s[18:19], 0, v42
	v_add_u32_e32 v42, 1, v40
	s_nop 0
	v_cndmask_b32_e64 v41, v40, v41, s[18:19]
	v_fma_f32 v40, -v42, v40, v38
	v_cmp_lt_f32_e64 s[18:19], 0, v40
	s_nop 1
	v_cndmask_b32_e64 v40, v41, v42, s[18:19]
	v_mul_f32_e32 v41, 0x37800000, v40
	v_cndmask_b32_e32 v40, v40, v41, vcc
	v_cmp_class_f32_e32 vcc, v38, v108
	v_cndmask_b32_e64 v41, v11, v15, s[16:17]
	s_nop 0
	v_cndmask_b32_e32 v42, v40, v38, vcc
	v_div_scale_f32 v43, s[18:19], v42, v42, 1.0
	v_rcp_f32_e32 v44, v43
	v_cndmask_b32_e64 v38, v8, v12, s[16:17]
	v_cndmask_b32_e64 v40, v10, v14, s[16:17]
	v_fma_f32 v45, -v43, v44, 1.0
	v_fmac_f32_e32 v44, v45, v44
	v_div_scale_f32 v45, vcc, 1.0, v42, 1.0
	v_mul_f32_e32 v46, v45, v44
	v_fma_f32 v47, -v43, v46, v45
	v_fmac_f32_e32 v46, v47, v44
	v_fma_f32 v43, -v43, v46, v45
	v_div_fmas_f32 v43, v43, v44, v46
	v_div_fixup_f32 v42, v43, v42, 1.0
	v_pk_mul_f32 v[44:45], v[42:43], v[56:57] op_sel_hi:[0,1]
	v_pk_mul_f32 v[36:37], v[42:43], v[36:37] op_sel_hi:[0,1]
	v_pk_mul_f32 v[38:39], v[38:39], v[44:45]
	v_pk_mul_f32 v[36:37], v[40:41], v[36:37]
	v_pk_mul_f32 v[40:41], v[42:43], v[78:79] op_sel_hi:[0,1]
	v_cndmask_b32_e64 v45, v1, v5, s[16:17]
	v_cndmask_b32_e64 v44, v0, v4, s[16:17]
	v_pk_mul_f32 v[40:41], v[44:45], v[40:41]
	v_pk_mul_f32 v[42:43], v[42:43], v[50:51] op_sel_hi:[0,1]
	v_cndmask_b32_e64 v45, v3, v7, s[16:17]
	v_cndmask_b32_e64 v44, v2, v6, s[16:17]
	v_pk_mul_f32 v[42:43], v[44:45], v[42:43] op_sel:[0,1] op_sel_hi:[1,0]
	ds_swizzle_b32 v44, v38 offset:swizzle(SWAP,1)
	ds_swizzle_b32 v45, v39 offset:swizzle(SWAP,1)
	ds_swizzle_b32 v46, v36 offset:swizzle(SWAP,1)
	ds_swizzle_b32 v47, v37 offset:swizzle(SWAP,1)
	ds_swizzle_b32 v50, v40 offset:swizzle(SWAP,1)
	ds_swizzle_b32 v51, v41 offset:swizzle(SWAP,1)
	ds_swizzle_b32 v48, v42 offset:swizzle(SWAP,1)
	ds_swizzle_b32 v49, v43 offset:swizzle(SWAP,1)
	v_lshl_add_u64 v[56:57], v[58:59], 0, v[80:81]
	v_lshl_add_u64 v[56:57], v[74:75], 1, v[56:57]
	v_lshl_add_u64 v[56:57], v[56:57], 0, v[64:65]
	global_store_dwordx4 v[56:57], v[52:55], off nt
	s_and_saveexec_b64 s[18:19], s[2:3]
	s_cbranch_execz .LBB0_238
	v_lshl_add_u32 v74, v131, 6, s60
	ds_read2_b32 v[52:53], v74 offset0:8 offset1:9
	ds_read2_b32 v[54:55], v74 offset0:10 offset1:11
	ds_read2_b32 v[56:57], v74 offset0:12 offset1:13
	ds_read2_b32 v[58:59], v74 offset0:14 offset1:15
	s_waitcnt lgkmcnt(3)
	v_pk_mul_f32 v[44:45], v[52:53], v[44:45]
	s_waitcnt lgkmcnt(2)
	v_pk_mul_f32 v[46:47], v[54:55], v[46:47]
	s_waitcnt lgkmcnt(1)
	v_pk_mul_f32 v[50:51], v[56:57], v[50:51]
	ds_read2_b32 v[52:53], v74 offset1:1
	ds_read2_b32 v[54:55], v74 offset0:2 offset1:3
	ds_read2_b32 v[56:57], v74 offset0:4 offset1:5
	ds_read2_b32 v[74:75], v74 offset0:6 offset1:7
	s_waitcnt lgkmcnt(4)
	v_pk_mul_f32 v[48:49], v[58:59], v[48:49]
	v_cndmask_b32_e64 v45, v45, -v45, s[4:5]
	v_cndmask_b32_e64 v44, v44, -v44, s[4:5]
	v_cndmask_b32_e64 v47, v47, -v47, s[4:5]
	v_cndmask_b32_e64 v46, v46, -v46, s[4:5]
	v_cndmask_b32_e64 v50, v50, -v50, s[4:5]
	v_cndmask_b32_e64 v51, v51, -v51, s[4:5]
	v_cndmask_b32_e64 v48, v48, -v48, s[4:5]
	v_cndmask_b32_e64 v49, v49, -v49, s[4:5]
	s_waitcnt lgkmcnt(0)
	v_pk_fma_f32 v[42:43], v[42:43], v[74:75], v[48:49]
	v_pk_fma_f32 v[40:41], v[40:41], v[56:57], v[50:51]
	v_pk_fma_f32 v[36:37], v[36:37], v[54:55], v[46:47]
	v_pk_fma_f32 v[38:39], v[38:39], v[52:53], v[44:45]
.LBB0_238:
	s_or_b64 exec, exec, s[18:19]
	s_waitcnt vmcnt(10)
	v_lshlrev_b32_e32 v52, 16, v32
	v_and_b32_e32 v53, 0xffff0000, v32
	s_waitcnt lgkmcnt(2)
	v_pk_mul_f32 v[50:51], v[52:53], v[52:53]
	v_lshlrev_b32_e32 v32, 16, v33
	v_and_b32_e32 v33, 0xffff0000, v33
	v_pk_mul_f32 v[54:55], v[32:33], v[32:33]
	v_add_f32_e32 v45, v50, v51
	v_lshlrev_b32_e32 v56, 16, v34
	v_and_b32_e32 v57, 0xffff0000, v34
	v_add_f32_e32 v45, v54, v45
	v_and_b32_e32 v46, 0xffff0000, v35
	v_lshlrev_b32_e32 v47, 16, v35
	v_pk_mul_f32 v[34:35], v[56:57], v[56:57]
	v_add_f32_e32 v45, v55, v45
	v_add_f32_e32 v34, v34, v45
	s_waitcnt lgkmcnt(0)
	v_pk_mul_f32 v[48:49], v[46:47], v[46:47]
	v_add_f32_e32 v34, v35, v34
	v_add_f32_e32 v34, v49, v34
	v_add_f32_e32 v45, v48, v34
	ds_swizzle_b32 v50, v45 offset:swizzle(SWAP,1)
	v_cndmask_b32_e64 v44, v119, 1.0, s[16:17]
	v_pk_mul_f32 v[34:35], v[44:45], v[38:39] op_sel_hi:[0,1]
	v_cvt_pk_bf16_f32 v48, v34, v35
	v_pk_mul_f32 v[34:35], v[44:45], v[36:37] op_sel_hi:[0,1]
	s_waitcnt lgkmcnt(0)
	v_add_f32_e32 v36, v45, v50
	ds_swizzle_b32 v37, v36 offset:swizzle(SWAP,2)
	v_cvt_pk_bf16_f32 v49, v34, v35
	v_pk_mul_f32 v[34:35], v[44:45], v[40:41] op_sel_hi:[0,1]
	v_cvt_pk_bf16_f32 v50, v34, v35
	v_pk_mul_f32 v[34:35], v[44:45], v[42:43] op_sel_hi:[0,1]
	s_waitcnt lgkmcnt(0)
	v_add_f32_e32 v36, v36, v37
	ds_swizzle_b32 v37, v36 offset:swizzle(SWAP,4)
	v_cvt_pk_bf16_f32 v51, v34, v35
	v_add_u32_e32 v38, s97, v131
	v_mov_b64_e32 v[34:35], s[38:39]
	v_mad_i64_i32 v[54:55], s[18:19], v38, s83, v[34:35]
	s_waitcnt lgkmcnt(0)
	v_add_f32_e32 v34, v36, v37
	v_fmamk_f32 v34, v34, 0x3c800000, v107
	v_mul_f32_e32 v35, 0x4f800000, v34
	v_cmp_gt_f32_e32 vcc, s84, v34
	v_cndmask_b32_e64 v58, 0, v120, s[16:17]
	v_mov_b32_e32 v59, v65
	v_cndmask_b32_e32 v34, v34, v35, vcc
	v_sqrt_f32_e32 v36, v34
	v_cndmask_b32_e64 v35, v9, v13, s[14:15]
	v_add_u32_e32 v37, -1, v36
	v_fma_f32 v38, -v37, v36, v34
	v_cmp_ge_f32_e64 s[16:17], 0, v38
	v_add_u32_e32 v38, 1, v36
	s_nop 0
	v_cndmask_b32_e64 v37, v36, v37, s[16:17]
	v_fma_f32 v36, -v38, v36, v34
	v_cmp_lt_f32_e64 s[16:17], 0, v36
	s_nop 1
	v_cndmask_b32_e64 v36, v37, v38, s[16:17]
	v_mul_f32_e32 v37, 0x37800000, v36
	v_cndmask_b32_e32 v36, v36, v37, vcc
	v_cmp_class_f32_e32 vcc, v34, v108
	v_cndmask_b32_e64 v37, v11, v15, s[14:15]
	s_nop 0
	v_cndmask_b32_e32 v38, v36, v34, vcc
	v_div_scale_f32 v39, s[16:17], v38, v38, 1.0
	v_rcp_f32_e32 v40, v39
	v_cndmask_b32_e64 v34, v8, v12, s[14:15]
	v_cndmask_b32_e64 v36, v10, v14, s[14:15]
	v_fma_f32 v41, -v39, v40, 1.0
	v_fmac_f32_e32 v40, v41, v40
	v_div_scale_f32 v41, vcc, 1.0, v38, 1.0
	v_mul_f32_e32 v42, v41, v40
	v_fma_f32 v43, -v39, v42, v41
	v_fmac_f32_e32 v42, v43, v40
	v_fma_f32 v39, -v39, v42, v41
	v_div_fmas_f32 v39, v39, v40, v42
	v_div_fixup_f32 v38, v39, v38, 1.0
	v_pk_mul_f32 v[40:41], v[38:39], v[52:53] op_sel_hi:[0,1]
	v_pk_mul_f32 v[32:33], v[38:39], v[32:33] op_sel_hi:[0,1]
	v_pk_mul_f32 v[34:35], v[34:35], v[40:41]
	v_pk_mul_f32 v[32:33], v[36:37], v[32:33]
	v_pk_mul_f32 v[36:37], v[38:39], v[56:57] op_sel_hi:[0,1]
	v_cndmask_b32_e64 v41, v1, v5, s[14:15]
	v_cndmask_b32_e64 v40, v0, v4, s[14:15]
	v_pk_mul_f32 v[36:37], v[40:41], v[36:37]
	v_pk_mul_f32 v[38:39], v[38:39], v[46:47] op_sel_hi:[0,1]
	v_cndmask_b32_e64 v41, v3, v7, s[14:15]
	v_cndmask_b32_e64 v40, v2, v6, s[14:15]
	v_pk_mul_f32 v[38:39], v[40:41], v[38:39] op_sel:[0,1] op_sel_hi:[1,0]
	ds_swizzle_b32 v40, v34 offset:swizzle(SWAP,1)
	ds_swizzle_b32 v41, v35 offset:swizzle(SWAP,1)
	ds_swizzle_b32 v42, v32 offset:swizzle(SWAP,1)
	ds_swizzle_b32 v43, v33 offset:swizzle(SWAP,1)
	ds_swizzle_b32 v46, v36 offset:swizzle(SWAP,1)
	ds_swizzle_b32 v47, v37 offset:swizzle(SWAP,1)
	ds_swizzle_b32 v44, v38 offset:swizzle(SWAP,1)
	ds_swizzle_b32 v45, v39 offset:swizzle(SWAP,1)
	v_lshl_add_u64 v[52:53], v[54:55], 0, v[58:59]
	v_lshl_add_u64 v[52:53], v[76:77], 1, v[52:53]
	v_lshl_add_u64 v[52:53], v[52:53], 0, v[64:65]
	global_store_dwordx4 v[52:53], v[48:51], off nt
	s_and_saveexec_b64 s[16:17], s[2:3]
	s_cbranch_execz .LBB0_240
	v_lshl_add_u32 v56, v130, 6, s60
	ds_read2_b32 v[48:49], v56 offset0:8 offset1:9
	ds_read2_b32 v[50:51], v56 offset0:10 offset1:11
	ds_read2_b32 v[52:53], v56 offset0:12 offset1:13
	ds_read2_b32 v[54:55], v56 offset0:14 offset1:15
	s_waitcnt lgkmcnt(3)
	v_pk_mul_f32 v[40:41], v[48:49], v[40:41]
	s_waitcnt lgkmcnt(2)
	v_pk_mul_f32 v[42:43], v[50:51], v[42:43]
	s_waitcnt lgkmcnt(1)
	v_pk_mul_f32 v[46:47], v[52:53], v[46:47]
	ds_read2_b32 v[48:49], v56 offset1:1
	ds_read2_b32 v[50:51], v56 offset0:2 offset1:3
	ds_read2_b32 v[52:53], v56 offset0:4 offset1:5
	ds_read2_b32 v[56:57], v56 offset0:6 offset1:7
	s_waitcnt lgkmcnt(4)
	v_pk_mul_f32 v[44:45], v[54:55], v[44:45]
	v_cndmask_b32_e64 v41, v41, -v41, s[4:5]
	v_cndmask_b32_e64 v40, v40, -v40, s[4:5]
	v_cndmask_b32_e64 v43, v43, -v43, s[4:5]
	v_cndmask_b32_e64 v42, v42, -v42, s[4:5]
	v_cndmask_b32_e64 v46, v46, -v46, s[4:5]
	v_cndmask_b32_e64 v47, v47, -v47, s[4:5]
	v_cndmask_b32_e64 v44, v44, -v44, s[4:5]
	v_cndmask_b32_e64 v45, v45, -v45, s[4:5]
	s_waitcnt lgkmcnt(0)
	v_pk_fma_f32 v[38:39], v[38:39], v[56:57], v[44:45]
	v_pk_fma_f32 v[36:37], v[36:37], v[52:53], v[46:47]
	v_pk_fma_f32 v[32:33], v[32:33], v[50:51], v[42:43]
	v_pk_fma_f32 v[34:35], v[34:35], v[48:49], v[40:41]
.LBB0_240:
	s_or_b64 exec, exec, s[16:17]
	s_waitcnt vmcnt(10)
	v_lshlrev_b32_e32 v48, 16, v28
	v_and_b32_e32 v49, 0xffff0000, v28
	s_waitcnt lgkmcnt(2)
	v_pk_mul_f32 v[46:47], v[48:49], v[48:49]
	v_lshlrev_b32_e32 v28, 16, v29
	v_and_b32_e32 v29, 0xffff0000, v29
	v_pk_mul_f32 v[50:51], v[28:29], v[28:29]
	v_add_f32_e32 v41, v46, v47
	v_lshlrev_b32_e32 v52, 16, v30
	v_and_b32_e32 v53, 0xffff0000, v30
	v_add_f32_e32 v41, v50, v41
	v_and_b32_e32 v42, 0xffff0000, v31
	v_lshlrev_b32_e32 v43, 16, v31
	v_pk_mul_f32 v[30:31], v[52:53], v[52:53]
	v_add_f32_e32 v41, v51, v41
	v_add_f32_e32 v30, v30, v41
	s_waitcnt lgkmcnt(0)
	v_pk_mul_f32 v[44:45], v[42:43], v[42:43]
	v_add_f32_e32 v30, v31, v30
	v_add_f32_e32 v30, v45, v30
	v_add_f32_e32 v41, v44, v30
	ds_swizzle_b32 v46, v41 offset:swizzle(SWAP,1)
	v_cndmask_b32_e64 v40, v119, 1.0, s[14:15]
	v_pk_mul_f32 v[30:31], v[40:41], v[34:35] op_sel_hi:[0,1]
	v_cvt_pk_bf16_f32 v44, v30, v31
	v_pk_mul_f32 v[30:31], v[40:41], v[32:33] op_sel_hi:[0,1]
	s_waitcnt lgkmcnt(0)
	v_add_f32_e32 v32, v41, v46
	ds_swizzle_b32 v33, v32 offset:swizzle(SWAP,2)
	v_cvt_pk_bf16_f32 v45, v30, v31
	v_pk_mul_f32 v[30:31], v[40:41], v[36:37] op_sel_hi:[0,1]
	v_cvt_pk_bf16_f32 v46, v30, v31
	v_pk_mul_f32 v[30:31], v[40:41], v[38:39] op_sel_hi:[0,1]
	s_waitcnt lgkmcnt(0)
	v_add_f32_e32 v32, v32, v33
	ds_swizzle_b32 v33, v32 offset:swizzle(SWAP,4)
	v_cvt_pk_bf16_f32 v47, v30, v31
	v_add_u32_e32 v34, s97, v130
	v_mov_b64_e32 v[30:31], s[38:39]
	v_mad_i64_i32 v[50:51], s[16:17], v34, s83, v[30:31]
	s_waitcnt lgkmcnt(0)
	v_add_f32_e32 v30, v32, v33
	v_fmamk_f32 v30, v30, 0x3c800000, v107
	v_mul_f32_e32 v31, 0x4f800000, v30
	v_cmp_gt_f32_e32 vcc, s84, v30
	v_cndmask_b32_e64 v54, 0, v120, s[14:15]
	v_mov_b32_e32 v55, v65
	v_cndmask_b32_e32 v30, v30, v31, vcc
	v_sqrt_f32_e32 v32, v30
	v_cndmask_b32_e64 v31, v9, v13, s[12:13]
	v_add_u32_e32 v33, -1, v32
	v_fma_f32 v34, -v33, v32, v30
	v_cmp_ge_f32_e64 s[14:15], 0, v34
	v_add_u32_e32 v34, 1, v32
	s_nop 0
	v_cndmask_b32_e64 v33, v32, v33, s[14:15]
	v_fma_f32 v32, -v34, v32, v30
	v_cmp_lt_f32_e64 s[14:15], 0, v32
	s_nop 1
	v_cndmask_b32_e64 v32, v33, v34, s[14:15]
	v_mul_f32_e32 v33, 0x37800000, v32
	v_cndmask_b32_e32 v32, v32, v33, vcc
	v_cmp_class_f32_e32 vcc, v30, v108
	v_cndmask_b32_e64 v33, v11, v15, s[12:13]
	s_nop 0
	v_cndmask_b32_e32 v34, v32, v30, vcc
	v_div_scale_f32 v35, s[14:15], v34, v34, 1.0
	v_rcp_f32_e32 v36, v35
	v_cndmask_b32_e64 v30, v8, v12, s[12:13]
	v_cndmask_b32_e64 v32, v10, v14, s[12:13]
	v_fma_f32 v37, -v35, v36, 1.0
	v_fmac_f32_e32 v36, v37, v36
	v_div_scale_f32 v37, vcc, 1.0, v34, 1.0
	v_mul_f32_e32 v38, v37, v36
	v_fma_f32 v39, -v35, v38, v37
	v_fmac_f32_e32 v38, v39, v36
	v_fma_f32 v35, -v35, v38, v37
	v_div_fmas_f32 v35, v35, v36, v38
	v_div_fixup_f32 v34, v35, v34, 1.0
	v_pk_mul_f32 v[36:37], v[34:35], v[48:49] op_sel_hi:[0,1]
	v_pk_mul_f32 v[28:29], v[34:35], v[28:29] op_sel_hi:[0,1]
	v_pk_mul_f32 v[30:31], v[30:31], v[36:37]
	v_pk_mul_f32 v[28:29], v[32:33], v[28:29]
	v_pk_mul_f32 v[32:33], v[34:35], v[52:53] op_sel_hi:[0,1]
	v_cndmask_b32_e64 v37, v1, v5, s[12:13]
	v_cndmask_b32_e64 v36, v0, v4, s[12:13]
	v_pk_mul_f32 v[32:33], v[36:37], v[32:33]
	v_pk_mul_f32 v[34:35], v[34:35], v[42:43] op_sel_hi:[0,1]
	v_cndmask_b32_e64 v37, v3, v7, s[12:13]
	v_cndmask_b32_e64 v36, v2, v6, s[12:13]
	v_pk_mul_f32 v[34:35], v[36:37], v[34:35] op_sel:[0,1] op_sel_hi:[1,0]
	ds_swizzle_b32 v36, v30 offset:swizzle(SWAP,1)
	ds_swizzle_b32 v37, v31 offset:swizzle(SWAP,1)
	ds_swizzle_b32 v38, v28 offset:swizzle(SWAP,1)
	ds_swizzle_b32 v39, v29 offset:swizzle(SWAP,1)
	ds_swizzle_b32 v42, v32 offset:swizzle(SWAP,1)
	ds_swizzle_b32 v43, v33 offset:swizzle(SWAP,1)
	ds_swizzle_b32 v40, v34 offset:swizzle(SWAP,1)
	ds_swizzle_b32 v41, v35 offset:swizzle(SWAP,1)
	v_lshl_add_u64 v[48:49], v[50:51], 0, v[54:55]
	v_lshl_add_u64 v[48:49], v[72:73], 1, v[48:49]
	v_lshl_add_u64 v[48:49], v[48:49], 0, v[64:65]
	global_store_dwordx4 v[48:49], v[44:47], off nt
	s_and_saveexec_b64 s[14:15], s[2:3]
	s_cbranch_execz .LBB0_242
	v_lshl_add_u32 v52, v129, 6, s60
	ds_read2_b32 v[44:45], v52 offset0:8 offset1:9
	ds_read2_b32 v[46:47], v52 offset0:10 offset1:11
	ds_read2_b32 v[48:49], v52 offset0:12 offset1:13
	ds_read2_b32 v[50:51], v52 offset0:14 offset1:15
	s_waitcnt lgkmcnt(3)
	v_pk_mul_f32 v[36:37], v[44:45], v[36:37]
	s_waitcnt lgkmcnt(2)
	v_pk_mul_f32 v[38:39], v[46:47], v[38:39]
	s_waitcnt lgkmcnt(1)
	v_pk_mul_f32 v[42:43], v[48:49], v[42:43]
	ds_read2_b32 v[44:45], v52 offset1:1
	ds_read2_b32 v[46:47], v52 offset0:2 offset1:3
	ds_read2_b32 v[48:49], v52 offset0:4 offset1:5
	ds_read2_b32 v[52:53], v52 offset0:6 offset1:7
	s_waitcnt lgkmcnt(4)
	v_pk_mul_f32 v[40:41], v[50:51], v[40:41]
	v_cndmask_b32_e64 v37, v37, -v37, s[4:5]
	v_cndmask_b32_e64 v36, v36, -v36, s[4:5]
	v_cndmask_b32_e64 v39, v39, -v39, s[4:5]
	v_cndmask_b32_e64 v38, v38, -v38, s[4:5]
	v_cndmask_b32_e64 v42, v42, -v42, s[4:5]
	v_cndmask_b32_e64 v43, v43, -v43, s[4:5]
	v_cndmask_b32_e64 v40, v40, -v40, s[4:5]
	v_cndmask_b32_e64 v41, v41, -v41, s[4:5]
	s_waitcnt lgkmcnt(0)
	v_pk_fma_f32 v[34:35], v[34:35], v[52:53], v[40:41]
	v_pk_fma_f32 v[32:33], v[32:33], v[48:49], v[42:43]
	v_pk_fma_f32 v[28:29], v[28:29], v[46:47], v[38:39]
	v_pk_fma_f32 v[30:31], v[30:31], v[44:45], v[36:37]
.LBB0_242:
	s_or_b64 exec, exec, s[14:15]
	s_waitcnt vmcnt(10)
	v_lshlrev_b32_e32 v44, 16, v24
	v_and_b32_e32 v45, 0xffff0000, v24
	s_waitcnt lgkmcnt(2)
	v_pk_mul_f32 v[42:43], v[44:45], v[44:45]
	v_lshlrev_b32_e32 v24, 16, v25
	v_and_b32_e32 v25, 0xffff0000, v25
	v_pk_mul_f32 v[46:47], v[24:25], v[24:25]
	v_add_f32_e32 v37, v42, v43
	v_lshlrev_b32_e32 v48, 16, v26
	v_and_b32_e32 v49, 0xffff0000, v26
	v_add_f32_e32 v37, v46, v37
	v_and_b32_e32 v38, 0xffff0000, v27
	v_lshlrev_b32_e32 v39, 16, v27
	v_pk_mul_f32 v[26:27], v[48:49], v[48:49]
	v_add_f32_e32 v37, v47, v37
	v_add_f32_e32 v26, v26, v37
	s_waitcnt lgkmcnt(0)
	v_pk_mul_f32 v[40:41], v[38:39], v[38:39]
	v_add_f32_e32 v26, v27, v26
	v_add_f32_e32 v26, v41, v26
	v_add_f32_e32 v37, v40, v26
	ds_swizzle_b32 v42, v37 offset:swizzle(SWAP,1)
	v_cndmask_b32_e64 v36, v119, 1.0, s[12:13]
	v_pk_mul_f32 v[26:27], v[36:37], v[30:31] op_sel_hi:[0,1]
	v_cvt_pk_bf16_f32 v40, v26, v27
	v_pk_mul_f32 v[26:27], v[36:37], v[28:29] op_sel_hi:[0,1]
	s_waitcnt lgkmcnt(0)
	v_add_f32_e32 v28, v37, v42
	ds_swizzle_b32 v29, v28 offset:swizzle(SWAP,2)
	v_cvt_pk_bf16_f32 v41, v26, v27
	v_pk_mul_f32 v[26:27], v[36:37], v[32:33] op_sel_hi:[0,1]
	v_cvt_pk_bf16_f32 v42, v26, v27
	v_pk_mul_f32 v[26:27], v[36:37], v[34:35] op_sel_hi:[0,1]
	s_waitcnt lgkmcnt(0)
	v_add_f32_e32 v28, v28, v29
	ds_swizzle_b32 v29, v28 offset:swizzle(SWAP,4)
	v_cvt_pk_bf16_f32 v43, v26, v27
	v_add_u32_e32 v30, s97, v129
	v_mov_b64_e32 v[26:27], s[38:39]
	v_mad_i64_i32 v[46:47], s[14:15], v30, s83, v[26:27]
	s_waitcnt lgkmcnt(0)
	v_add_f32_e32 v26, v28, v29
	v_fmamk_f32 v26, v26, 0x3c800000, v107
	v_mul_f32_e32 v27, 0x4f800000, v26
	v_cmp_gt_f32_e32 vcc, s84, v26
	v_cndmask_b32_e64 v50, 0, v120, s[12:13]
	v_mov_b32_e32 v51, v65
	v_cndmask_b32_e32 v26, v26, v27, vcc
	v_sqrt_f32_e32 v28, v26
	v_cndmask_b32_e64 v27, v9, v13, s[10:11]
	v_add_u32_e32 v29, -1, v28
	v_fma_f32 v30, -v29, v28, v26
	v_cmp_ge_f32_e64 s[12:13], 0, v30
	v_add_u32_e32 v30, 1, v28
	s_nop 0
	v_cndmask_b32_e64 v29, v28, v29, s[12:13]
	v_fma_f32 v28, -v30, v28, v26
	v_cmp_lt_f32_e64 s[12:13], 0, v28
	s_nop 1
	v_cndmask_b32_e64 v28, v29, v30, s[12:13]
	v_mul_f32_e32 v29, 0x37800000, v28
	v_cndmask_b32_e32 v28, v28, v29, vcc
	v_cmp_class_f32_e32 vcc, v26, v108
	v_cndmask_b32_e64 v29, v11, v15, s[10:11]
	s_nop 0
	v_cndmask_b32_e32 v30, v28, v26, vcc
	v_div_scale_f32 v31, s[12:13], v30, v30, 1.0
	v_rcp_f32_e32 v32, v31
	v_cndmask_b32_e64 v26, v8, v12, s[10:11]
	v_cndmask_b32_e64 v28, v10, v14, s[10:11]
	v_fma_f32 v33, -v31, v32, 1.0
	v_fmac_f32_e32 v32, v33, v32
	v_div_scale_f32 v33, vcc, 1.0, v30, 1.0
	v_mul_f32_e32 v34, v33, v32
	v_fma_f32 v35, -v31, v34, v33
	v_fmac_f32_e32 v34, v35, v32
	v_fma_f32 v31, -v31, v34, v33
	v_div_fmas_f32 v31, v31, v32, v34
	v_div_fixup_f32 v30, v31, v30, 1.0
	v_pk_mul_f32 v[32:33], v[30:31], v[44:45] op_sel_hi:[0,1]
	v_pk_mul_f32 v[24:25], v[30:31], v[24:25] op_sel_hi:[0,1]
	v_pk_mul_f32 v[26:27], v[26:27], v[32:33]
	v_pk_mul_f32 v[24:25], v[28:29], v[24:25]
	v_pk_mul_f32 v[28:29], v[30:31], v[48:49] op_sel_hi:[0,1]
	v_cndmask_b32_e64 v33, v1, v5, s[10:11]
	v_cndmask_b32_e64 v32, v0, v4, s[10:11]
	v_pk_mul_f32 v[28:29], v[32:33], v[28:29]
	v_pk_mul_f32 v[30:31], v[30:31], v[38:39] op_sel_hi:[0,1]
	v_cndmask_b32_e64 v33, v3, v7, s[10:11]
	v_cndmask_b32_e64 v32, v2, v6, s[10:11]
	v_pk_mul_f32 v[30:31], v[32:33], v[30:31] op_sel:[0,1] op_sel_hi:[1,0]
	ds_swizzle_b32 v32, v26 offset:swizzle(SWAP,1)
	ds_swizzle_b32 v33, v27 offset:swizzle(SWAP,1)
	ds_swizzle_b32 v34, v24 offset:swizzle(SWAP,1)
	ds_swizzle_b32 v35, v25 offset:swizzle(SWAP,1)
	ds_swizzle_b32 v38, v28 offset:swizzle(SWAP,1)
	ds_swizzle_b32 v39, v29 offset:swizzle(SWAP,1)
	ds_swizzle_b32 v36, v30 offset:swizzle(SWAP,1)
	ds_swizzle_b32 v37, v31 offset:swizzle(SWAP,1)
	v_lshl_add_u64 v[44:45], v[46:47], 0, v[50:51]
	v_lshl_add_u64 v[44:45], v[70:71], 1, v[44:45]
	v_lshl_add_u64 v[44:45], v[44:45], 0, v[64:65]
	global_store_dwordx4 v[44:45], v[40:43], off nt
	s_and_saveexec_b64 s[12:13], s[2:3]
	s_cbranch_execz .LBB0_244
	v_lshl_add_u32 v48, v128, 6, s60
	ds_read2_b32 v[40:41], v48 offset0:8 offset1:9
	ds_read2_b32 v[42:43], v48 offset0:10 offset1:11
	ds_read2_b32 v[44:45], v48 offset0:12 offset1:13
	ds_read2_b32 v[46:47], v48 offset0:14 offset1:15
	s_waitcnt lgkmcnt(3)
	v_pk_mul_f32 v[32:33], v[40:41], v[32:33]
	s_waitcnt lgkmcnt(2)
	v_pk_mul_f32 v[34:35], v[42:43], v[34:35]
	s_waitcnt lgkmcnt(1)
	v_pk_mul_f32 v[38:39], v[44:45], v[38:39]
	ds_read2_b32 v[40:41], v48 offset1:1
	ds_read2_b32 v[42:43], v48 offset0:2 offset1:3
	ds_read2_b32 v[44:45], v48 offset0:4 offset1:5
	ds_read2_b32 v[48:49], v48 offset0:6 offset1:7
	s_waitcnt lgkmcnt(4)
	v_pk_mul_f32 v[36:37], v[46:47], v[36:37]
	v_cndmask_b32_e64 v33, v33, -v33, s[4:5]
	v_cndmask_b32_e64 v32, v32, -v32, s[4:5]
	v_cndmask_b32_e64 v35, v35, -v35, s[4:5]
	v_cndmask_b32_e64 v34, v34, -v34, s[4:5]
	v_cndmask_b32_e64 v38, v38, -v38, s[4:5]
	v_cndmask_b32_e64 v39, v39, -v39, s[4:5]
	v_cndmask_b32_e64 v36, v36, -v36, s[4:5]
	v_cndmask_b32_e64 v37, v37, -v37, s[4:5]
	s_waitcnt lgkmcnt(0)
	v_pk_fma_f32 v[30:31], v[30:31], v[48:49], v[36:37]
	v_pk_fma_f32 v[28:29], v[28:29], v[44:45], v[38:39]
	v_pk_fma_f32 v[24:25], v[24:25], v[42:43], v[34:35]
	v_pk_fma_f32 v[26:27], v[26:27], v[40:41], v[32:33]
.LBB0_244:
	s_or_b64 exec, exec, s[12:13]
	s_waitcnt vmcnt(10)
	v_lshlrev_b32_e32 v40, 16, v20
	v_and_b32_e32 v41, 0xffff0000, v20
	s_waitcnt lgkmcnt(2)
	v_pk_mul_f32 v[38:39], v[40:41], v[40:41]
	v_lshlrev_b32_e32 v20, 16, v21
	v_and_b32_e32 v21, 0xffff0000, v21
	v_pk_mul_f32 v[42:43], v[20:21], v[20:21]
	v_add_f32_e32 v33, v38, v39
	v_lshlrev_b32_e32 v44, 16, v22
	v_and_b32_e32 v45, 0xffff0000, v22
	v_add_f32_e32 v33, v42, v33
	v_and_b32_e32 v34, 0xffff0000, v23
	v_lshlrev_b32_e32 v35, 16, v23
	v_pk_mul_f32 v[22:23], v[44:45], v[44:45]
	v_add_f32_e32 v33, v43, v33
	v_add_f32_e32 v22, v22, v33
	s_waitcnt lgkmcnt(0)
	v_pk_mul_f32 v[36:37], v[34:35], v[34:35]
	v_add_f32_e32 v22, v23, v22
	v_add_f32_e32 v22, v37, v22
	v_add_f32_e32 v33, v36, v22
	ds_swizzle_b32 v38, v33 offset:swizzle(SWAP,1)
	v_cndmask_b32_e64 v32, v119, 1.0, s[10:11]
	v_pk_mul_f32 v[22:23], v[32:33], v[26:27] op_sel_hi:[0,1]
	v_cvt_pk_bf16_f32 v36, v22, v23
	v_pk_mul_f32 v[22:23], v[32:33], v[24:25] op_sel_hi:[0,1]
	s_waitcnt lgkmcnt(0)
	v_add_f32_e32 v24, v33, v38
	ds_swizzle_b32 v25, v24 offset:swizzle(SWAP,2)
	v_cvt_pk_bf16_f32 v37, v22, v23
	v_pk_mul_f32 v[22:23], v[32:33], v[28:29] op_sel_hi:[0,1]
	v_cvt_pk_bf16_f32 v38, v22, v23
	v_pk_mul_f32 v[22:23], v[32:33], v[30:31] op_sel_hi:[0,1]
	s_waitcnt lgkmcnt(0)
	v_add_f32_e32 v24, v24, v25
	ds_swizzle_b32 v25, v24 offset:swizzle(SWAP,4)
	v_cvt_pk_bf16_f32 v39, v22, v23
	v_add_u32_e32 v26, s97, v128
	v_mov_b64_e32 v[22:23], s[38:39]
	v_mad_i64_i32 v[42:43], s[12:13], v26, s83, v[22:23]
	s_waitcnt lgkmcnt(0)
	v_add_f32_e32 v22, v24, v25
	v_fmamk_f32 v22, v22, 0x3c800000, v107
	v_mul_f32_e32 v23, 0x4f800000, v22
	v_cmp_gt_f32_e32 vcc, s84, v22
	v_cndmask_b32_e64 v46, 0, v120, s[10:11]
	v_mov_b32_e32 v47, v65
	v_cndmask_b32_e32 v22, v22, v23, vcc
	v_sqrt_f32_e32 v24, v22
	v_cndmask_b32_e64 v23, v9, v13, s[8:9]
	v_add_u32_e32 v25, -1, v24
	v_fma_f32 v26, -v25, v24, v22
	v_cmp_ge_f32_e64 s[10:11], 0, v26
	v_add_u32_e32 v26, 1, v24
	s_nop 0
	v_cndmask_b32_e64 v25, v24, v25, s[10:11]
	v_fma_f32 v24, -v26, v24, v22
	v_cmp_lt_f32_e64 s[10:11], 0, v24
	s_nop 1
	v_cndmask_b32_e64 v24, v25, v26, s[10:11]
	v_mul_f32_e32 v25, 0x37800000, v24
	v_cndmask_b32_e32 v24, v24, v25, vcc
	v_cmp_class_f32_e32 vcc, v22, v108
	v_cndmask_b32_e64 v25, v11, v15, s[8:9]
	s_nop 0
	v_cndmask_b32_e32 v26, v24, v22, vcc
	v_div_scale_f32 v27, s[10:11], v26, v26, 1.0
	v_rcp_f32_e32 v28, v27
	v_cndmask_b32_e64 v22, v8, v12, s[8:9]
	v_cndmask_b32_e64 v24, v10, v14, s[8:9]
	v_fma_f32 v29, -v27, v28, 1.0
	v_fmac_f32_e32 v28, v29, v28
	v_div_scale_f32 v29, vcc, 1.0, v26, 1.0
	v_mul_f32_e32 v30, v29, v28
	v_fma_f32 v31, -v27, v30, v29
	v_fmac_f32_e32 v30, v31, v28
	v_fma_f32 v27, -v27, v30, v29
	v_div_fmas_f32 v27, v27, v28, v30
	v_div_fixup_f32 v28, v27, v26, 1.0
	v_pk_mul_f32 v[26:27], v[28:29], v[40:41] op_sel_hi:[0,1]
	v_pk_mul_f32 v[20:21], v[28:29], v[20:21] op_sel_hi:[0,1]
	v_pk_mul_f32 v[26:27], v[22:23], v[26:27]
	v_pk_mul_f32 v[20:21], v[24:25], v[20:21]
	v_pk_mul_f32 v[22:23], v[28:29], v[44:45] op_sel_hi:[0,1]
	v_cndmask_b32_e64 v25, v1, v5, s[8:9]
	v_cndmask_b32_e64 v24, v0, v4, s[8:9]
	v_pk_mul_f32 v[22:23], v[24:25], v[22:23]
	v_pk_mul_f32 v[24:25], v[28:29], v[34:35] op_sel_hi:[0,1]
	v_cndmask_b32_e64 v29, v3, v7, s[8:9]
	v_cndmask_b32_e64 v28, v2, v6, s[8:9]
	v_pk_mul_f32 v[24:25], v[28:29], v[24:25] op_sel:[0,1] op_sel_hi:[1,0]
	ds_swizzle_b32 v28, v26 offset:swizzle(SWAP,1)
	ds_swizzle_b32 v29, v27 offset:swizzle(SWAP,1)
	ds_swizzle_b32 v30, v20 offset:swizzle(SWAP,1)
	ds_swizzle_b32 v31, v21 offset:swizzle(SWAP,1)
	ds_swizzle_b32 v34, v22 offset:swizzle(SWAP,1)
	ds_swizzle_b32 v35, v23 offset:swizzle(SWAP,1)
	ds_swizzle_b32 v32, v24 offset:swizzle(SWAP,1)
	ds_swizzle_b32 v33, v25 offset:swizzle(SWAP,1)
	v_lshl_add_u64 v[40:41], v[42:43], 0, v[46:47]
	v_lshl_add_u64 v[40:41], v[68:69], 1, v[40:41]
	v_lshl_add_u64 v[40:41], v[40:41], 0, v[64:65]
	global_store_dwordx4 v[40:41], v[36:39], off nt
	s_and_saveexec_b64 s[10:11], s[2:3]
	s_cbranch_execz .LBB0_246
	v_lshl_add_u32 v44, v126, 6, s60
	ds_read2_b32 v[36:37], v44 offset0:8 offset1:9
	ds_read2_b32 v[38:39], v44 offset0:10 offset1:11
	ds_read2_b32 v[40:41], v44 offset0:12 offset1:13
	ds_read2_b32 v[42:43], v44 offset0:14 offset1:15
	s_waitcnt lgkmcnt(3)
	v_pk_mul_f32 v[28:29], v[36:37], v[28:29]
	s_waitcnt lgkmcnt(2)
	v_pk_mul_f32 v[30:31], v[38:39], v[30:31]
	s_waitcnt lgkmcnt(1)
	v_pk_mul_f32 v[34:35], v[40:41], v[34:35]
	ds_read2_b32 v[36:37], v44 offset1:1
	ds_read2_b32 v[38:39], v44 offset0:2 offset1:3
	ds_read2_b32 v[40:41], v44 offset0:4 offset1:5
	ds_read2_b32 v[44:45], v44 offset0:6 offset1:7
	s_waitcnt lgkmcnt(4)
	v_pk_mul_f32 v[32:33], v[42:43], v[32:33]
	v_cndmask_b32_e64 v29, v29, -v29, s[4:5]
	v_cndmask_b32_e64 v28, v28, -v28, s[4:5]
	v_cndmask_b32_e64 v31, v31, -v31, s[4:5]
	v_cndmask_b32_e64 v30, v30, -v30, s[4:5]
	v_cndmask_b32_e64 v34, v34, -v34, s[4:5]
	v_cndmask_b32_e64 v35, v35, -v35, s[4:5]
	v_cndmask_b32_e64 v32, v32, -v32, s[4:5]
	v_cndmask_b32_e64 v33, v33, -v33, s[4:5]
	s_waitcnt lgkmcnt(0)
	v_pk_fma_f32 v[24:25], v[24:25], v[44:45], v[32:33]
	v_pk_fma_f32 v[22:23], v[22:23], v[40:41], v[34:35]
	v_pk_fma_f32 v[20:21], v[20:21], v[38:39], v[30:31]
	v_pk_fma_f32 v[26:27], v[26:27], v[36:37], v[28:29]
.LBB0_246:
	s_or_b64 exec, exec, s[10:11]
	s_waitcnt vmcnt(10)
	v_lshlrev_b32_e32 v36, 16, v16
	v_and_b32_e32 v37, 0xffff0000, v16
	s_waitcnt lgkmcnt(7)
	v_cndmask_b32_e64 v28, v119, 1.0, s[8:9]
	s_waitcnt lgkmcnt(2)
	v_pk_mul_f32 v[34:35], v[36:37], v[36:37]
	v_lshlrev_b32_e32 v16, 16, v17
	v_and_b32_e32 v17, 0xffff0000, v17
	v_pk_mul_f32 v[26:27], v[28:29], v[26:27] op_sel_hi:[0,1]
	v_pk_mul_f32 v[38:39], v[16:17], v[16:17]
	v_add_f32_e32 v29, v34, v35
	v_lshlrev_b32_e32 v40, 16, v18
	v_and_b32_e32 v41, 0xffff0000, v18
	v_add_f32_e32 v29, v38, v29
	s_waitcnt lgkmcnt(1)
	v_cvt_pk_bf16_f32 v32, v26, v27
	v_and_b32_e32 v26, 0xffff0000, v19
	v_lshlrev_b32_e32 v27, 16, v19
	v_pk_mul_f32 v[18:19], v[40:41], v[40:41]
	v_add_f32_e32 v29, v39, v29
	v_add_f32_e32 v18, v18, v29
	v_pk_mul_f32 v[30:31], v[26:27], v[26:27]
	v_add_f32_e32 v18, v19, v18
	v_add_f32_e32 v18, v31, v18
	v_add_f32_e32 v29, v30, v18
	ds_swizzle_b32 v30, v29 offset:swizzle(SWAP,1)
	v_pk_mul_f32 v[18:19], v[28:29], v[20:21] op_sel_hi:[0,1]
	s_waitcnt lgkmcnt(1)
	v_cvt_pk_bf16_f32 v33, v18, v19
	v_pk_mul_f32 v[18:19], v[28:29], v[22:23] op_sel_hi:[0,1]
	v_cvt_pk_bf16_f32 v34, v18, v19
	s_waitcnt lgkmcnt(0)
	v_add_f32_e32 v20, v29, v30
	ds_swizzle_b32 v21, v20 offset:swizzle(SWAP,2)
	v_pk_mul_f32 v[18:19], v[28:29], v[24:25] op_sel_hi:[0,1]
	v_cvt_pk_bf16_f32 v35, v18, v19
	v_add_u32_e32 v22, s97, v126
	v_mov_b64_e32 v[18:19], s[38:39]
	s_waitcnt lgkmcnt(0)
	v_add_f32_e32 v20, v20, v21
	ds_swizzle_b32 v21, v20 offset:swizzle(SWAP,4)
	v_mad_i64_i32 v[38:39], s[10:11], v22, s83, v[18:19]
	v_cndmask_b32_e64 v42, 0, v120, s[8:9]
	v_cndmask_b32_e64 v25, v1, v5, s[6:7]
	s_waitcnt lgkmcnt(0)
	v_add_f32_e32 v18, v20, v21
	v_fmamk_f32 v18, v18, 0x3c800000, v107
	v_mul_f32_e32 v19, 0x4f800000, v18
	v_cmp_gt_f32_e32 vcc, s84, v18
	v_cndmask_b32_e64 v21, v11, v15, s[6:7]
	v_mov_b32_e32 v43, v65
	v_cndmask_b32_e32 v20, v18, v19, vcc
	v_sqrt_f32_e32 v22, v20
	v_cndmask_b32_e64 v19, v9, v13, s[6:7]
	v_cndmask_b32_e64 v18, v8, v12, s[6:7]
	v_add_u32_e32 v23, -1, v22
	v_fma_f32 v24, -v23, v22, v20
	v_cmp_ge_f32_e64 s[8:9], 0, v24
	v_add_u32_e32 v24, 1, v22
	s_nop 0
	v_cndmask_b32_e64 v23, v22, v23, s[8:9]
	v_fma_f32 v22, -v24, v22, v20
	v_cmp_lt_f32_e64 s[8:9], 0, v22
	s_nop 1
	v_cndmask_b32_e64 v22, v23, v24, s[8:9]
	v_mul_f32_e32 v23, 0x37800000, v22
	v_cndmask_b32_e32 v22, v22, v23, vcc
	v_cmp_class_f32_e32 vcc, v20, v108
	v_cndmask_b32_e64 v24, v0, v4, s[6:7]
	s_nop 0
	v_cndmask_b32_e32 v22, v22, v20, vcc
	v_div_scale_f32 v23, s[8:9], v22, v22, 1.0
	v_rcp_f32_e32 v28, v23
	v_cndmask_b32_e64 v20, v10, v14, s[6:7]
	v_fma_f32 v29, -v23, v28, 1.0
	v_fmac_f32_e32 v28, v29, v28
	v_div_scale_f32 v29, vcc, 1.0, v22, 1.0
	v_mul_f32_e32 v30, v29, v28
	v_fma_f32 v31, -v23, v30, v29
	v_fmac_f32_e32 v30, v31, v28
	v_fma_f32 v23, -v23, v30, v29
	v_div_fmas_f32 v23, v23, v28, v30
	v_div_fixup_f32 v28, v23, v22, 1.0
	v_pk_mul_f32 v[16:17], v[28:29], v[16:17] op_sel_hi:[0,1]
	v_pk_mul_f32 v[22:23], v[28:29], v[36:37] op_sel_hi:[0,1]
	v_pk_mul_f32 v[20:21], v[20:21], v[16:17]
	v_pk_mul_f32 v[16:17], v[28:29], v[40:41] op_sel_hi:[0,1]
	v_pk_mul_f32 v[22:23], v[18:19], v[22:23]
	v_pk_mul_f32 v[16:17], v[24:25], v[16:17]
	v_cndmask_b32_e64 v19, v3, v7, s[6:7]
	v_cndmask_b32_e64 v18, v2, v6, s[6:7]
	v_pk_mul_f32 v[24:25], v[28:29], v[26:27] op_sel_hi:[0,1]
	v_pk_mul_f32 v[18:19], v[18:19], v[24:25] op_sel:[0,1] op_sel_hi:[1,0]
	ds_swizzle_b32 v24, v22 offset:swizzle(SWAP,1)
	ds_swizzle_b32 v25, v23 offset:swizzle(SWAP,1)
	ds_swizzle_b32 v26, v20 offset:swizzle(SWAP,1)
	ds_swizzle_b32 v27, v21 offset:swizzle(SWAP,1)
	ds_swizzle_b32 v30, v16 offset:swizzle(SWAP,1)
	ds_swizzle_b32 v31, v17 offset:swizzle(SWAP,1)
	ds_swizzle_b32 v28, v18 offset:swizzle(SWAP,1)
	ds_swizzle_b32 v29, v19 offset:swizzle(SWAP,1)
	v_lshl_add_u64 v[36:37], v[38:39], 0, v[42:43]
	v_lshl_add_u64 v[36:37], v[62:63], 1, v[36:37]
	v_lshl_add_u64 v[36:37], v[36:37], 0, v[64:65]
	global_store_dwordx4 v[36:37], v[32:35], off nt
	s_and_saveexec_b64 s[8:9], s[2:3]
	s_cbranch_execz .LBB0_223
	v_lshl_add_u32 v40, v127, 6, s60
	ds_read2_b32 v[32:33], v40 offset0:8 offset1:9
	ds_read2_b32 v[34:35], v40 offset0:10 offset1:11
	ds_read2_b32 v[36:37], v40 offset0:12 offset1:13
	ds_read2_b32 v[38:39], v40 offset0:14 offset1:15
	s_waitcnt lgkmcnt(3)
	v_pk_mul_f32 v[24:25], v[32:33], v[24:25]
	s_waitcnt lgkmcnt(2)
	v_pk_mul_f32 v[26:27], v[34:35], v[26:27]
	s_waitcnt lgkmcnt(1)
	v_pk_mul_f32 v[30:31], v[36:37], v[30:31]
	ds_read2_b32 v[32:33], v40 offset1:1
	ds_read2_b32 v[34:35], v40 offset0:2 offset1:3
	ds_read2_b32 v[36:37], v40 offset0:4 offset1:5
	ds_read2_b32 v[40:41], v40 offset0:6 offset1:7
	s_waitcnt lgkmcnt(4)
	v_pk_mul_f32 v[28:29], v[38:39], v[28:29]
	v_cndmask_b32_e64 v25, v25, -v25, s[4:5]
	v_cndmask_b32_e64 v24, v24, -v24, s[4:5]
	v_cndmask_b32_e64 v27, v27, -v27, s[4:5]
	v_cndmask_b32_e64 v26, v26, -v26, s[4:5]
	v_cndmask_b32_e64 v30, v30, -v30, s[4:5]
	v_cndmask_b32_e64 v31, v31, -v31, s[4:5]
	v_cndmask_b32_e64 v28, v28, -v28, s[4:5]
	v_cndmask_b32_e64 v29, v29, -v29, s[4:5]
	s_waitcnt lgkmcnt(0)
	v_pk_fma_f32 v[18:19], v[18:19], v[40:41], v[28:29]
	v_pk_fma_f32 v[16:17], v[16:17], v[36:37], v[30:31]
	v_pk_fma_f32 v[20:21], v[20:21], v[34:35], v[26:27]
	v_pk_fma_f32 v[22:23], v[22:23], v[32:33], v[24:25]
	s_branch .LBB0_223

.LBB0_249:
	s_waitcnt lgkmcnt(0)
	s_barrier
	s_lshl_b32 s6, s22, 2
	v_lshrrev_b32_e32 v2, 3, v67
	v_and_b32_e32 v102, 4, v2
	v_and_b32_e32 v2, 2, v2
	v_bfe_u32 v3, v67, 1, 1
	v_bfe_u32 v64, v67, 2, 2
	v_or3_b32 v123, v2, s6, v3
	v_lshlrev_b32_e32 v2, 3, v67
	v_or_b32_e32 v103, v102, v64
	v_and_b32_e32 v132, 8, v2
	v_bitop3_b32 v2, v102, 63, v64 bitop3:0x36
	v_cndmask_b32_e64 v2, v2, v103, s[2:3]
	v_bitop3_b32 v3, v102, 55, v64 bitop3:0x36
	v_or_b32_e32 v4, 8, v103
	v_lshlrev_b32_e32 v5, 2, v2
	v_cndmask_b32_e64 v3, v3, v4, s[2:3]
	v_lshl_add_u32 v4, v2, 8, s64
	v_and_b32_e32 v5, 12, v5
	v_bfe_u32 v2, v2, 2, 2
	v_bitop3_b32 v2, v5, v123, v2 bitop3:0x36
	v_lshlrev_b32_e32 v2, 4, v2
	v_add3_u32 v8, v4, v2, v132
	v_lshlrev_b32_e32 v2, 2, v3
	v_add3_u32 v12, v0, v1, s10
	v_lshl_add_u32 v4, v3, 8, s64
	v_and_b32_e32 v2, 12, v2
	v_bfe_u32 v3, v3, 2, 2
	v_add_u32_e32 v13, 0x2000, v12
	v_bitop3_b32 v5, v2, v123, v3 bitop3:0x36
	ds_read2_b64 v[0:3], v13 offset0:128 offset1:130
	v_lshlrev_b32_e32 v5, 4, v5
	v_add3_u32 v9, v4, v5, v132
	ds_read_b64_tr_b16 v[4:5], v8 offset:32768
	ds_read_b64_tr_b16 v[6:7], v9 offset:32768
	ds_read_b64_tr_b16 v[10:11], v9
	ds_read_b64_tr_b16 v[8:9], v8
	v_add_u32_e32 v133, 0x4800, v12
	s_waitcnt lgkmcnt(2)
	v_mfma_f32_32x32x16_bf16 v[48:63], v[0:3], v[4:7], 0
	ds_read2_b64 v[0:3], v133 offset1:2
	v_add_u32_e32 v134, 0x3000, v12
	v_or_b32_e32 v124, 16, v103
	v_bitop3_b32 v125, v102, 47, v64 bitop3:0x36
	v_cndmask_b32_e64 v124, v125, v124, s[2:3]
	v_bitop3_b32 v125, v103, 55, 16 bitop3:0x36
	v_or_b32_e32 v126, 24, v103
	s_waitcnt lgkmcnt(0)
	v_mfma_f32_32x32x16_bf16 v[32:47], v[8:11], v[0:3], 0
	ds_read2_b64 v[0:3], v134 offset0:192 offset1:194
	v_lshlrev_b32_e32 v127, 2, v124
	v_cndmask_b32_e64 v125, v125, v126, s[2:3]
	v_lshl_add_u32 v126, v124, 8, s64
	v_and_b32_e32 v127, 12, v127
	v_bfe_u32 v124, v124, 2, 2
	v_bitop3_b32 v124, v127, v123, v124 bitop3:0x36
	v_lshlrev_b32_e32 v124, 4, v124
	v_add3_u32 v128, v126, v124, v132
	v_lshlrev_b32_e32 v126, 2, v125
	v_lshl_add_u32 v124, v125, 8, s64
	v_and_b32_e32 v126, 12, v126
	v_bfe_u32 v125, v125, 2, 2
	v_add_u32_e32 v135, 0x5800, v12
	v_bitop3_b32 v125, v126, v123, v125 bitop3:0x36
	s_waitcnt lgkmcnt(0)
	v_mfma_f32_32x32x16_bf16 v[16:31], v[0:3], v[4:7], 0
	ds_read2_b64 v[0:3], v135 offset0:64 offset1:66
	ds_read2_b64 v[98:101], v13 offset0:132 offset1:134
	v_lshlrev_b32_e32 v125, 4, v125
	v_add3_u32 v129, v124, v125, v132
	ds_read_b64_tr_b16 v[124:125], v128 offset:32768
	ds_read_b64_tr_b16 v[126:127], v129 offset:32768
	ds_read_b64_tr_b16 v[130:131], v129
	ds_read_b64_tr_b16 v[128:129], v128
	s_mov_b32 s46, s21
	s_waitcnt lgkmcnt(2)
	v_mfma_f32_32x32x16_bf16 v[48:63], v[98:101], v[124:127], v[48:63]
	ds_read2_b64 v[98:101], v133 offset0:4 offset1:6
	s_waitcnt lgkmcnt(0)
	v_mfma_f32_32x32x16_bf16 v[32:47], v[128:131], v[98:101], v[32:47]
	ds_read2_b64 v[98:101], v134 offset0:196 offset1:198
	s_nop 7
	v_cvt_pk_bf16_f32 v48, v48, v49
	v_cvt_pk_bf16_f32 v49, v50, v51
	v_cvt_pk_bf16_f32 v50, v52, v53
	v_cvt_pk_bf16_f32 v51, v54, v55
	v_cvt_pk_bf16_f32 v52, v56, v57
	v_cvt_pk_bf16_f32 v53, v58, v59
	v_mfma_f32_32x32x16_bf16 v[0:15], v[8:11], v[0:3], 0
	v_xor_b32_e32 v34, 0x80000000, v34
	v_xor_b32_e32 v35, 0x80000000, v35
	v_xor_b32_e32 v36, 0x80000000, v36
	v_xor_b32_e32 v37, 0x80000000, v37
	v_xor_b32_e32 v33, 0x80000000, v33
	v_xor_b32_e32 v32, 0x80000000, v32
	v_xor_b32_e32 v38, 0x80000000, v38
	s_waitcnt lgkmcnt(0)
	v_mfma_f32_32x32x16_bf16 v[16:31], v[98:101], v[124:127], v[16:31]
	ds_read2_b64 v[98:101], v135 offset0:68 offset1:70
	v_xor_b32_e32 v39, 0x80000000, v39
	v_cvt_pk_bf16_f32 v32, v32, v33
	v_cvt_pk_bf16_f32 v33, v34, v35
	v_cvt_pk_bf16_f32 v34, v36, v37
	v_xor_b32_e32 v40, 0x80000000, v40
	v_xor_b32_e32 v41, 0x80000000, v41
	s_waitcnt lgkmcnt(0)
	v_mfma_f32_32x32x16_bf16 v[0:15], v[128:131], v[98:101], v[0:15]
	v_or_b32_e32 v98, 32, v103
	v_bitop3_b32 v99, v102, 31, v64 bitop3:0x36
	v_cndmask_b32_e64 v98, v99, v98, s[2:3]
	v_bitop3_b32 v99, v103, 55, 32 bitop3:0x36
	v_or_b32_e32 v100, 40, v103
	v_lshlrev_b32_e32 v101, 2, v98
	v_cndmask_b32_e64 v99, v99, v100, s[2:3]
	v_lshl_add_u32 v100, v98, 8, s64
	v_and_b32_e32 v101, 12, v101
	v_bfe_u32 v98, v98, 2, 2
	v_bitop3_b32 v98, v101, v123, v98 bitop3:0x36
	v_lshlrev_b32_e32 v98, 4, v98
	v_add3_u32 v128, v100, v98, v132
	v_lshlrev_b32_e32 v98, 2, v99
	v_lshl_add_u32 v124, v99, 8, s64
	v_and_b32_e32 v98, 12, v98
	v_bfe_u32 v99, v99, 2, 2
	v_bitop3_b32 v125, v98, v123, v99 bitop3:0x36
	ds_read2_b64 v[98:101], v134 offset0:200 offset1:202
	v_lshlrev_b32_e32 v125, 4, v125
	v_add3_u32 v129, v124, v125, v132
	ds_read_b64_tr_b16 v[124:125], v128 offset:32768
	ds_read_b64_tr_b16 v[126:127], v129 offset:32768
	ds_read_b64_tr_b16 v[130:131], v129
	ds_read_b64_tr_b16 v[128:129], v128
	s_waitcnt lgkmcnt(2)
	v_mfma_f32_32x32x16_bf16 v[16:31], v[98:101], v[124:127], v[16:31]
	ds_read2_b64 v[98:101], v135 offset0:72 offset1:74
	v_bitop3_b32 v64, v102, 15, v64 bitop3:0x36
	v_xor_b32_e32 v42, 0x80000000, v42
	v_xor_b32_e32 v43, 0x80000000, v43
	v_xor_b32_e32 v44, 0x80000000, v44
	v_xor_b32_e32 v45, 0x80000000, v45
	v_xor_b32_e32 v46, 0x80000000, v46
	s_waitcnt lgkmcnt(0)
	v_mfma_f32_32x32x16_bf16 v[0:15], v[128:131], v[98:101], v[0:15]
	v_or_b32_e32 v98, 48, v103
	v_cndmask_b32_e64 v64, v64, v98, s[2:3]
	v_bitop3_b32 v98, v103, 55, 48 bitop3:0x36
	v_or_b32_e32 v99, 56, v103
	v_lshlrev_b32_e32 v100, 2, v64
	v_cndmask_b32_e64 v98, v98, v99, s[2:3]
	v_lshl_add_u32 v99, v64, 8, s64
	v_and_b32_e32 v100, 12, v100
	v_bfe_u32 v64, v64, 2, 2
	v_bitop3_b32 v64, v100, v123, v64 bitop3:0x36
	v_lshlrev_b32_e32 v64, 4, v64
	v_add3_u32 v64, v99, v64, v132
	v_lshlrev_b32_e32 v99, 2, v98
	v_lshl_add_u32 v102, v98, 8, s64
	v_and_b32_e32 v99, 12, v99
	v_bfe_u32 v98, v98, 2, 2
	v_bitop3_b32 v103, v99, v123, v98 bitop3:0x36
	ds_read2_b64 v[98:101], v134 offset0:204 offset1:206
	v_lshlrev_b32_e32 v103, 4, v103
	v_add3_u32 v102, v102, v103, v132
	ds_read_b64_tr_b16 v[124:125], v64 offset:32768
	ds_read_b64_tr_b16 v[126:127], v102 offset:32768
	ds_read_b64_tr_b16 v[130:131], v102
	ds_read_b64_tr_b16 v[128:129], v64
	s_waitcnt lgkmcnt(2)
	v_mfma_f32_32x32x16_bf16 v[16:31], v[98:101], v[124:127], v[16:31]
	ds_read2_b64 v[98:101], v135 offset0:76 offset1:78
	v_and_b32_e32 v64, 63, v67
	s_add_u32 s2, s4, 0xe000
	s_addc_u32 s3, s5, 0
	s_lshl_b32 s6, s22, 1
	v_xor_b32_e32 v47, 0x80000000, v47
	v_cvt_pk_bf16_f32 v35, v38, v39
	s_waitcnt lgkmcnt(0)
	v_mfma_f32_32x32x16_bf16 v[0:15], v[128:131], v[98:101], v[0:15]
	v_lshlrev_b32_e32 v99, 4, v64
	v_lshlrev_b32_e32 v98, 5, v64
	v_lshl_or_b32 v64, s22, 11, v99
	v_lshl_add_u64 v[36:37], s[4:5], 0, v[64:65]
	v_lshl_or_b32 v56, s22, 12, v98
	s_or_b32 s6, s6, 1
	v_cvt_pk_bf16_f32 v54, v60, v61
	s_nop 4
	v_xor_b32_e32 v2, 0x80000000, v2
	v_xor_b32_e32 v3, 0x80000000, v3
	v_xor_b32_e32 v4, 0x80000000, v4
	v_xor_b32_e32 v5, 0x80000000, v5
	v_xor_b32_e32 v1, 0x80000000, v1
	v_xor_b32_e32 v0, 0x80000000, v0
	v_xor_b32_e32 v6, 0x80000000, v6
	v_xor_b32_e32 v7, 0x80000000, v7
	v_cvt_pk_bf16_f32 v0, v0, v1
	v_cvt_pk_bf16_f32 v1, v2, v3
	v_cvt_pk_bf16_f32 v2, v4, v5
	v_add_co_u32_e32 v4, vcc, s93, v36
	v_cvt_pk_bf16_f32 v55, v62, v63
	global_store_dwordx4 v56, v[48:51], s[2:3] nt
	global_store_dwordx4 v56, v[52:55], s[2:3] offset:16 nt
	global_store_dwordx4 v64, v[32:35], s[4:5] nt
	v_lshl_or_b32 v38, s6, 10, v99
	v_cvt_pk_bf16_f32 v16, v16, v17
	v_cvt_pk_bf16_f32 v32, v40, v41
	v_cvt_pk_bf16_f32 v33, v42, v43
	v_cvt_pk_bf16_f32 v34, v44, v45
	v_cvt_pk_bf16_f32 v35, v46, v47
	v_cvt_pk_bf16_f32 v17, v18, v19
	v_cvt_pk_bf16_f32 v18, v20, v21
	v_cvt_pk_bf16_f32 v19, v22, v23
	v_cvt_pk_bf16_f32 v20, v24, v25
	v_lshl_or_b32 v24, s6, 11, v98
	v_xor_b32_e32 v8, 0x80000000, v8
	v_xor_b32_e32 v9, 0x80000000, v9
	v_xor_b32_e32 v10, 0x80000000, v10
	v_xor_b32_e32 v11, 0x80000000, v11
	v_xor_b32_e32 v12, 0x80000000, v12
	v_xor_b32_e32 v13, 0x80000000, v13
	v_xor_b32_e32 v14, 0x80000000, v14
	v_xor_b32_e32 v15, 0x80000000, v15
	v_cvt_pk_bf16_f32 v3, v6, v7
	v_addc_co_u32_e32 v5, vcc, 0, v37, vcc
	s_add_i32 s20, s20, 2
	global_store_dwordx4 v38, v[32:35], s[4:5] nt
	v_cvt_pk_bf16_f32 v21, v26, v27
	v_cvt_pk_bf16_f32 v22, v28, v29
	v_cvt_pk_bf16_f32 v23, v30, v31
	global_store_dwordx4 v24, v[16:19], s[2:3] nt
	global_store_dwordx4 v24, v[20:23], s[2:3] offset:16 nt
	global_store_dwordx4 v[4:5], v[0:3], off nt
	s_cmp_eq_u32 s21, 6
	v_mov_b32_e32 v123, v67
	v_cvt_pk_bf16_f32 v0, v8, v9
	v_cvt_pk_bf16_f32 v1, v10, v11
	v_cvt_pk_bf16_f32 v2, v12, v13
	v_cvt_pk_bf16_f32 v3, v14, v15
	global_store_dwordx4 v[4:5], v[0:3], off offset:1024 nt
	s_cbranch_scc1 .LBB0_215

.LBB0_325:
	s_or_b64 exec, exec, s[14:15]
	s_and_b64 s[12:13], s[12:13], exec
	s_cselect_b32 s14, 0, 0x1000
	s_and_b64 s[12:13], s[10:11], exec
	s_cselect_b32 s12, 0x800, 0
	s_or_b32 s12, s14, s12
	v_lshl_or_b32 v64, v17, 4, s12
	v_cvt_pk_bf16_f32 v18, v20, v0
	v_cvt_pk_bf16_f32 v20, v1, v4
	v_lshl_add_u64 v[0:1], s[4:5], 0, v[64:65]
	v_lshl_add_u64 v[14:15], v[0:1], 0, s[48:49]
	v_add_co_u32_e32 v0, vcc, s91, v0
	v_cvt_pk_bf16_f32 v19, v19, v2
	s_waitcnt lgkmcnt(0)
	v_cvt_pk_bf16_f32 v21, v3, v6
	v_addc_co_u32_e32 v1, vcc, 0, v1, vcc
	global_store_dwordx4 v[0:1], v[18:21], off nt
	v_cvt_pk_bf16_f32 v0, v5, v8
	v_cvt_pk_bf16_f32 v1, v7, v10
	v_cvt_pk_bf16_f32 v2, v9, v12
	v_cvt_pk_bf16_f32 v3, v11, v13
	global_store_dwordx4 v[14:15], v[0:3], off offset:1024 nt

.LBB0_329:
	s_add_i32 s26, s16, 16
	s_cmp_gt_i32 s26, 15
	s_mov_b64 s[14:15], -1
	s_cbranch_scc0 .LBB0_331
	s_and_b32 s14, s26, 3
	s_lshl_b32 s15, s14, 4
	v_or_b32_e32 v9, s15, v3
	v_bitop3_b32 v10, s15, 63, v3 bitop3:0x36
	v_cndmask_b32_e64 v10, v10, v9, s[2:3]
	v_bitop3_b32 v11, s15, 55, v3 bitop3:0x36
	v_or_b32_e32 v9, 8, v9
	v_lshlrev_b32_e32 v13, 2, v10
	v_cndmask_b32_e64 v9, v11, v9, s[2:3]
	v_and_or_b32 v11, s16, -4, v4
	v_lshl_add_u32 v12, v10, 8, s64
	v_and_b32_e32 v13, 12, v13
	v_bfe_u32 v10, v10, 2, 2
	v_bitop3_b32 v10, v13, v11, v10 bitop3:0x36
	v_lshlrev_b32_e32 v10, 4, v10
	v_add3_u32 v10, v12, v10, v5
	v_lshlrev_b32_e32 v12, 2, v9
	ds_read_b64_tr_b16 v[14:15], v10
	v_lshl_add_u32 v10, v9, 8, s64
	v_and_b32_e32 v12, 12, v12
	v_bfe_u32 v9, v9, 2, 2
	v_bitop3_b32 v9, v12, v11, v9 bitop3:0x36
	v_lshlrev_b32_e32 v9, 4, v9
	v_lshl_add_u32 v18, s14, 6, v7
	v_add3_u32 v9, v10, v9, v5
	ds_read_b128 v[10:13], v18 offset:1024
	ds_read_b64_tr_b16 v[22:23], v9
	ds_read_b128 v[18:21], v18 offset:1056
	s_waitcnt lgkmcnt(3)
	v_and_b32_e32 v27, 0xffff0000, v14
	v_lshlrev_b32_e32 v26, 16, v14
	s_waitcnt lgkmcnt(2)
	v_pk_mul_f32 v[10:11], v[10:11], v[26:27]
	v_and_b32_e32 v27, 0xffff0000, v15
	v_lshlrev_b32_e32 v26, 16, v15
	v_pk_mul_f32 v[12:13], v[12:13], v[26:27]
	v_cvt_pk_bf16_f32 v10, v10, v11
	v_cvt_pk_bf16_f32 v11, v12, v13
	s_waitcnt lgkmcnt(1)
	v_and_b32_e32 v13, 0xffff0000, v22
	v_lshlrev_b32_e32 v12, 16, v22
	v_and_b32_e32 v15, 0xffff0000, v23
	v_lshlrev_b32_e32 v14, 16, v23
	s_waitcnt lgkmcnt(0)
	v_pk_mul_f32 v[12:13], v[18:19], v[12:13]
	v_pk_mul_f32 v[14:15], v[20:21], v[14:15]
	v_cvt_pk_bf16_f32 v12, v12, v13
	v_cvt_pk_bf16_f32 v13, v14, v15
	global_store_dwordx4 v8, v[10:13], s[12:13] nt
	s_mov_b64 s[14:15], 0
.LBB0_331:
	s_andn2_b64 vcc, exec, s[14:15]
	s_cbranch_vccnz .LBB0_328
	s_and_b32 s14, s17, 0xffffffe0
	v_or_b32_e32 v9, s14, v24
	v_sub_u32_e32 v10, 63, v9
	v_cndmask_b32_e64 v10, v10, v9, s[2:3]
	v_lshlrev_b32_e32 v11, 2, v10
	s_and_b32 s14, s27, 14
	v_and_b32_e32 v13, 12, v11
	v_bfe_u32 v15, v10, 2, 2
	v_lshl_add_u32 v12, v10, 8, v6
	v_bitop3_b32 v10, v13, s14, v15 bitop3:0x36
	v_lshl_add_u32 v9, v9, 2, s23
	v_lshl_add_u32 v10, v10, 4, v12
	ds_read_b32 v14, v9 offset:512
	ds_read_b64 v[10:11], v10 offset:16384
	s_or_b32 s14, s14, 1
	v_bitop3_b32 v9, v13, s14, v15 bitop3:0x36
	v_lshl_add_u32 v9, v9, 4, v12
	ds_read_b64 v[12:13], v9 offset:16384
	s_waitcnt lgkmcnt(1)
	v_lshlrev_b32_e32 v18, 16, v10
	v_and_b32_e32 v19, 0xffff0000, v10
	v_pk_mul_f32 v[18:19], v[14:15], v[18:19] op_sel_hi:[0,1]
	v_cvt_pk_bf16_f32 v10, v18, v19
	v_lshlrev_b32_e32 v18, 16, v11
	v_and_b32_e32 v19, 0xffff0000, v11
	v_pk_mul_f32 v[18:19], v[14:15], v[18:19] op_sel_hi:[0,1]
	v_cvt_pk_bf16_f32 v11, v18, v19
	s_waitcnt lgkmcnt(0)
	v_lshlrev_b32_e32 v18, 16, v12
	v_and_b32_e32 v19, 0xffff0000, v12
	v_pk_mul_f32 v[18:19], v[14:15], v[18:19] op_sel_hi:[0,1]
	v_cvt_pk_bf16_f32 v12, v18, v19
	v_lshlrev_b32_e32 v18, 16, v13
	v_and_b32_e32 v19, 0xffff0000, v13
	v_pk_mul_f32 v[14:15], v[14:15], v[18:19] op_sel_hi:[0,1]
	v_cvt_pk_bf16_f32 v13, v14, v15
	global_store_dwordx4 v[0:1], v[10:13], off nt
	s_branch .LBB0_328
.LBB0_333:
	v_cmp_eq_u32_e32 vcc, 0, v2
	s_and_b64 s[12:13], s[10:11], vcc
	s_and_saveexec_b64 s[10:11], s[12:13]
	s_cbranch_execz .LBB0_335
	v_mov_b32_e32 v0, s23
	ds_read_b32 v0, v0 offset:764
	s_lshl_b64 s[8:9], s[8:9], 2
	s_add_u32 s8, s67, s8
	s_addc_u32 s9, s68, s9
	s_waitcnt lgkmcnt(0)
	global_store_dword v65, v0, s[8:9] nt

.LBB0_1575:
	v_add_u32_e32 v16, s6, v67
	v_ashrrev_i32_e32 v16, 5, v16
	v_and_b32_e32 v52, -8, v16
	v_add_u32_e32 v21, s96, v16
	v_or_b32_e32 v18, 7, v16
	v_add_u32_e32 v35, -1, v52
	v_or_b32_e32 v37, 2, v52
	v_or_b32_e32 v39, 3, v52
	v_or_b32_e32 v41, 4, v52
	v_or_b32_e32 v43, 5, v52
	v_or_b32_e32 v45, 6, v52
	v_add_u32_e32 v47, 8, v52
	v_or_b32_e32 v22, 1, v52
	v_cmp_gt_u32_e32 vcc, s74, v21
	v_mad_i64_i32 v[16:17], s[2:3], v52, s73, v[6:7]
	v_mad_i64_i32 v[18:19], s[2:3], v18, s73, v[6:7]
	v_add_u32_e32 v20, s97, v52
	v_cndmask_b32_e64 v48, 0, 1, vcc
	v_add_u32_e32 v49, s96, v35
	v_add_u32_e32 v50, s96, v47
	v_mad_i64_i32 v[22:23], s[2:3], v22, s73, v[6:7]
	v_mad_i64_i32 v[24:25], s[2:3], v37, s73, v[6:7]
	v_mad_i64_i32 v[26:27], s[2:3], v39, s73, v[6:7]
	v_mad_i64_i32 v[28:29], s[2:3], v41, s73, v[6:7]
	v_mad_i64_i32 v[30:31], s[2:3], v43, s73, v[6:7]
	v_mad_i64_i32 v[32:33], s[2:3], v45, s73, v[6:7]
	v_ashrrev_i32_e32 v21, 31, v20
	v_cndmask_b32_e32 v51, v52, v37, vcc
	v_or_b32_e32 v48, v52, v48
	v_cndmask_b32_e32 v55, v52, v43, vcc
	v_cmp_gt_u32_e64 s[4:5], s74, v49
	v_cmp_gt_u32_e64 s[2:3], s74, v50
	global_load_dwordx2 v[12:13], v[0:1], off
	global_load_dwordx2 v[14:15], v[2:3], off
	global_load_dwordx2 v[10:11], v[4:5], off
	global_load_dword v56, v[16:17], off offset:1024
	global_load_dword v57, v[16:17], off offset:2048
	v_or_b32_e32 v34, 1, v20
	v_or_b32_e32 v36, 2, v20
	v_or_b32_e32 v38, 3, v20
	v_or_b32_e32 v40, 4, v20
	v_or_b32_e32 v42, 5, v20
	v_or_b32_e32 v44, 6, v20
	v_or_b32_e32 v46, 7, v20
	v_cndmask_b32_e32 v53, v52, v39, vcc
	v_cndmask_b32_e32 v54, v52, v41, vcc
	v_cndmask_b32_e32 v58, v52, v45, vcc
	v_cndmask_b32_e64 v59, 0, 7, vcc
	global_load_dword v60, v[28:29], off
	global_load_dword v61, v[30:31], off
	global_load_dword v62, v[32:33], off
	global_load_dword v63, v[18:19], off
	v_cndmask_b32_e64 v64, v52, v35, s[4:5]
	v_cndmask_b32_e64 v68, v52, v47, s[2:3]
	v_lshlrev_b64 v[18:19], 12, v[20:21]
	v_mad_i64_i32 v[20:21], s[8:9], v51, s73, v[6:7]
	v_mad_i64_i32 v[28:29], s[8:9], v48, s73, v[6:7]
	v_mad_i64_i32 v[48:49], s[8:9], v55, s73, v[6:7]
	v_mad_i64_i32 v[30:31], s[8:9], v53, s73, v[6:7]
	v_mad_i64_i32 v[32:33], s[8:9], v54, s73, v[6:7]
	v_mad_i64_i32 v[50:51], s[8:9], v58, s73, v[6:7]
	v_or_b32_e32 v58, v59, v52
	v_mad_i64_i32 v[52:53], s[8:9], v64, s73, v[6:7]
	v_mad_i64_i32 v[54:55], s[8:9], v68, s73, v[6:7]
	global_load_dword v59, v[20:21], off offset:2048
	global_load_dword v64, v[28:29], off offset:1024
	global_load_dword v68, v[28:29], off offset:2048
	global_load_dword v69, v[20:21], off offset:1024
	global_load_dword v70, v[30:31], off offset:1024
	global_load_dword v71, v[30:31], off offset:2048
	global_load_dword v72, v[32:33], off offset:1024
	global_load_dword v73, v[32:33], off offset:2048
	global_load_dword v74, v[48:49], off offset:1024
	s_nop 0
	global_load_dword v48, v[48:49], off offset:2048
	s_nop 0
	global_load_dword v49, v[50:51], off offset:1024
	v_mad_i64_i32 v[20:21], s[8:9], v58, s73, v[6:7]
	global_load_dword v50, v[50:51], off offset:2048
	s_nop 0
	global_load_dword v51, v[52:53], off offset:1024
	s_nop 0
	global_load_dword v52, v[52:53], off offset:2048
	s_nop 0
	global_load_dword v53, v[16:17], off
	global_load_dword v58, v[20:21], off offset:1024
	global_load_dword v75, v[20:21], off offset:2048
	global_load_dword v76, v[54:55], off offset:1024
	s_nop 0
	global_load_dword v54, v[54:55], off offset:2048
	s_nop 0
	global_load_dword v77, v[22:23], off
	global_load_dword v78, v[24:25], off
	global_load_dword v79, v[26:27], off
	v_ashrrev_i32_e32 v35, 31, v34
	v_ashrrev_i32_e32 v37, 31, v36
	v_ashrrev_i32_e32 v39, 31, v38
	v_ashrrev_i32_e32 v41, 31, v40
	v_ashrrev_i32_e32 v45, 31, v44
	v_ashrrev_i32_e32 v43, 31, v42
	v_ashrrev_i32_e32 v47, 31, v46
	v_lshlrev_b64 v[34:35], 12, v[34:35]
	v_lshlrev_b64 v[36:37], 12, v[36:37]
	v_lshlrev_b64 v[38:39], 12, v[38:39]
	v_lshlrev_b64 v[40:41], 12, v[40:41]
	v_lshlrev_b64 v[44:45], 12, v[44:45]
	v_lshlrev_b64 v[42:43], 12, v[42:43]
	v_lshlrev_b64 v[46:47], 12, v[46:47]
	v_lshl_add_u64 v[16:17], v[8:9], 0, v[34:35]
	v_lshl_add_u64 v[20:21], v[8:9], 0, v[36:37]
	v_lshl_add_u64 v[22:23], v[8:9], 0, v[38:39]
	v_lshl_add_u64 v[24:25], v[8:9], 0, v[40:41]
	v_lshl_add_u64 v[28:29], v[8:9], 0, v[44:45]
	v_lshl_add_u64 v[26:27], v[8:9], 0, v[42:43]
	v_lshl_add_u64 v[30:31], v[8:9], 0, v[46:47]
	s_addk_i32 s6, 0x200
	s_cmpk_eq_i32 s6, 0x800
	v_lshl_add_u64 v[18:19], v[8:9], 0, v[18:19]
	s_waitcnt vmcnt(27)
	v_cndmask_b32_e32 v33, 0, v56, vcc
	s_waitcnt vmcnt(26)
	v_cndmask_b32_e32 v35, 0, v57, vcc
	v_lshlrev_b32_e32 v32, 16, v33
	v_lshlrev_b32_e32 v34, 16, v35
	v_and_b32_e32 v33, 0xffff0000, v33
	v_and_b32_e32 v35, 0xffff0000, v35
	v_pk_mul_f32 v[32:33], v[32:33], v[34:35]
	s_waitcnt vmcnt(25)
	v_lshlrev_b32_e32 v36, 16, v60
	v_and_b32_e32 v37, 0xffff0000, v60
	s_waitcnt vmcnt(24)
	v_lshlrev_b32_e32 v38, 16, v61
	v_and_b32_e32 v39, 0xffff0000, v61
	s_waitcnt vmcnt(23)
	v_lshlrev_b32_e32 v40, 16, v62
	v_and_b32_e32 v41, 0xffff0000, v62
	s_waitcnt vmcnt(22)
	v_lshlrev_b32_e32 v42, 16, v63
	v_and_b32_e32 v43, 0xffff0000, v63
	v_pk_mul_f32 v[34:35], v[14:15], v[32:33]
	s_waitcnt vmcnt(21)
	v_cndmask_b32_e32 v45, 0, v59, vcc
	s_waitcnt vmcnt(20)
	v_cndmask_b32_e32 v55, 0, v64, vcc
	s_waitcnt vmcnt(19)
	v_cndmask_b32_e32 v56, 0, v68, vcc
	s_waitcnt vmcnt(18)
	v_cndmask_b32_e32 v57, 0, v69, vcc
	s_waitcnt vmcnt(17)
	v_cndmask_b32_e32 v59, 0, v70, vcc
	s_waitcnt vmcnt(16)
	v_cndmask_b32_e32 v60, 0, v71, vcc
	s_waitcnt vmcnt(15)
	v_cndmask_b32_e32 v61, 0, v72, vcc
	s_waitcnt vmcnt(14)
	v_cndmask_b32_e32 v62, 0, v73, vcc
	s_waitcnt vmcnt(13)
	v_cndmask_b32_e32 v63, 0, v74, vcc
	s_waitcnt vmcnt(12)
	v_cndmask_b32_e32 v64, 0, v48, vcc
	s_waitcnt vmcnt(11)
	v_cndmask_b32_e32 v71, 0, v49, vcc
	s_waitcnt vmcnt(10)
	v_cndmask_b32_e32 v73, 0, v50, vcc
	s_waitcnt vmcnt(9)
	v_cndmask_b32_e64 v81, 0, v51, s[4:5]
	s_waitcnt vmcnt(8)
	v_cndmask_b32_e64 v83, 0, v52, s[4:5]
	v_lshlrev_b32_e32 v44, 16, v45
	v_and_b32_e32 v45, 0xffff0000, v45
	s_waitcnt vmcnt(7)
	v_lshlrev_b32_e32 v46, 16, v53
	v_and_b32_e32 v47, 0xffff0000, v53
	v_lshlrev_b32_e32 v48, 16, v55
	v_lshlrev_b32_e32 v50, 16, v56
	v_and_b32_e32 v49, 0xffff0000, v55
	v_and_b32_e32 v51, 0xffff0000, v56
	v_lshlrev_b32_e32 v52, 16, v57
	v_and_b32_e32 v53, 0xffff0000, v57
	s_waitcnt vmcnt(6)
	v_cndmask_b32_e32 v84, 0, v58, vcc
	s_waitcnt vmcnt(5)
	v_cndmask_b32_e32 v85, 0, v75, vcc
	s_waitcnt vmcnt(3)
	v_cndmask_b32_e64 v87, 0, v54, s[2:3]
	v_lshlrev_b32_e32 v54, 16, v59
	v_lshlrev_b32_e32 v56, 16, v60
	v_and_b32_e32 v55, 0xffff0000, v59
	v_and_b32_e32 v57, 0xffff0000, v60
	v_lshlrev_b32_e32 v58, 16, v61
	v_lshlrev_b32_e32 v60, 16, v62
	v_and_b32_e32 v59, 0xffff0000, v61
	v_and_b32_e32 v61, 0xffff0000, v62
	v_cndmask_b32_e64 v86, 0, v76, s[2:3]
	v_lshlrev_b32_e32 v62, 16, v63
	v_lshlrev_b32_e32 v68, 16, v64
	v_and_b32_e32 v63, 0xffff0000, v63
	v_and_b32_e32 v69, 0xffff0000, v64
	v_lshlrev_b32_e32 v70, 16, v71
	v_lshlrev_b32_e32 v72, 16, v73
	v_and_b32_e32 v71, 0xffff0000, v71
	v_and_b32_e32 v73, 0xffff0000, v73
	v_pk_mul_f32 v[44:45], v[52:53], v[44:45]
	v_pk_mul_f32 v[52:53], v[58:59], v[60:61]
	v_lshlrev_b32_e32 v58, 16, v84
	v_lshlrev_b32_e32 v60, 16, v85
	v_and_b32_e32 v59, 0xffff0000, v84
	v_and_b32_e32 v61, 0xffff0000, v85
	v_lshlrev_b32_e32 v80, 16, v81
	v_lshlrev_b32_e32 v82, 16, v83
	v_and_b32_e32 v81, 0xffff0000, v81
	v_and_b32_e32 v83, 0xffff0000, v83
	v_pk_mul_f32 v[48:49], v[48:49], v[50:51]
	v_pk_mul_f32 v[50:51], v[54:55], v[56:57]
	v_pk_mul_f32 v[54:55], v[62:63], v[68:69]
	v_pk_mul_f32 v[56:57], v[70:71], v[72:73]
	v_lshlrev_b32_e32 v62, 16, v86
	v_lshlrev_b32_e32 v68, 16, v87
	v_and_b32_e32 v63, 0xffff0000, v86
	v_and_b32_e32 v69, 0xffff0000, v87
	v_pk_mul_f32 v[58:59], v[58:59], v[60:61]
	v_pk_mul_f32 v[70:71], v[80:81], v[82:83]
	v_pk_mul_f32 v[72:73], v[14:15], v[48:49]
	v_pk_mul_f32 v[80:81], v[14:15], v[44:45]
	v_pk_mul_f32 v[60:61], v[62:63], v[68:69]
	v_pk_mul_f32 v[62:63], v[14:15], v[50:51]
	v_pk_mul_f32 v[68:69], v[14:15], v[52:53]
	v_pk_mul_f32 v[82:83], v[14:15], v[54:55]
	v_pk_mul_f32 v[84:85], v[14:15], v[56:57]
	v_pk_mul_f32 v[14:15], v[14:15], v[58:59]
	v_pk_fma_f32 v[34:35], v[12:13], v[70:71], v[34:35]
	v_pk_fma_f32 v[32:33], v[12:13], v[32:33], v[72:73]
	v_pk_fma_f32 v[70:71], v[12:13], v[48:49], v[80:81]
	v_pk_fma_f32 v[62:63], v[12:13], v[44:45], v[62:63]
	v_pk_fma_f32 v[68:69], v[12:13], v[50:51], v[68:69]
	v_pk_fma_f32 v[72:73], v[12:13], v[52:53], v[82:83]
	v_pk_fma_f32 v[80:81], v[12:13], v[54:55], v[84:85]
	v_pk_fma_f32 v[12:13], v[12:13], v[56:57], v[14:15]
	v_pk_fma_f32 v[34:35], v[10:11], v[48:49], v[34:35]
	v_pk_fma_f32 v[32:33], v[10:11], v[44:45], v[32:33]
	v_pk_fma_f32 v[44:45], v[10:11], v[50:51], v[70:71]
	v_pk_fma_f32 v[48:49], v[10:11], v[52:53], v[62:63]
	v_pk_fma_f32 v[50:51], v[10:11], v[54:55], v[68:69]
	v_pk_fma_f32 v[52:53], v[10:11], v[56:57], v[72:73]
	v_pk_fma_f32 v[54:55], v[10:11], v[58:59], v[80:81]
	v_pk_fma_f32 v[10:11], v[10:11], v[60:61], v[12:13]
	s_waitcnt vmcnt(2)
	v_lshlrev_b32_e32 v74, 16, v77
	v_and_b32_e32 v75, 0xffff0000, v77
	s_waitcnt vmcnt(1)
	v_lshlrev_b32_e32 v76, 16, v78
	v_and_b32_e32 v77, 0xffff0000, v78
	s_waitcnt vmcnt(0)
	v_lshlrev_b32_e32 v78, 16, v79
	v_and_b32_e32 v79, 0xffff0000, v79
	v_pk_mul_f32 v[14:15], v[34:35], v[46:47]
	v_pk_mul_f32 v[10:11], v[10:11], v[42:43]
	v_pk_mul_f32 v[32:33], v[32:33], v[74:75]
	v_pk_mul_f32 v[34:35], v[44:45], v[76:77]
	v_pk_mul_f32 v[44:45], v[48:49], v[78:79]
	v_pk_mul_f32 v[36:37], v[50:51], v[36:37]
	v_pk_mul_f32 v[38:39], v[52:53], v[38:39]
	v_pk_mul_f32 v[40:41], v[54:55], v[40:41]
	v_cvt_pk_bf16_f32 v12, v14, v15
	v_cvt_pk_bf16_f32 v10, v10, v11
	v_cvt_pk_bf16_f32 v13, v32, v33
	v_cvt_pk_bf16_f32 v14, v34, v35
	v_cvt_pk_bf16_f32 v15, v44, v45
	v_cvt_pk_bf16_f32 v32, v36, v37
	v_cvt_pk_bf16_f32 v33, v38, v39
	v_cvt_pk_bf16_f32 v34, v40, v41
	global_store_dword v[18:19], v12, off nt
	global_store_dword v[16:17], v13, off nt
	global_store_dword v[20:21], v14, off nt
	global_store_dword v[22:23], v15, off nt
	global_store_dword v[24:25], v32, off nt
	global_store_dword v[26:27], v33, off nt
	global_store_dword v[28:29], v34, off nt
	global_store_dword v[30:31], v10, off nt
	s_cbranch_scc0 .LBB0_1575
	v_mov_b32_e32 v123, v67
	s_load_dwordx2 s[2:3], s[34:35], 0x8
	s_load_dwordx4 s[8:11], s[34:35], 0x28
	v_ashrrev_i32_e32 v0, 3, v123
	v_add_u32_e32 v2, s97, v0
	v_ashrrev_i32_e32 v3, 31, v2
	v_and_b32_e32 v16, 7, v123
	s_waitcnt lgkmcnt(0)
	v_lshl_add_u64 v[2:3], v[2:3], 2, s[2:3]
	global_load_dword v1, v[2:3], off
	v_lshlrev_b32_e32 v2, 1, v16
	v_cvt_f32_ubyte0_e32 v2, v2
	v_mul_f32_e32 v17, 0xbd800000, v2
	v_cmp_eq_f32_e32 vcc, 0, v17
	v_readfirstlane_b32 s14, v123
	s_waitcnt vmcnt(0)
	v_cvt_f32_i32_e32 v1, v1
	v_cndmask_b32_e64 v12, v110, 1.0, vcc
	v_frexp_mant_f32_e32 v2, v12
	v_cmp_gt_f32_e64 s[2:3], s75, v2
	s_nop 1
	v_cndmask_b32_e64 v3, 1.0, 2.0, s[2:3]
	v_mul_f32_e32 v2, v2, v3
	v_add_f32_e32 v5, 1.0, v2
	v_rcp_f32_e32 v10, v5
	v_add_f32_e32 v3, -1.0, v5
	v_sub_f32_e32 v7, v2, v3
	v_add_f32_e32 v3, -1.0, v2
	v_mul_f32_e32 v11, v3, v10
	v_mul_f32_e32 v4, v5, v11
	v_fma_f32 v6, v11, v5, -v4
	v_fmac_f32_e32 v6, v11, v7
	v_add_f32_e32 v2, v4, v6
	v_sub_f32_e32 v5, v3, v2
	v_pk_add_f32 v[8:9], v[2:3], v[4:5] neg_lo:[0,1] neg_hi:[0,1]
	v_mov_b32_e32 v7, v2
	v_pk_add_f32 v[2:3], v[8:9], v[6:7] neg_lo:[0,1] neg_hi:[0,1]
	s_nop 0
	v_add_f32_e32 v2, v2, v3
	v_add_f32_e32 v2, v5, v2
	v_mul_f32_e32 v3, v10, v2
	v_add_f32_e32 v2, v11, v3
	v_sub_f32_e32 v4, v2, v11
	v_sub_f32_e32 v13, v3, v4
	v_mul_f32_e32 v3, v2, v2
	v_fma_f32 v5, v2, v2, -v3
	v_add_f32_e32 v4, v13, v13
	v_fmac_f32_e32 v5, v2, v4
	v_add_f32_e32 v4, v3, v5
	v_fmamk_f32 v6, v4, 0x3e76c4e1, v104
	v_fmaak_f32 v6, v4, v6, 0x3ecccdef
	v_sub_f32_e32 v3, v4, v3
	v_sub_f32_e32 v14, v5, v3
	v_mul_f32_e32 v3, v4, v6
	v_fma_f32 v5, v4, v6, -v3
	v_fmac_f32_e32 v5, v14, v6
	v_add_f32_e32 v6, v3, v5
	v_add_f32_e32 v7, 0x3f2aaaaa, v6
	v_sub_f32_e32 v3, v6, v3
	v_sub_f32_e32 v3, v5, v3
	v_add_f32_e32 v5, 0xbf2aaaaa, v7
	v_add_f32_e32 v3, 0x31739010, v3
	v_sub_f32_e32 v5, v6, v5
	v_pk_mul_f32 v[8:9], v[2:3], v[4:5]
	v_pk_add_f32 v[10:11], v[2:3], v[4:5]
	v_fma_f32 v6, v4, v2, -v8
	v_fmac_f32_e32 v6, v4, v13
	v_mov_b32_e32 v9, v11
	v_fmac_f32_e32 v6, v14, v2
	v_pk_add_f32 v[4:5], v[8:9], v[6:7]
	v_ldexp_f32 v14, v13, 1
	v_sub_f32_e32 v3, v4, v8
	v_sub_f32_e32 v3, v6, v3
	v_sub_f32_e32 v6, v7, v5
	v_add_f32_e32 v10, v11, v6
	v_pk_mul_f32 v[6:7], v[4:5], v[4:5] op_sel:[0,1] op_sel_hi:[1,0]
	v_cvt_f64_f32_e32 v[8:9], v12
	v_frexp_exp_i32_f64_e32 v7, v[8:9]
	v_subbrev_co_u32_e64 v7, s[2:3], 0, v7, s[2:3]
	v_cvt_f32_i32_e32 v7, v7
	v_fma_f32 v8, v4, v5, -v6
	v_fmac_f32_e32 v8, v4, v10
	v_fmac_f32_e32 v8, v3, v5
	v_mul_f32_e32 v4, 0x3f317218, v7
	v_fma_f32 v10, v7, s76, -v4
	v_fmac_f32_e32 v10, 0xb102e308, v7
	v_ldexp_f32 v11, v2, 1
	v_add_f32_e32 v5, v6, v8
	v_pk_add_f32 v[2:3], v[4:5], v[10:11]
	v_mov_b32_e32 v12, v5
	v_mov_b32_e32 v13, v3
	v_mov_b32_e32 v7, v11
	v_pk_add_f32 v[6:7], v[12:13], v[6:7] neg_lo:[0,1] neg_hi:[0,1]
	v_mov_b32_e32 v9, v5
	v_pk_add_f32 v[6:7], v[8:9], v[6:7] neg_lo:[0,1] neg_hi:[0,1]
	v_mov_b32_e32 v11, v2
	v_add_f32_e32 v5, v14, v6
	v_add_f32_e32 v5, v5, v7
	v_pk_add_f32 v[6:7], v[2:3], v[4:5] neg_lo:[0,1] neg_hi:[0,1]
	v_pk_add_f32 v[8:9], v[2:3], v[4:5]
	v_mov_b32_e32 v4, v5
	v_mov_b32_e32 v7, v9
	v_pk_add_f32 v[12:13], v[10:11], v[6:7] neg_lo:[0,1] neg_hi:[0,1]
	v_pk_add_f32 v[6:7], v[10:11], v[6:7]
	v_mov_b32_e32 v5, v2
	v_pk_add_f32 v[10:11], v[6:7], v[2:3] op_sel:[1,0] op_sel_hi:[0,1] neg_lo:[0,1] neg_hi:[0,1]
	v_pk_add_f32 v[14:15], v[8:9], v[10:11] op_sel_hi:[1,0] neg_lo:[0,1] neg_hi:[0,1]
	v_mov_b32_e32 v8, v9
	v_mov_b32_e32 v9, v7
	v_pk_mov_b32 v[10:11], v[2:3], v[10:11] op_sel:[1,0]
	v_mov_b32_e32 v14, v12
	v_pk_add_f32 v[8:9], v[8:9], v[10:11] neg_lo:[0,1] neg_hi:[0,1]
	v_mov_b32_e32 v13, v7
	v_pk_add_f32 v[2:3], v[4:5], v[8:9] neg_lo:[0,1] neg_hi:[0,1]
	s_nop 0
	v_pk_add_f32 v[4:5], v[14:15], v[2:3]
	s_nop 0
	v_pk_add_f32 v[8:9], v[4:5], v[4:5] op_sel:[0,1] op_sel_hi:[1,0]
	s_nop 0
	v_pk_add_f32 v[6:7], v[6:7], v[8:9] op_sel:[1,0] op_sel_hi:[0,1]
	v_mov_b32_e32 v5, v6
	v_pk_add_f32 v[10:11], v[4:5], v[12:13] neg_lo:[0,1] neg_hi:[0,1]
	v_mov_b32_e32 v3, v8
	v_sub_f32_e32 v4, v4, v10
	v_pk_add_f32 v[2:3], v[2:3], v[10:11] neg_lo:[0,1] neg_hi:[0,1]
	v_sub_f32_e32 v4, v12, v4
	v_add_f32_e32 v2, v2, v4
	v_add_f32_e32 v2, v2, v3
	v_add_f32_e32 v3, v6, v2
	v_sub_f32_e32 v4, v3, v6
	v_sub_f32_e32 v2, v2, v4
	v_mul_f32_e32 v4, v17, v3
	v_fma_f32 v3, v17, v3, -v4
	v_fmac_f32_e32 v3, v17, v2
	v_add_f32_e32 v2, v4, v3
	v_cmp_class_f32_e64 s[2:3], v4, s77
	v_sub_f32_e32 v5, v2, v4
	v_sub_f32_e32 v3, v3, v5
	v_cndmask_b32_e64 v2, v2, v4, s[2:3]
	v_cmp_eq_f32_e64 s[2:3], s79, v2
	s_nop 1
	v_cndmask_b32_e64 v4, 0, v111, s[2:3]
	v_sub_f32_e32 v5, v2, v4
	v_mul_f32_e32 v6, 0x3fb8aa3b, v5
	v_fma_f32 v7, v5, s80, -v6
	v_rndne_f32_e32 v8, v6
	v_fmac_f32_e32 v7, 0x32a5705f, v5
	v_sub_f32_e32 v6, v6, v8
	v_add_f32_e32 v6, v6, v7
	v_exp_f32_e32 v6, v6
	v_cvt_i32_f32_e32 v7, v8
	v_cmp_neq_f32_e64 s[2:3], |v2|, s78
	s_nop 1
	v_cndmask_b32_e64 v2, 0, v3, s[2:3]
	v_ldexp_f32 v3, v6, v7
	v_cmp_ngt_f32_e64 s[2:3], s81, v5
	v_add_f32_e32 v2, v4, v2
	s_nop 0
	v_cndmask_b32_e64 v3, 0, v3, s[2:3]
	v_cmp_nlt_f32_e64 s[2:3], s79, v5
	s_nop 1
	v_cndmask_b32_e64 v3, v112, v3, s[2:3]
	v_fma_f32 v2, v3, v2, v3
	v_cmp_class_f32_e64 s[2:3], v3, s77
	s_nop 1
	v_cndmask_b32_e64 v2, v2, v3, s[2:3]
	v_cmp_neq_f32_e64 s[2:3], v17, |v17|
	s_nop 1
	v_cndmask_b32_e64 v3, v112, 0, s[2:3]
	v_cndmask_b32_e64 v3, v3, 1.0, vcc
	v_cmp_class_f32_e64 s[2:3], v17, s77
	s_nop 1
	v_cndmask_b32_e64 v2, |v2|, v3, s[2:3]
	v_mul_f32_e32 v1, v2, v1
	s_brev_b32 s2, 18
	v_and_b32_e32 v2, 0x7fffffff, v1
	v_cmp_nlt_f32_e64 s[2:3], |v1|, s2
	s_and_saveexec_b64 s[4:5], s[2:3]
	s_xor_b64 s[12:13], exec, s[4:5]
	s_cbranch_execz .LBB0_1578
	v_lshrrev_b32_e32 v3, 23, v2
	v_add_u32_e32 v3, 0xffffff88, v3
	v_cmp_lt_u32_e32 vcc, 63, v3
	s_mov_b32 s6, 0xfe5163ab
	s_nop 0
	v_cndmask_b32_e32 v4, 0, v113, vcc
	v_add_u32_e32 v3, v4, v3
	v_cmp_lt_u32_e64 s[2:3], 31, v3
	s_nop 1
	v_cndmask_b32_e64 v4, 0, v114, s[2:3]
	v_add_u32_e32 v3, v4, v3
	v_cmp_lt_u32_e64 s[4:5], 31, v3
	s_nop 1
	v_cndmask_b32_e64 v4, 0, v114, s[4:5]
	v_add_u32_e32 v3, v4, v3
	v_and_b32_e32 v4, 0x7fffff, v2
	v_or_b32_e32 v17, 0x800000, v4
	v_mad_u64_u32 v[4:5], s[6:7], v17, s6, 0
	v_mov_b32_e32 v64, v5
	s_mov_b32 s6, 0x3c439041
	v_mad_u64_u32 v[6:7], s[6:7], v17, s6, v[64:65]
	v_mov_b32_e32 v64, v7
	s_mov_b32 s6, 0xdb629599
	v_mad_u64_u32 v[8:9], s[6:7], v17, s6, v[64:65]
	v_mov_b32_e32 v64, v9
	s_mov_b32 s6, 0xf534ddc0
	v_mad_u64_u32 v[10:11], s[6:7], v17, s6, v[64:65]
	v_mov_b32_e32 v64, v11
	s_mov_b32 s6, 0xfc2757d1
	v_mad_u64_u32 v[12:13], s[6:7], v17, s6, v[64:65]
	v_mov_b32_e32 v64, v13
	s_mov_b32 s6, 0x4e441529
	v_mad_u64_u32 v[14:15], s[6:7], v17, s6, v[64:65]
	v_mov_b32_e32 v64, v15
	s_mov_b32 s6, 0xa2f9836e
	v_mad_u64_u32 v[18:19], s[6:7], v17, s6, v[64:65]
	v_cndmask_b32_e32 v5, v14, v10, vcc
	v_cndmask_b32_e32 v7, v18, v12, vcc
	v_cndmask_b32_e32 v11, v19, v14, vcc
	v_cndmask_b32_e64 v9, v7, v5, s[2:3]
	v_cndmask_b32_e64 v7, v11, v7, s[2:3]
	v_cndmask_b32_e32 v11, v12, v8, vcc
	v_cndmask_b32_e64 v5, v5, v11, s[2:3]
	v_sub_u32_e32 v12, 32, v3
	v_cmp_eq_u32_e64 s[6:7], 0, v3
	v_cndmask_b32_e32 v3, v10, v6, vcc
	v_cndmask_b32_e64 v7, v7, v9, s[4:5]
	v_cndmask_b32_e64 v9, v9, v5, s[4:5]
	v_cndmask_b32_e64 v6, v11, v3, s[2:3]
	v_alignbit_b32 v13, v7, v9, v12
	v_cndmask_b32_e64 v5, v5, v6, s[4:5]
	v_cndmask_b32_e64 v7, v13, v7, s[6:7]
	v_alignbit_b32 v10, v9, v5, v12
	v_cndmask_b32_e32 v4, v8, v4, vcc
	v_cndmask_b32_e64 v9, v10, v9, s[6:7]
	v_bfe_u32 v13, v7, 29, 1
	v_cndmask_b32_e64 v3, v3, v4, s[2:3]
	v_alignbit_b32 v10, v7, v9, 30
	v_sub_u32_e32 v14, 0, v13
	v_cndmask_b32_e64 v3, v6, v3, s[4:5]
	v_xor_b32_e32 v10, v10, v14
	v_alignbit_b32 v4, v5, v3, v12
	v_cndmask_b32_e64 v4, v4, v5, s[6:7]
	v_ffbh_u32_e32 v6, v10
	v_alignbit_b32 v5, v9, v4, 30
	v_min_u32_e32 v6, 32, v6
	v_alignbit_b32 v3, v4, v3, 30
	v_xor_b32_e32 v5, v5, v14
	v_sub_u32_e32 v8, 31, v6
	v_xor_b32_e32 v3, v3, v14
	v_alignbit_b32 v9, v10, v5, v8
	v_alignbit_b32 v3, v5, v3, v8
	v_alignbit_b32 v4, v9, v3, 9
	v_ffbh_u32_e32 v5, v4
	v_min_u32_e32 v5, 32, v5
	v_lshrrev_b32_e32 v11, 29, v7
	v_not_b32_e32 v8, v5
	v_alignbit_b32 v3, v4, v3, v8
	v_lshlrev_b32_e32 v4, 31, v11
	v_or_b32_e32 v8, 0x33000000, v4
	v_add_lshl_u32 v5, v5, v6, 23
	v_lshrrev_b32_e32 v3, 9, v3
	v_sub_u32_e32 v5, v8, v5
	v_or_b32_e32 v4, 0.5, v4
	v_lshlrev_b32_e32 v6, 23, v6
	v_or_b32_e32 v3, v5, v3
	v_lshrrev_b32_e32 v5, 9, v9
	v_sub_u32_e32 v4, v4, v6
	v_or_b32_e32 v4, v5, v4
	v_mul_f32_e32 v5, 0x3fc90fda, v4
	s_mov_b32 s2, 0x3fc90fda
	v_fma_f32 v6, v4, s2, -v5
	v_fmac_f32_e32 v6, 0x33a22168, v4
	v_fmac_f32_e32 v6, 0x3fc90fda, v3
	v_lshrrev_b32_e32 v4, 30, v7
	v_add_f32_e32 v3, v5, v6
	v_add_u32_e32 v4, v13, v4

.LBB0_1581:
	s_or_b64 exec, exec, s[8:9]
	s_waitcnt lgkmcnt(7)
	v_cndmask_b32_e64 v28, v119, 1.0, s[6:7]
	s_waitcnt lgkmcnt(6)
	v_pk_mul_f32 v[20:21], v[28:29], v[26:27] op_sel_hi:[0,1]
	v_pk_mul_f32 v[22:23], v[28:29], v[24:25] op_sel_hi:[0,1]
	v_pk_mul_f32 v[16:17], v[28:29], v[16:17] op_sel_hi:[0,1]
	v_cvt_pk_bf16_f32 v20, v20, v21
	v_cvt_pk_bf16_f32 v21, v22, v23
	v_cvt_pk_bf16_f32 v22, v16, v17
	v_pk_mul_f32 v[16:17], v[28:29], v[18:19] op_sel_hi:[0,1]
	v_cvt_pk_bf16_f32 v23, v16, v17
	v_add_u32_e32 v18, s97, v126
	v_mov_b64_e32 v[16:17], s[38:39]
	v_mad_i64_i32 v[16:17], s[8:9], v18, s83, v[16:17]
	v_cndmask_b32_e64 v18, 0, v120, s[6:7]
	v_mov_b32_e32 v19, v65
	v_lshl_add_u64 v[16:17], v[16:17], 0, v[18:19]
	v_lshl_add_u64 v[16:17], v[68:69], 1, v[16:17]
	v_add_co_u32_e32 v125, vcc, 12, v125
	v_lshl_add_u64 v[16:17], v[16:17], 0, v[64:65]
	s_andn2_b64 vcc, exec, vcc
	v_add_u32_e32 v124, 0x300, v124
	global_store_dwordx4 v[16:17], v[20:23], off nt
	s_cbranch_vccnz .LBB0_1606

.LBB0_1584:
	s_or_b64 exec, exec, s[30:31]
	s_waitcnt vmcnt(10)
	v_lshlrev_b32_e32 v138, 16, v56
	v_and_b32_e32 v139, 0xffff0000, v56
	s_waitcnt lgkmcnt(2)
	v_pk_mul_f32 v[102:103], v[138:139], v[138:139]
	v_lshlrev_b32_e32 v56, 16, v57
	v_and_b32_e32 v57, 0xffff0000, v57
	v_pk_mul_f32 v[140:141], v[56:57], v[56:57]
	v_add_f32_e32 v97, v102, v103
	v_lshlrev_b32_e32 v142, 16, v58
	v_and_b32_e32 v143, 0xffff0000, v58
	v_add_f32_e32 v97, v140, v97
	v_and_b32_e32 v98, 0xffff0000, v59
	v_lshlrev_b32_e32 v99, 16, v59
	v_pk_mul_f32 v[58:59], v[142:143], v[142:143]
	v_add_f32_e32 v97, v141, v97
	v_add_f32_e32 v58, v58, v97
	s_waitcnt lgkmcnt(0)
	v_pk_mul_f32 v[100:101], v[98:99], v[98:99]
	v_add_f32_e32 v58, v59, v58
	v_add_f32_e32 v58, v101, v58
	v_add_f32_e32 v97, v100, v58
	ds_swizzle_b32 v102, v97 offset:swizzle(SWAP,1)
	v_cndmask_b32_e64 v96, v119, 1.0, s[28:29]
	v_pk_mul_f32 v[58:59], v[96:97], v[94:95] op_sel_hi:[0,1]
	v_cvt_pk_bf16_f32 v100, v58, v59
	v_pk_mul_f32 v[58:59], v[96:97], v[92:93] op_sel_hi:[0,1]
	s_waitcnt lgkmcnt(0)
	v_add_f32_e32 v92, v97, v102
	ds_swizzle_b32 v93, v92 offset:swizzle(SWAP,2)
	v_cvt_pk_bf16_f32 v101, v58, v59
	v_pk_mul_f32 v[58:59], v[96:97], v[60:61] op_sel_hi:[0,1]
	v_cvt_pk_bf16_f32 v102, v58, v59
	v_pk_mul_f32 v[58:59], v[96:97], v[62:63] op_sel_hi:[0,1]
	s_waitcnt lgkmcnt(0)
	v_add_f32_e32 v60, v92, v93
	ds_swizzle_b32 v61, v60 offset:swizzle(SWAP,4)
	v_cvt_pk_bf16_f32 v103, v58, v59
	v_add_u32_e32 v62, s97, v137
	v_mov_b64_e32 v[58:59], s[38:39]
	v_mad_i64_i32 v[140:141], s[30:31], v62, s83, v[58:59]
	s_waitcnt lgkmcnt(0)
	v_add_f32_e32 v58, v60, v61
	v_fmamk_f32 v58, v58, 0x3c800000, v107
	v_mul_f32_e32 v59, 0x4f800000, v58
	v_cmp_gt_f32_e32 vcc, s84, v58
	v_cndmask_b32_e64 v144, 0, v120, s[28:29]
	v_mov_b32_e32 v145, v65
	v_cndmask_b32_e32 v58, v58, v59, vcc
	v_sqrt_f32_e32 v60, v58
	v_cndmask_b32_e64 v59, v9, v13, s[26:27]
	v_add_u32_e32 v61, -1, v60
	v_fma_f32 v62, -v61, v60, v58
	v_cmp_ge_f32_e64 s[28:29], 0, v62
	v_add_u32_e32 v62, 1, v60
	s_nop 0
	v_cndmask_b32_e64 v61, v60, v61, s[28:29]
	v_fma_f32 v60, -v62, v60, v58
	v_cmp_lt_f32_e64 s[28:29], 0, v60
	s_nop 1
	v_cndmask_b32_e64 v60, v61, v62, s[28:29]
	v_mul_f32_e32 v61, 0x37800000, v60
	v_cndmask_b32_e32 v60, v60, v61, vcc
	v_cmp_class_f32_e32 vcc, v58, v108
	v_cndmask_b32_e64 v61, v11, v15, s[26:27]
	s_nop 0
	v_cndmask_b32_e32 v62, v60, v58, vcc
	v_div_scale_f32 v63, s[28:29], v62, v62, 1.0
	v_rcp_f32_e32 v92, v63
	v_cndmask_b32_e64 v58, v8, v12, s[26:27]
	v_cndmask_b32_e64 v60, v10, v14, s[26:27]
	v_fma_f32 v93, -v63, v92, 1.0
	v_fmac_f32_e32 v92, v93, v92
	v_div_scale_f32 v93, vcc, 1.0, v62, 1.0
	v_mul_f32_e32 v94, v93, v92
	v_fma_f32 v95, -v63, v94, v93
	v_fmac_f32_e32 v94, v95, v92
	v_fma_f32 v63, -v63, v94, v93
	v_div_fmas_f32 v63, v63, v92, v94
	v_div_fixup_f32 v92, v63, v62, 1.0
	v_pk_mul_f32 v[62:63], v[92:93], v[138:139] op_sel_hi:[0,1]
	v_pk_mul_f32 v[56:57], v[92:93], v[56:57] op_sel_hi:[0,1]
	v_pk_mul_f32 v[62:63], v[58:59], v[62:63]
	v_pk_mul_f32 v[60:61], v[60:61], v[56:57]
	v_pk_mul_f32 v[56:57], v[92:93], v[142:143] op_sel_hi:[0,1]
	v_cndmask_b32_e64 v59, v1, v5, s[26:27]
	v_cndmask_b32_e64 v58, v0, v4, s[26:27]
	v_pk_mul_f32 v[56:57], v[58:59], v[56:57]
	v_pk_mul_f32 v[58:59], v[92:93], v[98:99] op_sel_hi:[0,1]
	v_cndmask_b32_e64 v93, v3, v7, s[26:27]
	v_cndmask_b32_e64 v92, v2, v6, s[26:27]
	v_pk_mul_f32 v[58:59], v[92:93], v[58:59] op_sel:[0,1] op_sel_hi:[1,0]
	ds_swizzle_b32 v92, v62 offset:swizzle(SWAP,1)
	ds_swizzle_b32 v93, v63 offset:swizzle(SWAP,1)
	ds_swizzle_b32 v94, v60 offset:swizzle(SWAP,1)
	ds_swizzle_b32 v95, v61 offset:swizzle(SWAP,1)
	ds_swizzle_b32 v98, v56 offset:swizzle(SWAP,1)
	ds_swizzle_b32 v99, v57 offset:swizzle(SWAP,1)
	ds_swizzle_b32 v96, v58 offset:swizzle(SWAP,1)
	ds_swizzle_b32 v97, v59 offset:swizzle(SWAP,1)
	v_lshl_add_u64 v[138:139], v[140:141], 0, v[144:145]
	v_lshl_add_u64 v[90:91], v[90:91], 1, v[138:139]
	v_lshl_add_u64 v[90:91], v[90:91], 0, v[64:65]
	global_store_dwordx4 v[90:91], v[100:103], off nt
	s_and_saveexec_b64 s[28:29], s[2:3]
	s_cbranch_execz .LBB0_1586
	v_lshl_add_u32 v137, v136, 6, s60
	ds_read2_b32 v[90:91], v137 offset0:8 offset1:9
	ds_read2_b32 v[100:101], v137 offset0:10 offset1:11
	ds_read2_b32 v[102:103], v137 offset0:12 offset1:13
	ds_read2_b32 v[138:139], v137 offset0:14 offset1:15
	s_waitcnt lgkmcnt(3)
	v_pk_mul_f32 v[90:91], v[90:91], v[92:93]
	s_waitcnt lgkmcnt(2)
	v_pk_mul_f32 v[92:93], v[100:101], v[94:95]
	s_waitcnt lgkmcnt(1)
	v_pk_mul_f32 v[94:95], v[102:103], v[98:99]
	ds_read2_b32 v[98:99], v137 offset1:1
	ds_read2_b32 v[100:101], v137 offset0:2 offset1:3
	ds_read2_b32 v[102:103], v137 offset0:4 offset1:5
	ds_read2_b32 v[140:141], v137 offset0:6 offset1:7
	s_waitcnt lgkmcnt(4)
	v_pk_mul_f32 v[96:97], v[138:139], v[96:97]
	v_cndmask_b32_e64 v91, v91, -v91, s[4:5]
	v_cndmask_b32_e64 v90, v90, -v90, s[4:5]
	v_cndmask_b32_e64 v93, v93, -v93, s[4:5]
	v_cndmask_b32_e64 v92, v92, -v92, s[4:5]
	v_cndmask_b32_e64 v94, v94, -v94, s[4:5]
	v_cndmask_b32_e64 v95, v95, -v95, s[4:5]
	v_cndmask_b32_e64 v96, v96, -v96, s[4:5]
	v_cndmask_b32_e64 v97, v97, -v97, s[4:5]
	s_waitcnt lgkmcnt(0)
	v_pk_fma_f32 v[58:59], v[58:59], v[140:141], v[96:97]
	v_pk_fma_f32 v[56:57], v[56:57], v[102:103], v[94:95]
	v_pk_fma_f32 v[60:61], v[60:61], v[100:101], v[92:93]
	v_pk_fma_f32 v[62:63], v[62:63], v[98:99], v[90:91]
.LBB0_1586:
	s_or_b64 exec, exec, s[28:29]
	s_waitcnt vmcnt(10) lgkmcnt(3)
	v_lshlrev_b32_e32 v98, 16, v52
	s_waitcnt lgkmcnt(2)
	v_and_b32_e32 v99, 0xffff0000, v52
	s_waitcnt lgkmcnt(0)
	v_pk_mul_f32 v[96:97], v[98:99], v[98:99]
	v_lshlrev_b32_e32 v52, 16, v53
	v_and_b32_e32 v53, 0xffff0000, v53
	v_pk_mul_f32 v[100:101], v[52:53], v[52:53]
	v_add_f32_e32 v91, v96, v97
	v_lshlrev_b32_e32 v102, 16, v54
	v_and_b32_e32 v103, 0xffff0000, v54
	v_add_f32_e32 v91, v100, v91
	v_and_b32_e32 v92, 0xffff0000, v55
	v_lshlrev_b32_e32 v93, 16, v55
	v_pk_mul_f32 v[54:55], v[102:103], v[102:103]
	v_add_f32_e32 v91, v101, v91
	v_add_f32_e32 v54, v54, v91
	v_pk_mul_f32 v[94:95], v[92:93], v[92:93]
	v_add_f32_e32 v54, v55, v54
	v_add_f32_e32 v54, v95, v54
	v_add_f32_e32 v91, v94, v54
	ds_swizzle_b32 v96, v91 offset:swizzle(SWAP,1)
	v_cndmask_b32_e64 v90, v119, 1.0, s[26:27]
	v_pk_mul_f32 v[54:55], v[90:91], v[62:63] op_sel_hi:[0,1]
	v_cvt_pk_bf16_f32 v94, v54, v55
	v_pk_mul_f32 v[54:55], v[90:91], v[60:61] op_sel_hi:[0,1]
	s_waitcnt lgkmcnt(0)
	v_add_f32_e32 v60, v91, v96
	ds_swizzle_b32 v61, v60 offset:swizzle(SWAP,2)
	v_cvt_pk_bf16_f32 v95, v54, v55
	v_pk_mul_f32 v[54:55], v[90:91], v[56:57] op_sel_hi:[0,1]
	v_cvt_pk_bf16_f32 v96, v54, v55
	v_pk_mul_f32 v[54:55], v[90:91], v[58:59] op_sel_hi:[0,1]
	s_waitcnt lgkmcnt(0)
	v_add_f32_e32 v56, v60, v61
	ds_swizzle_b32 v57, v56 offset:swizzle(SWAP,4)
	v_cvt_pk_bf16_f32 v97, v54, v55
	v_add_u32_e32 v58, s97, v136
	v_mov_b64_e32 v[54:55], s[38:39]
	v_mad_i64_i32 v[100:101], s[28:29], v58, s83, v[54:55]
	s_waitcnt lgkmcnt(0)
	v_add_f32_e32 v54, v56, v57
	v_fmamk_f32 v54, v54, 0x3c800000, v107
	v_mul_f32_e32 v55, 0x4f800000, v54
	v_cmp_gt_f32_e32 vcc, s84, v54
	v_cndmask_b32_e64 v136, 0, v120, s[26:27]
	v_mov_b32_e32 v137, v65
	v_cndmask_b32_e32 v54, v54, v55, vcc
	v_sqrt_f32_e32 v56, v54
	v_cndmask_b32_e64 v55, v9, v13, s[24:25]
	v_add_u32_e32 v57, -1, v56
	v_fma_f32 v58, -v57, v56, v54
	v_cmp_ge_f32_e64 s[26:27], 0, v58
	v_add_u32_e32 v58, 1, v56
	s_nop 0
	v_cndmask_b32_e64 v57, v56, v57, s[26:27]
	v_fma_f32 v56, -v58, v56, v54
	v_cmp_lt_f32_e64 s[26:27], 0, v56
	s_nop 1
	v_cndmask_b32_e64 v56, v57, v58, s[26:27]
	v_mul_f32_e32 v57, 0x37800000, v56
	v_cndmask_b32_e32 v56, v56, v57, vcc
	v_cmp_class_f32_e32 vcc, v54, v108
	v_cndmask_b32_e64 v57, v11, v15, s[24:25]
	s_nop 0
	v_cndmask_b32_e32 v58, v56, v54, vcc
	v_div_scale_f32 v59, s[26:27], v58, v58, 1.0
	v_rcp_f32_e32 v60, v59
	v_cndmask_b32_e64 v54, v8, v12, s[24:25]
	v_cndmask_b32_e64 v56, v10, v14, s[24:25]
	v_fma_f32 v61, -v59, v60, 1.0
	v_fmac_f32_e32 v60, v61, v60
	v_div_scale_f32 v61, vcc, 1.0, v58, 1.0
	v_mul_f32_e32 v62, v61, v60
	v_fma_f32 v63, -v59, v62, v61
	v_fmac_f32_e32 v62, v63, v60
	v_fma_f32 v59, -v59, v62, v61
	v_div_fmas_f32 v59, v59, v60, v62
	v_div_fixup_f32 v60, v59, v58, 1.0
	v_pk_mul_f32 v[58:59], v[60:61], v[98:99] op_sel_hi:[0,1]
	v_pk_mul_f32 v[52:53], v[60:61], v[52:53] op_sel_hi:[0,1]
	v_pk_mul_f32 v[58:59], v[54:55], v[58:59]
	v_pk_mul_f32 v[56:57], v[56:57], v[52:53]
	v_pk_mul_f32 v[52:53], v[60:61], v[102:103] op_sel_hi:[0,1]
	v_cndmask_b32_e64 v55, v1, v5, s[24:25]
	v_cndmask_b32_e64 v54, v0, v4, s[24:25]
	v_pk_mul_f32 v[52:53], v[54:55], v[52:53]
	v_pk_mul_f32 v[54:55], v[60:61], v[92:93] op_sel_hi:[0,1]
	v_cndmask_b32_e64 v61, v3, v7, s[24:25]
	v_cndmask_b32_e64 v60, v2, v6, s[24:25]
	v_pk_mul_f32 v[54:55], v[60:61], v[54:55] op_sel:[0,1] op_sel_hi:[1,0]
	ds_swizzle_b32 v60, v58 offset:swizzle(SWAP,1)
	ds_swizzle_b32 v61, v59 offset:swizzle(SWAP,1)
	ds_swizzle_b32 v62, v56 offset:swizzle(SWAP,1)
	ds_swizzle_b32 v63, v57 offset:swizzle(SWAP,1)
	ds_swizzle_b32 v92, v52 offset:swizzle(SWAP,1)
	ds_swizzle_b32 v93, v53 offset:swizzle(SWAP,1)
	ds_swizzle_b32 v90, v54 offset:swizzle(SWAP,1)
	ds_swizzle_b32 v91, v55 offset:swizzle(SWAP,1)
	v_lshl_add_u64 v[98:99], v[100:101], 0, v[136:137]
	v_lshl_add_u64 v[88:89], v[88:89], 1, v[98:99]
	v_lshl_add_u64 v[88:89], v[88:89], 0, v[64:65]
	global_store_dwordx4 v[88:89], v[94:97], off nt
	s_and_saveexec_b64 s[26:27], s[2:3]
	s_cbranch_execz .LBB0_1588
	v_lshl_add_u32 v100, v135, 6, s60
	ds_read2_b32 v[88:89], v100 offset0:8 offset1:9
	ds_read2_b32 v[94:95], v100 offset0:10 offset1:11
	ds_read2_b32 v[96:97], v100 offset0:12 offset1:13
	ds_read2_b32 v[98:99], v100 offset0:14 offset1:15
	s_waitcnt lgkmcnt(3)
	v_pk_mul_f32 v[60:61], v[88:89], v[60:61]
	s_waitcnt lgkmcnt(2)
	v_pk_mul_f32 v[62:63], v[94:95], v[62:63]
	s_waitcnt lgkmcnt(1)
	v_pk_mul_f32 v[88:89], v[96:97], v[92:93]
	ds_read2_b32 v[92:93], v100 offset1:1
	ds_read2_b32 v[94:95], v100 offset0:2 offset1:3
	ds_read2_b32 v[96:97], v100 offset0:4 offset1:5
	ds_read2_b32 v[100:101], v100 offset0:6 offset1:7
	s_waitcnt lgkmcnt(4)
	v_pk_mul_f32 v[90:91], v[98:99], v[90:91]
	v_cndmask_b32_e64 v61, v61, -v61, s[4:5]
	v_cndmask_b32_e64 v60, v60, -v60, s[4:5]
	v_cndmask_b32_e64 v63, v63, -v63, s[4:5]
	v_cndmask_b32_e64 v62, v62, -v62, s[4:5]
	v_cndmask_b32_e64 v88, v88, -v88, s[4:5]
	v_cndmask_b32_e64 v89, v89, -v89, s[4:5]
	v_cndmask_b32_e64 v90, v90, -v90, s[4:5]
	v_cndmask_b32_e64 v91, v91, -v91, s[4:5]
	s_waitcnt lgkmcnt(0)
	v_pk_fma_f32 v[54:55], v[54:55], v[100:101], v[90:91]
	v_pk_fma_f32 v[52:53], v[52:53], v[96:97], v[88:89]
	v_pk_fma_f32 v[56:57], v[56:57], v[94:95], v[62:63]
	v_pk_fma_f32 v[58:59], v[58:59], v[92:93], v[60:61]
.LBB0_1588:
	s_or_b64 exec, exec, s[26:27]
	s_waitcnt vmcnt(10) lgkmcnt(3)
	v_lshlrev_b32_e32 v92, 16, v48
	s_waitcnt lgkmcnt(2)
	v_and_b32_e32 v93, 0xffff0000, v48
	s_waitcnt lgkmcnt(0)
	v_pk_mul_f32 v[90:91], v[92:93], v[92:93]
	v_lshlrev_b32_e32 v48, 16, v49
	v_and_b32_e32 v49, 0xffff0000, v49
	v_pk_mul_f32 v[94:95], v[48:49], v[48:49]
	v_add_f32_e32 v61, v90, v91
	v_lshlrev_b32_e32 v96, 16, v50
	v_and_b32_e32 v97, 0xffff0000, v50
	v_add_f32_e32 v61, v94, v61
	v_and_b32_e32 v62, 0xffff0000, v51
	v_lshlrev_b32_e32 v63, 16, v51
	v_pk_mul_f32 v[50:51], v[96:97], v[96:97]
	v_add_f32_e32 v61, v95, v61
	v_add_f32_e32 v50, v50, v61
	v_pk_mul_f32 v[88:89], v[62:63], v[62:63]
	v_add_f32_e32 v50, v51, v50
	v_add_f32_e32 v50, v89, v50
	v_add_f32_e32 v61, v88, v50
	ds_swizzle_b32 v90, v61 offset:swizzle(SWAP,1)
	v_cndmask_b32_e64 v60, v119, 1.0, s[24:25]
	v_pk_mul_f32 v[50:51], v[60:61], v[58:59] op_sel_hi:[0,1]
	v_cvt_pk_bf16_f32 v88, v50, v51
	v_pk_mul_f32 v[50:51], v[60:61], v[56:57] op_sel_hi:[0,1]
	s_waitcnt lgkmcnt(0)
	v_add_f32_e32 v56, v61, v90
	ds_swizzle_b32 v57, v56 offset:swizzle(SWAP,2)
	v_cvt_pk_bf16_f32 v89, v50, v51
	v_pk_mul_f32 v[50:51], v[60:61], v[52:53] op_sel_hi:[0,1]
	v_cvt_pk_bf16_f32 v90, v50, v51
	v_pk_mul_f32 v[50:51], v[60:61], v[54:55] op_sel_hi:[0,1]
	s_waitcnt lgkmcnt(0)
	v_add_f32_e32 v52, v56, v57
	ds_swizzle_b32 v53, v52 offset:swizzle(SWAP,4)
	v_cvt_pk_bf16_f32 v91, v50, v51
	v_add_u32_e32 v54, s97, v135
	v_mov_b64_e32 v[50:51], s[38:39]
	v_mad_i64_i32 v[94:95], s[26:27], v54, s83, v[50:51]
	s_waitcnt lgkmcnt(0)
	v_add_f32_e32 v50, v52, v53
	v_fmamk_f32 v50, v50, 0x3c800000, v107
	v_mul_f32_e32 v51, 0x4f800000, v50
	v_cmp_gt_f32_e32 vcc, s84, v50
	v_cndmask_b32_e64 v98, 0, v120, s[24:25]
	v_mov_b32_e32 v99, v65
	v_cndmask_b32_e32 v50, v50, v51, vcc
	v_sqrt_f32_e32 v52, v50
	v_cndmask_b32_e64 v51, v9, v13, s[22:23]
	v_add_u32_e32 v53, -1, v52
	v_fma_f32 v54, -v53, v52, v50
	v_cmp_ge_f32_e64 s[24:25], 0, v54
	v_add_u32_e32 v54, 1, v52
	s_nop 0
	v_cndmask_b32_e64 v53, v52, v53, s[24:25]
	v_fma_f32 v52, -v54, v52, v50
	v_cmp_lt_f32_e64 s[24:25], 0, v52
	s_nop 1
	v_cndmask_b32_e64 v52, v53, v54, s[24:25]
	v_mul_f32_e32 v53, 0x37800000, v52
	v_cndmask_b32_e32 v52, v52, v53, vcc
	v_cmp_class_f32_e32 vcc, v50, v108
	v_cndmask_b32_e64 v53, v11, v15, s[22:23]
	s_nop 0
	v_cndmask_b32_e32 v54, v52, v50, vcc
	v_div_scale_f32 v55, s[24:25], v54, v54, 1.0
	v_rcp_f32_e32 v56, v55
	v_cndmask_b32_e64 v50, v8, v12, s[22:23]
	v_cndmask_b32_e64 v52, v10, v14, s[22:23]
	v_fma_f32 v57, -v55, v56, 1.0
	v_fmac_f32_e32 v56, v57, v56
	v_div_scale_f32 v57, vcc, 1.0, v54, 1.0
	v_mul_f32_e32 v58, v57, v56
	v_fma_f32 v59, -v55, v58, v57
	v_fmac_f32_e32 v58, v59, v56
	v_fma_f32 v55, -v55, v58, v57
	v_div_fmas_f32 v55, v55, v56, v58
	v_div_fixup_f32 v56, v55, v54, 1.0
	v_pk_mul_f32 v[54:55], v[56:57], v[92:93] op_sel_hi:[0,1]
	v_pk_mul_f32 v[48:49], v[56:57], v[48:49] op_sel_hi:[0,1]
	v_pk_mul_f32 v[54:55], v[50:51], v[54:55]
	v_pk_mul_f32 v[52:53], v[52:53], v[48:49]
	v_pk_mul_f32 v[48:49], v[56:57], v[96:97] op_sel_hi:[0,1]
	v_cndmask_b32_e64 v51, v1, v5, s[22:23]
	v_cndmask_b32_e64 v50, v0, v4, s[22:23]
	v_pk_mul_f32 v[48:49], v[50:51], v[48:49]
	v_pk_mul_f32 v[50:51], v[56:57], v[62:63] op_sel_hi:[0,1]
	v_cndmask_b32_e64 v57, v3, v7, s[22:23]
	v_cndmask_b32_e64 v56, v2, v6, s[22:23]
	v_pk_mul_f32 v[50:51], v[56:57], v[50:51] op_sel:[0,1] op_sel_hi:[1,0]
	ds_swizzle_b32 v56, v54 offset:swizzle(SWAP,1)
	ds_swizzle_b32 v57, v55 offset:swizzle(SWAP,1)
	ds_swizzle_b32 v58, v52 offset:swizzle(SWAP,1)
	ds_swizzle_b32 v59, v53 offset:swizzle(SWAP,1)
	ds_swizzle_b32 v62, v48 offset:swizzle(SWAP,1)
	ds_swizzle_b32 v63, v49 offset:swizzle(SWAP,1)
	ds_swizzle_b32 v60, v50 offset:swizzle(SWAP,1)
	ds_swizzle_b32 v61, v51 offset:swizzle(SWAP,1)
	v_lshl_add_u64 v[92:93], v[94:95], 0, v[98:99]
	v_lshl_add_u64 v[86:87], v[86:87], 1, v[92:93]
	v_lshl_add_u64 v[86:87], v[86:87], 0, v[64:65]
	global_store_dwordx4 v[86:87], v[88:91], off nt
	s_and_saveexec_b64 s[24:25], s[2:3]
	s_cbranch_execz .LBB0_1590
	v_lshl_add_u32 v94, v134, 6, s60
	ds_read2_b32 v[86:87], v94 offset0:8 offset1:9
	ds_read2_b32 v[88:89], v94 offset0:10 offset1:11
	ds_read2_b32 v[90:91], v94 offset0:12 offset1:13
	ds_read2_b32 v[92:93], v94 offset0:14 offset1:15
	s_waitcnt lgkmcnt(3)
	v_pk_mul_f32 v[56:57], v[86:87], v[56:57]
	s_waitcnt lgkmcnt(2)
	v_pk_mul_f32 v[58:59], v[88:89], v[58:59]
	s_waitcnt lgkmcnt(1)
	v_pk_mul_f32 v[62:63], v[90:91], v[62:63]
	ds_read2_b32 v[86:87], v94 offset1:1
	ds_read2_b32 v[88:89], v94 offset0:2 offset1:3
	ds_read2_b32 v[90:91], v94 offset0:4 offset1:5
	ds_read2_b32 v[94:95], v94 offset0:6 offset1:7
	s_waitcnt lgkmcnt(4)
	v_pk_mul_f32 v[60:61], v[92:93], v[60:61]
	v_cndmask_b32_e64 v57, v57, -v57, s[4:5]
	v_cndmask_b32_e64 v56, v56, -v56, s[4:5]
	v_cndmask_b32_e64 v59, v59, -v59, s[4:5]
	v_cndmask_b32_e64 v58, v58, -v58, s[4:5]
	v_cndmask_b32_e64 v62, v62, -v62, s[4:5]
	v_cndmask_b32_e64 v63, v63, -v63, s[4:5]
	v_cndmask_b32_e64 v60, v60, -v60, s[4:5]
	v_cndmask_b32_e64 v61, v61, -v61, s[4:5]
	s_waitcnt lgkmcnt(0)
	v_pk_fma_f32 v[50:51], v[50:51], v[94:95], v[60:61]
	v_pk_fma_f32 v[48:49], v[48:49], v[90:91], v[62:63]
	v_pk_fma_f32 v[52:53], v[52:53], v[88:89], v[58:59]
	v_pk_fma_f32 v[54:55], v[54:55], v[86:87], v[56:57]
.LBB0_1590:
	s_or_b64 exec, exec, s[24:25]
	s_waitcnt vmcnt(10)
	v_lshlrev_b32_e32 v86, 16, v44
	v_and_b32_e32 v87, 0xffff0000, v44
	s_waitcnt lgkmcnt(2)
	v_pk_mul_f32 v[62:63], v[86:87], v[86:87]
	v_lshlrev_b32_e32 v44, 16, v45
	v_and_b32_e32 v45, 0xffff0000, v45
	v_pk_mul_f32 v[88:89], v[44:45], v[44:45]
	v_add_f32_e32 v57, v62, v63
	v_lshlrev_b32_e32 v90, 16, v46
	v_and_b32_e32 v91, 0xffff0000, v46
	v_add_f32_e32 v57, v88, v57
	v_and_b32_e32 v58, 0xffff0000, v47
	v_lshlrev_b32_e32 v59, 16, v47
	v_pk_mul_f32 v[46:47], v[90:91], v[90:91]
	v_add_f32_e32 v57, v89, v57
	v_add_f32_e32 v46, v46, v57
	s_waitcnt lgkmcnt(0)
	v_pk_mul_f32 v[60:61], v[58:59], v[58:59]
	v_add_f32_e32 v46, v47, v46
	v_add_f32_e32 v46, v61, v46
	v_add_f32_e32 v57, v60, v46
	ds_swizzle_b32 v62, v57 offset:swizzle(SWAP,1)
	v_cndmask_b32_e64 v56, v119, 1.0, s[22:23]
	v_pk_mul_f32 v[46:47], v[56:57], v[54:55] op_sel_hi:[0,1]
	v_cvt_pk_bf16_f32 v60, v46, v47
	v_pk_mul_f32 v[46:47], v[56:57], v[52:53] op_sel_hi:[0,1]
	s_waitcnt lgkmcnt(0)
	v_add_f32_e32 v52, v57, v62
	ds_swizzle_b32 v53, v52 offset:swizzle(SWAP,2)
	v_cvt_pk_bf16_f32 v61, v46, v47
	v_pk_mul_f32 v[46:47], v[56:57], v[48:49] op_sel_hi:[0,1]
	v_cvt_pk_bf16_f32 v62, v46, v47
	v_pk_mul_f32 v[46:47], v[56:57], v[50:51] op_sel_hi:[0,1]
	s_waitcnt lgkmcnt(0)
	v_add_f32_e32 v48, v52, v53
	ds_swizzle_b32 v49, v48 offset:swizzle(SWAP,4)
	v_cvt_pk_bf16_f32 v63, v46, v47
	v_add_u32_e32 v50, s97, v134
	v_mov_b64_e32 v[46:47], s[38:39]
	v_mad_i64_i32 v[88:89], s[24:25], v50, s83, v[46:47]
	s_waitcnt lgkmcnt(0)
	v_add_f32_e32 v46, v48, v49
	v_fmamk_f32 v46, v46, 0x3c800000, v107
	v_mul_f32_e32 v47, 0x4f800000, v46
	v_cmp_gt_f32_e32 vcc, s84, v46
	v_cndmask_b32_e64 v92, 0, v120, s[22:23]
	v_mov_b32_e32 v93, v65
	v_cndmask_b32_e32 v46, v46, v47, vcc
	v_sqrt_f32_e32 v48, v46
	v_cndmask_b32_e64 v47, v9, v13, s[20:21]
	v_add_u32_e32 v49, -1, v48
	v_fma_f32 v50, -v49, v48, v46
	v_cmp_ge_f32_e64 s[22:23], 0, v50
	v_add_u32_e32 v50, 1, v48
	s_nop 0
	v_cndmask_b32_e64 v49, v48, v49, s[22:23]
	v_fma_f32 v48, -v50, v48, v46
	v_cmp_lt_f32_e64 s[22:23], 0, v48
	s_nop 1
	v_cndmask_b32_e64 v48, v49, v50, s[22:23]
	v_mul_f32_e32 v49, 0x37800000, v48
	v_cndmask_b32_e32 v48, v48, v49, vcc
	v_cmp_class_f32_e32 vcc, v46, v108
	v_cndmask_b32_e64 v49, v11, v15, s[20:21]
	s_nop 0
	v_cndmask_b32_e32 v50, v48, v46, vcc
	v_div_scale_f32 v51, s[22:23], v50, v50, 1.0
	v_rcp_f32_e32 v52, v51
	v_cndmask_b32_e64 v46, v8, v12, s[20:21]
	v_cndmask_b32_e64 v48, v10, v14, s[20:21]
	v_fma_f32 v53, -v51, v52, 1.0
	v_fmac_f32_e32 v52, v53, v52
	v_div_scale_f32 v53, vcc, 1.0, v50, 1.0
	v_mul_f32_e32 v54, v53, v52
	v_fma_f32 v55, -v51, v54, v53
	v_fmac_f32_e32 v54, v55, v52
	v_fma_f32 v51, -v51, v54, v53
	v_div_fmas_f32 v51, v51, v52, v54
	v_div_fixup_f32 v52, v51, v50, 1.0
	v_pk_mul_f32 v[50:51], v[52:53], v[86:87] op_sel_hi:[0,1]
	v_pk_mul_f32 v[44:45], v[52:53], v[44:45] op_sel_hi:[0,1]
	v_pk_mul_f32 v[50:51], v[46:47], v[50:51]
	v_pk_mul_f32 v[48:49], v[48:49], v[44:45]
	v_pk_mul_f32 v[44:45], v[52:53], v[90:91] op_sel_hi:[0,1]
	v_cndmask_b32_e64 v47, v1, v5, s[20:21]
	v_cndmask_b32_e64 v46, v0, v4, s[20:21]
	v_pk_mul_f32 v[44:45], v[46:47], v[44:45]
	v_pk_mul_f32 v[46:47], v[52:53], v[58:59] op_sel_hi:[0,1]
	v_cndmask_b32_e64 v53, v3, v7, s[20:21]
	v_cndmask_b32_e64 v52, v2, v6, s[20:21]
	v_pk_mul_f32 v[46:47], v[52:53], v[46:47] op_sel:[0,1] op_sel_hi:[1,0]
	ds_swizzle_b32 v52, v50 offset:swizzle(SWAP,1)
	ds_swizzle_b32 v53, v51 offset:swizzle(SWAP,1)
	ds_swizzle_b32 v54, v48 offset:swizzle(SWAP,1)
	ds_swizzle_b32 v55, v49 offset:swizzle(SWAP,1)
	ds_swizzle_b32 v58, v44 offset:swizzle(SWAP,1)
	ds_swizzle_b32 v59, v45 offset:swizzle(SWAP,1)
	ds_swizzle_b32 v56, v46 offset:swizzle(SWAP,1)
	ds_swizzle_b32 v57, v47 offset:swizzle(SWAP,1)
	v_lshl_add_u64 v[86:87], v[88:89], 0, v[92:93]
	v_lshl_add_u64 v[84:85], v[84:85], 1, v[86:87]
	v_lshl_add_u64 v[84:85], v[84:85], 0, v[64:65]
	global_store_dwordx4 v[84:85], v[60:63], off nt
	s_and_saveexec_b64 s[22:23], s[2:3]
	s_cbranch_execz .LBB0_1592
	v_lshl_add_u32 v88, v133, 6, s60
	ds_read2_b32 v[60:61], v88 offset0:8 offset1:9
	ds_read2_b32 v[62:63], v88 offset0:10 offset1:11
	ds_read2_b32 v[84:85], v88 offset0:12 offset1:13
	ds_read2_b32 v[86:87], v88 offset0:14 offset1:15
	s_waitcnt lgkmcnt(3)
	v_pk_mul_f32 v[52:53], v[60:61], v[52:53]
	s_waitcnt lgkmcnt(2)
	v_pk_mul_f32 v[54:55], v[62:63], v[54:55]
	s_waitcnt lgkmcnt(1)
	v_pk_mul_f32 v[58:59], v[84:85], v[58:59]
	ds_read2_b32 v[60:61], v88 offset1:1
	ds_read2_b32 v[62:63], v88 offset0:2 offset1:3
	ds_read2_b32 v[84:85], v88 offset0:4 offset1:5
	ds_read2_b32 v[88:89], v88 offset0:6 offset1:7
	s_waitcnt lgkmcnt(4)
	v_pk_mul_f32 v[56:57], v[86:87], v[56:57]
	v_cndmask_b32_e64 v53, v53, -v53, s[4:5]
	v_cndmask_b32_e64 v52, v52, -v52, s[4:5]
	v_cndmask_b32_e64 v55, v55, -v55, s[4:5]
	v_cndmask_b32_e64 v54, v54, -v54, s[4:5]
	v_cndmask_b32_e64 v58, v58, -v58, s[4:5]
	v_cndmask_b32_e64 v59, v59, -v59, s[4:5]
	v_cndmask_b32_e64 v56, v56, -v56, s[4:5]
	v_cndmask_b32_e64 v57, v57, -v57, s[4:5]
	s_waitcnt lgkmcnt(0)
	v_pk_fma_f32 v[46:47], v[46:47], v[88:89], v[56:57]
	v_pk_fma_f32 v[44:45], v[44:45], v[84:85], v[58:59]
	v_pk_fma_f32 v[48:49], v[48:49], v[62:63], v[54:55]
	v_pk_fma_f32 v[50:51], v[50:51], v[60:61], v[52:53]
.LBB0_1592:
	s_or_b64 exec, exec, s[22:23]
	s_waitcnt vmcnt(10)
	v_lshlrev_b32_e32 v60, 16, v40
	v_and_b32_e32 v61, 0xffff0000, v40
	s_waitcnt lgkmcnt(2)
	v_pk_mul_f32 v[58:59], v[60:61], v[60:61]
	v_lshlrev_b32_e32 v40, 16, v41
	v_and_b32_e32 v41, 0xffff0000, v41
	v_pk_mul_f32 v[62:63], v[40:41], v[40:41]
	v_add_f32_e32 v53, v58, v59
	v_lshlrev_b32_e32 v84, 16, v42
	v_and_b32_e32 v85, 0xffff0000, v42
	v_add_f32_e32 v53, v62, v53
	v_and_b32_e32 v54, 0xffff0000, v43
	v_lshlrev_b32_e32 v55, 16, v43
	v_pk_mul_f32 v[42:43], v[84:85], v[84:85]
	v_add_f32_e32 v53, v63, v53
	v_add_f32_e32 v42, v42, v53
	s_waitcnt lgkmcnt(0)
	v_pk_mul_f32 v[56:57], v[54:55], v[54:55]
	v_add_f32_e32 v42, v43, v42
	v_add_f32_e32 v42, v57, v42
	v_add_f32_e32 v53, v56, v42
	ds_swizzle_b32 v58, v53 offset:swizzle(SWAP,1)
	v_cndmask_b32_e64 v52, v119, 1.0, s[20:21]
	v_pk_mul_f32 v[42:43], v[52:53], v[50:51] op_sel_hi:[0,1]
	v_cvt_pk_bf16_f32 v56, v42, v43
	v_pk_mul_f32 v[42:43], v[52:53], v[48:49] op_sel_hi:[0,1]
	s_waitcnt lgkmcnt(0)
	v_add_f32_e32 v48, v53, v58
	ds_swizzle_b32 v49, v48 offset:swizzle(SWAP,2)
	v_cvt_pk_bf16_f32 v57, v42, v43
	v_pk_mul_f32 v[42:43], v[52:53], v[44:45] op_sel_hi:[0,1]
	v_cvt_pk_bf16_f32 v58, v42, v43
	v_pk_mul_f32 v[42:43], v[52:53], v[46:47] op_sel_hi:[0,1]
	s_waitcnt lgkmcnt(0)
	v_add_f32_e32 v44, v48, v49
	ds_swizzle_b32 v45, v44 offset:swizzle(SWAP,4)
	v_cvt_pk_bf16_f32 v59, v42, v43
	v_add_u32_e32 v46, s97, v133
	v_mov_b64_e32 v[42:43], s[38:39]
	v_mad_i64_i32 v[62:63], s[22:23], v46, s83, v[42:43]
	s_waitcnt lgkmcnt(0)
	v_add_f32_e32 v42, v44, v45
	v_fmamk_f32 v42, v42, 0x3c800000, v107
	v_mul_f32_e32 v43, 0x4f800000, v42
	v_cmp_gt_f32_e32 vcc, s84, v42
	v_cndmask_b32_e64 v86, 0, v120, s[20:21]
	v_mov_b32_e32 v87, v65
	v_cndmask_b32_e32 v42, v42, v43, vcc
	v_sqrt_f32_e32 v44, v42
	v_cndmask_b32_e64 v43, v9, v13, s[18:19]
	v_add_u32_e32 v45, -1, v44
	v_fma_f32 v46, -v45, v44, v42
	v_cmp_ge_f32_e64 s[20:21], 0, v46
	v_add_u32_e32 v46, 1, v44
	s_nop 0
	v_cndmask_b32_e64 v45, v44, v45, s[20:21]
	v_fma_f32 v44, -v46, v44, v42
	v_cmp_lt_f32_e64 s[20:21], 0, v44
	s_nop 1
	v_cndmask_b32_e64 v44, v45, v46, s[20:21]
	v_mul_f32_e32 v45, 0x37800000, v44
	v_cndmask_b32_e32 v44, v44, v45, vcc
	v_cmp_class_f32_e32 vcc, v42, v108
	v_cndmask_b32_e64 v45, v11, v15, s[18:19]
	s_nop 0
	v_cndmask_b32_e32 v46, v44, v42, vcc
	v_div_scale_f32 v47, s[20:21], v46, v46, 1.0
	v_rcp_f32_e32 v48, v47
	v_cndmask_b32_e64 v42, v8, v12, s[18:19]
	v_cndmask_b32_e64 v44, v10, v14, s[18:19]
	v_fma_f32 v49, -v47, v48, 1.0
	v_fmac_f32_e32 v48, v49, v48
	v_div_scale_f32 v49, vcc, 1.0, v46, 1.0
	v_mul_f32_e32 v50, v49, v48
	v_fma_f32 v51, -v47, v50, v49
	v_fmac_f32_e32 v50, v51, v48
	v_fma_f32 v47, -v47, v50, v49
	v_div_fmas_f32 v47, v47, v48, v50
	v_div_fixup_f32 v48, v47, v46, 1.0
	v_pk_mul_f32 v[46:47], v[48:49], v[60:61] op_sel_hi:[0,1]
	v_pk_mul_f32 v[40:41], v[48:49], v[40:41] op_sel_hi:[0,1]
	v_pk_mul_f32 v[46:47], v[42:43], v[46:47]
	v_pk_mul_f32 v[44:45], v[44:45], v[40:41]
	v_pk_mul_f32 v[40:41], v[48:49], v[84:85] op_sel_hi:[0,1]
	v_cndmask_b32_e64 v43, v1, v5, s[18:19]
	v_cndmask_b32_e64 v42, v0, v4, s[18:19]
	v_pk_mul_f32 v[40:41], v[42:43], v[40:41]
	v_pk_mul_f32 v[42:43], v[48:49], v[54:55] op_sel_hi:[0,1]
	v_cndmask_b32_e64 v49, v3, v7, s[18:19]
	v_cndmask_b32_e64 v48, v2, v6, s[18:19]
	v_pk_mul_f32 v[42:43], v[48:49], v[42:43] op_sel:[0,1] op_sel_hi:[1,0]
	ds_swizzle_b32 v48, v46 offset:swizzle(SWAP,1)
	ds_swizzle_b32 v49, v47 offset:swizzle(SWAP,1)
	ds_swizzle_b32 v50, v44 offset:swizzle(SWAP,1)
	ds_swizzle_b32 v51, v45 offset:swizzle(SWAP,1)
	ds_swizzle_b32 v54, v40 offset:swizzle(SWAP,1)
	ds_swizzle_b32 v55, v41 offset:swizzle(SWAP,1)
	ds_swizzle_b32 v52, v42 offset:swizzle(SWAP,1)
	ds_swizzle_b32 v53, v43 offset:swizzle(SWAP,1)
	v_lshl_add_u64 v[60:61], v[62:63], 0, v[86:87]
	v_lshl_add_u64 v[60:61], v[82:83], 1, v[60:61]
	v_lshl_add_u64 v[60:61], v[60:61], 0, v[64:65]
	global_store_dwordx4 v[60:61], v[56:59], off nt
	s_and_saveexec_b64 s[20:21], s[2:3]
	s_cbranch_execz .LBB0_1594
	v_lshl_add_u32 v82, v132, 6, s60
	ds_read2_b32 v[56:57], v82 offset0:8 offset1:9
	ds_read2_b32 v[58:59], v82 offset0:10 offset1:11
	ds_read2_b32 v[60:61], v82 offset0:12 offset1:13
	ds_read2_b32 v[62:63], v82 offset0:14 offset1:15
	s_waitcnt lgkmcnt(3)
	v_pk_mul_f32 v[48:49], v[56:57], v[48:49]
	s_waitcnt lgkmcnt(2)
	v_pk_mul_f32 v[50:51], v[58:59], v[50:51]
	s_waitcnt lgkmcnt(1)
	v_pk_mul_f32 v[54:55], v[60:61], v[54:55]
	ds_read2_b32 v[56:57], v82 offset1:1
	ds_read2_b32 v[58:59], v82 offset0:2 offset1:3
	ds_read2_b32 v[60:61], v82 offset0:4 offset1:5
	ds_read2_b32 v[82:83], v82 offset0:6 offset1:7
	s_waitcnt lgkmcnt(4)
	v_pk_mul_f32 v[52:53], v[62:63], v[52:53]
	v_cndmask_b32_e64 v49, v49, -v49, s[4:5]
	v_cndmask_b32_e64 v48, v48, -v48, s[4:5]
	v_cndmask_b32_e64 v51, v51, -v51, s[4:5]
	v_cndmask_b32_e64 v50, v50, -v50, s[4:5]
	v_cndmask_b32_e64 v54, v54, -v54, s[4:5]
	v_cndmask_b32_e64 v55, v55, -v55, s[4:5]
	v_cndmask_b32_e64 v52, v52, -v52, s[4:5]
	v_cndmask_b32_e64 v53, v53, -v53, s[4:5]
	s_waitcnt lgkmcnt(0)
	v_pk_fma_f32 v[42:43], v[42:43], v[82:83], v[52:53]
	v_pk_fma_f32 v[40:41], v[40:41], v[60:61], v[54:55]
	v_pk_fma_f32 v[44:45], v[44:45], v[58:59], v[50:51]
	v_pk_fma_f32 v[46:47], v[46:47], v[56:57], v[48:49]
.LBB0_1594:
	s_or_b64 exec, exec, s[20:21]
	s_waitcnt vmcnt(10)
	v_lshlrev_b32_e32 v56, 16, v36
	v_and_b32_e32 v57, 0xffff0000, v36
	s_waitcnt lgkmcnt(2)
	v_pk_mul_f32 v[54:55], v[56:57], v[56:57]
	v_lshlrev_b32_e32 v36, 16, v37
	v_and_b32_e32 v37, 0xffff0000, v37
	v_pk_mul_f32 v[58:59], v[36:37], v[36:37]
	v_add_f32_e32 v49, v54, v55
	v_lshlrev_b32_e32 v60, 16, v38
	v_and_b32_e32 v61, 0xffff0000, v38
	v_add_f32_e32 v49, v58, v49
	v_and_b32_e32 v50, 0xffff0000, v39
	v_lshlrev_b32_e32 v51, 16, v39
	v_pk_mul_f32 v[38:39], v[60:61], v[60:61]
	v_add_f32_e32 v49, v59, v49
	v_add_f32_e32 v38, v38, v49
	s_waitcnt lgkmcnt(0)
	v_pk_mul_f32 v[52:53], v[50:51], v[50:51]
	v_add_f32_e32 v38, v39, v38
	v_add_f32_e32 v38, v53, v38
	v_add_f32_e32 v49, v52, v38
	ds_swizzle_b32 v54, v49 offset:swizzle(SWAP,1)
	v_cndmask_b32_e64 v48, v119, 1.0, s[18:19]
	v_pk_mul_f32 v[38:39], v[48:49], v[46:47] op_sel_hi:[0,1]
	v_cvt_pk_bf16_f32 v52, v38, v39
	v_pk_mul_f32 v[38:39], v[48:49], v[44:45] op_sel_hi:[0,1]
	s_waitcnt lgkmcnt(0)
	v_add_f32_e32 v44, v49, v54
	ds_swizzle_b32 v45, v44 offset:swizzle(SWAP,2)
	v_cvt_pk_bf16_f32 v53, v38, v39
	v_pk_mul_f32 v[38:39], v[48:49], v[40:41] op_sel_hi:[0,1]
	v_cvt_pk_bf16_f32 v54, v38, v39
	v_pk_mul_f32 v[38:39], v[48:49], v[42:43] op_sel_hi:[0,1]
	s_waitcnt lgkmcnt(0)
	v_add_f32_e32 v40, v44, v45
	ds_swizzle_b32 v41, v40 offset:swizzle(SWAP,4)
	v_cvt_pk_bf16_f32 v55, v38, v39
	v_add_u32_e32 v42, s97, v132
	v_mov_b64_e32 v[38:39], s[38:39]
	v_mad_i64_i32 v[58:59], s[20:21], v42, s83, v[38:39]
	s_waitcnt lgkmcnt(0)
	v_add_f32_e32 v38, v40, v41
	v_fmamk_f32 v38, v38, 0x3c800000, v107
	v_mul_f32_e32 v39, 0x4f800000, v38
	v_cmp_gt_f32_e32 vcc, s84, v38
	v_cndmask_b32_e64 v62, 0, v120, s[18:19]
	v_mov_b32_e32 v63, v65
	v_cndmask_b32_e32 v38, v38, v39, vcc
	v_sqrt_f32_e32 v40, v38
	v_cndmask_b32_e64 v39, v9, v13, s[16:17]
	v_add_u32_e32 v41, -1, v40
	v_fma_f32 v42, -v41, v40, v38
	v_cmp_ge_f32_e64 s[18:19], 0, v42
	v_add_u32_e32 v42, 1, v40
	s_nop 0
	v_cndmask_b32_e64 v41, v40, v41, s[18:19]
	v_fma_f32 v40, -v42, v40, v38
	v_cmp_lt_f32_e64 s[18:19], 0, v40
	s_nop 1
	v_cndmask_b32_e64 v40, v41, v42, s[18:19]
	v_mul_f32_e32 v41, 0x37800000, v40
	v_cndmask_b32_e32 v40, v40, v41, vcc
	v_cmp_class_f32_e32 vcc, v38, v108
	v_cndmask_b32_e64 v41, v11, v15, s[16:17]
	s_nop 0
	v_cndmask_b32_e32 v42, v40, v38, vcc
	v_div_scale_f32 v43, s[18:19], v42, v42, 1.0
	v_rcp_f32_e32 v44, v43
	v_cndmask_b32_e64 v38, v8, v12, s[16:17]
	v_cndmask_b32_e64 v40, v10, v14, s[16:17]
	v_fma_f32 v45, -v43, v44, 1.0
	v_fmac_f32_e32 v44, v45, v44
	v_div_scale_f32 v45, vcc, 1.0, v42, 1.0
	v_mul_f32_e32 v46, v45, v44
	v_fma_f32 v47, -v43, v46, v45
	v_fmac_f32_e32 v46, v47, v44
	v_fma_f32 v43, -v43, v46, v45
	v_div_fmas_f32 v43, v43, v44, v46
	v_div_fixup_f32 v44, v43, v42, 1.0
	v_pk_mul_f32 v[42:43], v[44:45], v[56:57] op_sel_hi:[0,1]
	v_pk_mul_f32 v[36:37], v[44:45], v[36:37] op_sel_hi:[0,1]
	v_pk_mul_f32 v[42:43], v[38:39], v[42:43]
	v_pk_mul_f32 v[40:41], v[40:41], v[36:37]
	v_pk_mul_f32 v[36:37], v[44:45], v[60:61] op_sel_hi:[0,1]
	v_cndmask_b32_e64 v39, v1, v5, s[16:17]
	v_cndmask_b32_e64 v38, v0, v4, s[16:17]
	v_pk_mul_f32 v[36:37], v[38:39], v[36:37]
	v_pk_mul_f32 v[38:39], v[44:45], v[50:51] op_sel_hi:[0,1]
	v_cndmask_b32_e64 v45, v3, v7, s[16:17]
	v_cndmask_b32_e64 v44, v2, v6, s[16:17]
	v_pk_mul_f32 v[38:39], v[44:45], v[38:39] op_sel:[0,1] op_sel_hi:[1,0]
	ds_swizzle_b32 v44, v42 offset:swizzle(SWAP,1)
	ds_swizzle_b32 v45, v43 offset:swizzle(SWAP,1)
	ds_swizzle_b32 v46, v40 offset:swizzle(SWAP,1)
	ds_swizzle_b32 v47, v41 offset:swizzle(SWAP,1)
	ds_swizzle_b32 v50, v36 offset:swizzle(SWAP,1)
	ds_swizzle_b32 v51, v37 offset:swizzle(SWAP,1)
	ds_swizzle_b32 v48, v38 offset:swizzle(SWAP,1)
	ds_swizzle_b32 v49, v39 offset:swizzle(SWAP,1)
	v_lshl_add_u64 v[56:57], v[58:59], 0, v[62:63]
	v_lshl_add_u64 v[56:57], v[80:81], 1, v[56:57]
	v_lshl_add_u64 v[56:57], v[56:57], 0, v[64:65]
	global_store_dwordx4 v[56:57], v[52:55], off nt
	s_and_saveexec_b64 s[18:19], s[2:3]
	s_cbranch_execz .LBB0_1596
	v_lshl_add_u32 v60, v131, 6, s60
	ds_read2_b32 v[52:53], v60 offset0:8 offset1:9
	ds_read2_b32 v[54:55], v60 offset0:10 offset1:11
	ds_read2_b32 v[56:57], v60 offset0:12 offset1:13
	ds_read2_b32 v[58:59], v60 offset0:14 offset1:15
	s_waitcnt lgkmcnt(3)
	v_pk_mul_f32 v[44:45], v[52:53], v[44:45]
	s_waitcnt lgkmcnt(2)
	v_pk_mul_f32 v[46:47], v[54:55], v[46:47]
	s_waitcnt lgkmcnt(1)
	v_pk_mul_f32 v[50:51], v[56:57], v[50:51]
	ds_read2_b32 v[52:53], v60 offset1:1
	ds_read2_b32 v[54:55], v60 offset0:2 offset1:3
	ds_read2_b32 v[56:57], v60 offset0:4 offset1:5
	ds_read2_b32 v[60:61], v60 offset0:6 offset1:7
	s_waitcnt lgkmcnt(4)
	v_pk_mul_f32 v[48:49], v[58:59], v[48:49]
	v_cndmask_b32_e64 v45, v45, -v45, s[4:5]
	v_cndmask_b32_e64 v44, v44, -v44, s[4:5]
	v_cndmask_b32_e64 v47, v47, -v47, s[4:5]
	v_cndmask_b32_e64 v46, v46, -v46, s[4:5]
	v_cndmask_b32_e64 v50, v50, -v50, s[4:5]
	v_cndmask_b32_e64 v51, v51, -v51, s[4:5]
	v_cndmask_b32_e64 v48, v48, -v48, s[4:5]
	v_cndmask_b32_e64 v49, v49, -v49, s[4:5]
	s_waitcnt lgkmcnt(0)
	v_pk_fma_f32 v[38:39], v[38:39], v[60:61], v[48:49]
	v_pk_fma_f32 v[36:37], v[36:37], v[56:57], v[50:51]
	v_pk_fma_f32 v[40:41], v[40:41], v[54:55], v[46:47]
	v_pk_fma_f32 v[42:43], v[42:43], v[52:53], v[44:45]
.LBB0_1596:
	s_or_b64 exec, exec, s[18:19]
	s_waitcnt vmcnt(10)
	v_lshlrev_b32_e32 v52, 16, v32
	v_and_b32_e32 v53, 0xffff0000, v32
	s_waitcnt lgkmcnt(2)
	v_pk_mul_f32 v[50:51], v[52:53], v[52:53]
	v_lshlrev_b32_e32 v32, 16, v33
	v_and_b32_e32 v33, 0xffff0000, v33
	v_pk_mul_f32 v[54:55], v[32:33], v[32:33]
	v_add_f32_e32 v45, v50, v51
	v_lshlrev_b32_e32 v56, 16, v34
	v_and_b32_e32 v57, 0xffff0000, v34
	v_add_f32_e32 v45, v54, v45
	v_and_b32_e32 v46, 0xffff0000, v35
	v_lshlrev_b32_e32 v47, 16, v35
	v_pk_mul_f32 v[34:35], v[56:57], v[56:57]
	v_add_f32_e32 v45, v55, v45
	v_add_f32_e32 v34, v34, v45
	s_waitcnt lgkmcnt(0)
	v_pk_mul_f32 v[48:49], v[46:47], v[46:47]
	v_add_f32_e32 v34, v35, v34
	v_add_f32_e32 v34, v49, v34
	v_add_f32_e32 v45, v48, v34
	ds_swizzle_b32 v50, v45 offset:swizzle(SWAP,1)
	v_cndmask_b32_e64 v44, v119, 1.0, s[16:17]
	v_pk_mul_f32 v[34:35], v[44:45], v[42:43] op_sel_hi:[0,1]
	v_cvt_pk_bf16_f32 v48, v34, v35
	v_pk_mul_f32 v[34:35], v[44:45], v[40:41] op_sel_hi:[0,1]
	s_waitcnt lgkmcnt(0)
	v_add_f32_e32 v40, v45, v50
	ds_swizzle_b32 v41, v40 offset:swizzle(SWAP,2)
	v_cvt_pk_bf16_f32 v49, v34, v35
	v_pk_mul_f32 v[34:35], v[44:45], v[36:37] op_sel_hi:[0,1]
	v_cvt_pk_bf16_f32 v50, v34, v35
	v_pk_mul_f32 v[34:35], v[44:45], v[38:39] op_sel_hi:[0,1]
	s_waitcnt lgkmcnt(0)
	v_add_f32_e32 v36, v40, v41
	ds_swizzle_b32 v37, v36 offset:swizzle(SWAP,4)
	v_cvt_pk_bf16_f32 v51, v34, v35
	v_add_u32_e32 v38, s97, v131
	v_mov_b64_e32 v[34:35], s[38:39]
	v_mad_i64_i32 v[54:55], s[18:19], v38, s83, v[34:35]
	s_waitcnt lgkmcnt(0)
	v_add_f32_e32 v34, v36, v37
	v_fmamk_f32 v34, v34, 0x3c800000, v107
	v_mul_f32_e32 v35, 0x4f800000, v34
	v_cmp_gt_f32_e32 vcc, s84, v34
	v_cndmask_b32_e64 v58, 0, v120, s[16:17]
	v_mov_b32_e32 v59, v65
	v_cndmask_b32_e32 v34, v34, v35, vcc
	v_sqrt_f32_e32 v36, v34
	v_cndmask_b32_e64 v35, v9, v13, s[14:15]
	v_add_u32_e32 v37, -1, v36
	v_fma_f32 v38, -v37, v36, v34
	v_cmp_ge_f32_e64 s[16:17], 0, v38
	v_add_u32_e32 v38, 1, v36
	s_nop 0
	v_cndmask_b32_e64 v37, v36, v37, s[16:17]
	v_fma_f32 v36, -v38, v36, v34
	v_cmp_lt_f32_e64 s[16:17], 0, v36
	s_nop 1
	v_cndmask_b32_e64 v36, v37, v38, s[16:17]
	v_mul_f32_e32 v37, 0x37800000, v36
	v_cndmask_b32_e32 v36, v36, v37, vcc
	v_cmp_class_f32_e32 vcc, v34, v108
	v_cndmask_b32_e64 v37, v11, v15, s[14:15]
	s_nop 0
	v_cndmask_b32_e32 v38, v36, v34, vcc
	v_div_scale_f32 v39, s[16:17], v38, v38, 1.0
	v_rcp_f32_e32 v40, v39
	v_cndmask_b32_e64 v34, v8, v12, s[14:15]
	v_cndmask_b32_e64 v36, v10, v14, s[14:15]
	v_fma_f32 v41, -v39, v40, 1.0
	v_fmac_f32_e32 v40, v41, v40
	v_div_scale_f32 v41, vcc, 1.0, v38, 1.0
	v_mul_f32_e32 v42, v41, v40
	v_fma_f32 v43, -v39, v42, v41
	v_fmac_f32_e32 v42, v43, v40
	v_fma_f32 v39, -v39, v42, v41
	v_div_fmas_f32 v39, v39, v40, v42
	v_div_fixup_f32 v40, v39, v38, 1.0
	v_pk_mul_f32 v[38:39], v[40:41], v[52:53] op_sel_hi:[0,1]
	v_pk_mul_f32 v[32:33], v[40:41], v[32:33] op_sel_hi:[0,1]
	v_pk_mul_f32 v[38:39], v[34:35], v[38:39]
	v_pk_mul_f32 v[36:37], v[36:37], v[32:33]
	v_pk_mul_f32 v[32:33], v[40:41], v[56:57] op_sel_hi:[0,1]
	v_cndmask_b32_e64 v35, v1, v5, s[14:15]
	v_cndmask_b32_e64 v34, v0, v4, s[14:15]
	v_pk_mul_f32 v[32:33], v[34:35], v[32:33]
	v_pk_mul_f32 v[34:35], v[40:41], v[46:47] op_sel_hi:[0,1]
	v_cndmask_b32_e64 v41, v3, v7, s[14:15]
	v_cndmask_b32_e64 v40, v2, v6, s[14:15]
	v_pk_mul_f32 v[34:35], v[40:41], v[34:35] op_sel:[0,1] op_sel_hi:[1,0]
	ds_swizzle_b32 v40, v38 offset:swizzle(SWAP,1)
	ds_swizzle_b32 v41, v39 offset:swizzle(SWAP,1)
	ds_swizzle_b32 v42, v36 offset:swizzle(SWAP,1)
	ds_swizzle_b32 v43, v37 offset:swizzle(SWAP,1)
	ds_swizzle_b32 v46, v32 offset:swizzle(SWAP,1)
	ds_swizzle_b32 v47, v33 offset:swizzle(SWAP,1)
	ds_swizzle_b32 v44, v34 offset:swizzle(SWAP,1)
	ds_swizzle_b32 v45, v35 offset:swizzle(SWAP,1)
	v_lshl_add_u64 v[52:53], v[54:55], 0, v[58:59]
	v_lshl_add_u64 v[52:53], v[78:79], 1, v[52:53]
	v_lshl_add_u64 v[52:53], v[52:53], 0, v[64:65]
	global_store_dwordx4 v[52:53], v[48:51], off nt
	s_and_saveexec_b64 s[16:17], s[2:3]
	s_cbranch_execz .LBB0_1598
	v_lshl_add_u32 v56, v130, 6, s60
	ds_read2_b32 v[48:49], v56 offset0:8 offset1:9
	ds_read2_b32 v[50:51], v56 offset0:10 offset1:11
	ds_read2_b32 v[52:53], v56 offset0:12 offset1:13
	ds_read2_b32 v[54:55], v56 offset0:14 offset1:15
	s_waitcnt lgkmcnt(3)
	v_pk_mul_f32 v[40:41], v[48:49], v[40:41]
	s_waitcnt lgkmcnt(2)
	v_pk_mul_f32 v[42:43], v[50:51], v[42:43]
	s_waitcnt lgkmcnt(1)
	v_pk_mul_f32 v[46:47], v[52:53], v[46:47]
	ds_read2_b32 v[48:49], v56 offset1:1
	ds_read2_b32 v[50:51], v56 offset0:2 offset1:3
	ds_read2_b32 v[52:53], v56 offset0:4 offset1:5
	ds_read2_b32 v[56:57], v56 offset0:6 offset1:7
	s_waitcnt lgkmcnt(4)
	v_pk_mul_f32 v[44:45], v[54:55], v[44:45]
	v_cndmask_b32_e64 v41, v41, -v41, s[4:5]
	v_cndmask_b32_e64 v40, v40, -v40, s[4:5]
	v_cndmask_b32_e64 v43, v43, -v43, s[4:5]
	v_cndmask_b32_e64 v42, v42, -v42, s[4:5]
	v_cndmask_b32_e64 v46, v46, -v46, s[4:5]
	v_cndmask_b32_e64 v47, v47, -v47, s[4:5]
	v_cndmask_b32_e64 v44, v44, -v44, s[4:5]
	v_cndmask_b32_e64 v45, v45, -v45, s[4:5]
	s_waitcnt lgkmcnt(0)
	v_pk_fma_f32 v[34:35], v[34:35], v[56:57], v[44:45]
	v_pk_fma_f32 v[32:33], v[32:33], v[52:53], v[46:47]
	v_pk_fma_f32 v[36:37], v[36:37], v[50:51], v[42:43]
	v_pk_fma_f32 v[38:39], v[38:39], v[48:49], v[40:41]
.LBB0_1598:
	s_or_b64 exec, exec, s[16:17]
	s_waitcnt vmcnt(10)
	v_lshlrev_b32_e32 v48, 16, v28
	v_and_b32_e32 v49, 0xffff0000, v28
	s_waitcnt lgkmcnt(2)
	v_pk_mul_f32 v[46:47], v[48:49], v[48:49]
	v_lshlrev_b32_e32 v28, 16, v29
	v_and_b32_e32 v29, 0xffff0000, v29
	v_pk_mul_f32 v[50:51], v[28:29], v[28:29]
	v_add_f32_e32 v41, v46, v47
	v_lshlrev_b32_e32 v52, 16, v30
	v_and_b32_e32 v53, 0xffff0000, v30
	v_add_f32_e32 v41, v50, v41
	v_and_b32_e32 v42, 0xffff0000, v31
	v_lshlrev_b32_e32 v43, 16, v31
	v_pk_mul_f32 v[30:31], v[52:53], v[52:53]
	v_add_f32_e32 v41, v51, v41
	v_add_f32_e32 v30, v30, v41
	s_waitcnt lgkmcnt(0)
	v_pk_mul_f32 v[44:45], v[42:43], v[42:43]
	v_add_f32_e32 v30, v31, v30
	v_add_f32_e32 v30, v45, v30
	v_add_f32_e32 v41, v44, v30
	ds_swizzle_b32 v46, v41 offset:swizzle(SWAP,1)
	v_cndmask_b32_e64 v40, v119, 1.0, s[14:15]
	v_pk_mul_f32 v[30:31], v[40:41], v[38:39] op_sel_hi:[0,1]
	v_cvt_pk_bf16_f32 v44, v30, v31
	v_pk_mul_f32 v[30:31], v[40:41], v[36:37] op_sel_hi:[0,1]
	s_waitcnt lgkmcnt(0)
	v_add_f32_e32 v36, v41, v46
	ds_swizzle_b32 v37, v36 offset:swizzle(SWAP,2)
	v_cvt_pk_bf16_f32 v45, v30, v31
	v_pk_mul_f32 v[30:31], v[40:41], v[32:33] op_sel_hi:[0,1]
	v_cvt_pk_bf16_f32 v46, v30, v31
	v_pk_mul_f32 v[30:31], v[40:41], v[34:35] op_sel_hi:[0,1]
	s_waitcnt lgkmcnt(0)
	v_add_f32_e32 v32, v36, v37
	ds_swizzle_b32 v33, v32 offset:swizzle(SWAP,4)
	v_cvt_pk_bf16_f32 v47, v30, v31
	v_add_u32_e32 v34, s97, v130
	v_mov_b64_e32 v[30:31], s[38:39]
	v_mad_i64_i32 v[50:51], s[16:17], v34, s83, v[30:31]
	s_waitcnt lgkmcnt(0)
	v_add_f32_e32 v30, v32, v33
	v_fmamk_f32 v30, v30, 0x3c800000, v107
	v_mul_f32_e32 v31, 0x4f800000, v30
	v_cmp_gt_f32_e32 vcc, s84, v30
	v_cndmask_b32_e64 v54, 0, v120, s[14:15]
	v_mov_b32_e32 v55, v65
	v_cndmask_b32_e32 v30, v30, v31, vcc
	v_sqrt_f32_e32 v32, v30
	v_cndmask_b32_e64 v31, v9, v13, s[12:13]
	v_add_u32_e32 v33, -1, v32
	v_fma_f32 v34, -v33, v32, v30
	v_cmp_ge_f32_e64 s[14:15], 0, v34
	v_add_u32_e32 v34, 1, v32
	s_nop 0
	v_cndmask_b32_e64 v33, v32, v33, s[14:15]
	v_fma_f32 v32, -v34, v32, v30
	v_cmp_lt_f32_e64 s[14:15], 0, v32
	s_nop 1
	v_cndmask_b32_e64 v32, v33, v34, s[14:15]
	v_mul_f32_e32 v33, 0x37800000, v32
	v_cndmask_b32_e32 v32, v32, v33, vcc
	v_cmp_class_f32_e32 vcc, v30, v108
	v_cndmask_b32_e64 v33, v11, v15, s[12:13]
	s_nop 0
	v_cndmask_b32_e32 v34, v32, v30, vcc
	v_div_scale_f32 v35, s[14:15], v34, v34, 1.0
	v_rcp_f32_e32 v36, v35
	v_cndmask_b32_e64 v30, v8, v12, s[12:13]
	v_cndmask_b32_e64 v32, v10, v14, s[12:13]
	v_fma_f32 v37, -v35, v36, 1.0
	v_fmac_f32_e32 v36, v37, v36
	v_div_scale_f32 v37, vcc, 1.0, v34, 1.0
	v_mul_f32_e32 v38, v37, v36
	v_fma_f32 v39, -v35, v38, v37
	v_fmac_f32_e32 v38, v39, v36
	v_fma_f32 v35, -v35, v38, v37
	v_div_fmas_f32 v35, v35, v36, v38
	v_div_fixup_f32 v36, v35, v34, 1.0
	v_pk_mul_f32 v[34:35], v[36:37], v[48:49] op_sel_hi:[0,1]
	v_pk_mul_f32 v[28:29], v[36:37], v[28:29] op_sel_hi:[0,1]
	v_pk_mul_f32 v[34:35], v[30:31], v[34:35]
	v_pk_mul_f32 v[32:33], v[32:33], v[28:29]
	v_pk_mul_f32 v[28:29], v[36:37], v[52:53] op_sel_hi:[0,1]
	v_cndmask_b32_e64 v31, v1, v5, s[12:13]
	v_cndmask_b32_e64 v30, v0, v4, s[12:13]
	v_pk_mul_f32 v[28:29], v[30:31], v[28:29]
	v_pk_mul_f32 v[30:31], v[36:37], v[42:43] op_sel_hi:[0,1]
	v_cndmask_b32_e64 v37, v3, v7, s[12:13]
	v_cndmask_b32_e64 v36, v2, v6, s[12:13]
	v_pk_mul_f32 v[30:31], v[36:37], v[30:31] op_sel:[0,1] op_sel_hi:[1,0]
	ds_swizzle_b32 v36, v34 offset:swizzle(SWAP,1)
	ds_swizzle_b32 v37, v35 offset:swizzle(SWAP,1)
	ds_swizzle_b32 v38, v32 offset:swizzle(SWAP,1)
	ds_swizzle_b32 v39, v33 offset:swizzle(SWAP,1)
	ds_swizzle_b32 v42, v28 offset:swizzle(SWAP,1)
	ds_swizzle_b32 v43, v29 offset:swizzle(SWAP,1)
	ds_swizzle_b32 v40, v30 offset:swizzle(SWAP,1)
	ds_swizzle_b32 v41, v31 offset:swizzle(SWAP,1)
	v_lshl_add_u64 v[48:49], v[50:51], 0, v[54:55]
	v_lshl_add_u64 v[48:49], v[76:77], 1, v[48:49]
	v_lshl_add_u64 v[48:49], v[48:49], 0, v[64:65]
	global_store_dwordx4 v[48:49], v[44:47], off nt
	s_and_saveexec_b64 s[14:15], s[2:3]
	s_cbranch_execz .LBB0_1600
	v_lshl_add_u32 v52, v129, 6, s60
	ds_read2_b32 v[44:45], v52 offset0:8 offset1:9
	ds_read2_b32 v[46:47], v52 offset0:10 offset1:11
	ds_read2_b32 v[48:49], v52 offset0:12 offset1:13
	ds_read2_b32 v[50:51], v52 offset0:14 offset1:15
	s_waitcnt lgkmcnt(3)
	v_pk_mul_f32 v[36:37], v[44:45], v[36:37]
	s_waitcnt lgkmcnt(2)
	v_pk_mul_f32 v[38:39], v[46:47], v[38:39]
	s_waitcnt lgkmcnt(1)
	v_pk_mul_f32 v[42:43], v[48:49], v[42:43]
	ds_read2_b32 v[44:45], v52 offset1:1
	ds_read2_b32 v[46:47], v52 offset0:2 offset1:3
	ds_read2_b32 v[48:49], v52 offset0:4 offset1:5
	ds_read2_b32 v[52:53], v52 offset0:6 offset1:7
	s_waitcnt lgkmcnt(4)
	v_pk_mul_f32 v[40:41], v[50:51], v[40:41]
	v_cndmask_b32_e64 v37, v37, -v37, s[4:5]
	v_cndmask_b32_e64 v36, v36, -v36, s[4:5]
	v_cndmask_b32_e64 v39, v39, -v39, s[4:5]
	v_cndmask_b32_e64 v38, v38, -v38, s[4:5]
	v_cndmask_b32_e64 v42, v42, -v42, s[4:5]
	v_cndmask_b32_e64 v43, v43, -v43, s[4:5]
	v_cndmask_b32_e64 v40, v40, -v40, s[4:5]
	v_cndmask_b32_e64 v41, v41, -v41, s[4:5]
	s_waitcnt lgkmcnt(0)
	v_pk_fma_f32 v[30:31], v[30:31], v[52:53], v[40:41]
	v_pk_fma_f32 v[28:29], v[28:29], v[48:49], v[42:43]
	v_pk_fma_f32 v[32:33], v[32:33], v[46:47], v[38:39]
	v_pk_fma_f32 v[34:35], v[34:35], v[44:45], v[36:37]
.LBB0_1600:
	s_or_b64 exec, exec, s[14:15]
	s_waitcnt vmcnt(10)
	v_lshlrev_b32_e32 v44, 16, v24
	v_and_b32_e32 v45, 0xffff0000, v24
	s_waitcnt lgkmcnt(2)
	v_pk_mul_f32 v[42:43], v[44:45], v[44:45]
	v_lshlrev_b32_e32 v24, 16, v25
	v_and_b32_e32 v25, 0xffff0000, v25
	v_pk_mul_f32 v[46:47], v[24:25], v[24:25]
	v_add_f32_e32 v37, v42, v43
	v_lshlrev_b32_e32 v48, 16, v26
	v_and_b32_e32 v49, 0xffff0000, v26
	v_add_f32_e32 v37, v46, v37
	v_and_b32_e32 v38, 0xffff0000, v27
	v_lshlrev_b32_e32 v39, 16, v27
	v_pk_mul_f32 v[26:27], v[48:49], v[48:49]
	v_add_f32_e32 v37, v47, v37
	v_add_f32_e32 v26, v26, v37
	s_waitcnt lgkmcnt(0)
	v_pk_mul_f32 v[40:41], v[38:39], v[38:39]
	v_add_f32_e32 v26, v27, v26
	v_add_f32_e32 v26, v41, v26
	v_add_f32_e32 v37, v40, v26
	ds_swizzle_b32 v42, v37 offset:swizzle(SWAP,1)
	v_cndmask_b32_e64 v36, v119, 1.0, s[12:13]
	v_pk_mul_f32 v[26:27], v[36:37], v[34:35] op_sel_hi:[0,1]
	v_cvt_pk_bf16_f32 v40, v26, v27
	v_pk_mul_f32 v[26:27], v[36:37], v[32:33] op_sel_hi:[0,1]
	s_waitcnt lgkmcnt(0)
	v_add_f32_e32 v32, v37, v42
	ds_swizzle_b32 v33, v32 offset:swizzle(SWAP,2)
	v_cvt_pk_bf16_f32 v41, v26, v27
	v_pk_mul_f32 v[26:27], v[36:37], v[28:29] op_sel_hi:[0,1]
	v_cvt_pk_bf16_f32 v42, v26, v27
	v_pk_mul_f32 v[26:27], v[36:37], v[30:31] op_sel_hi:[0,1]
	s_waitcnt lgkmcnt(0)
	v_add_f32_e32 v28, v32, v33
	ds_swizzle_b32 v29, v28 offset:swizzle(SWAP,4)
	v_cvt_pk_bf16_f32 v43, v26, v27
	v_add_u32_e32 v30, s97, v129
	v_mov_b64_e32 v[26:27], s[38:39]
	v_mad_i64_i32 v[46:47], s[14:15], v30, s83, v[26:27]
	s_waitcnt lgkmcnt(0)
	v_add_f32_e32 v26, v28, v29
	v_fmamk_f32 v26, v26, 0x3c800000, v107
	v_mul_f32_e32 v27, 0x4f800000, v26
	v_cmp_gt_f32_e32 vcc, s84, v26
	v_cndmask_b32_e64 v50, 0, v120, s[12:13]
	v_mov_b32_e32 v51, v65
	v_cndmask_b32_e32 v26, v26, v27, vcc
	v_sqrt_f32_e32 v28, v26
	v_cndmask_b32_e64 v27, v9, v13, s[10:11]
	v_add_u32_e32 v29, -1, v28
	v_fma_f32 v30, -v29, v28, v26
	v_cmp_ge_f32_e64 s[12:13], 0, v30
	v_add_u32_e32 v30, 1, v28
	s_nop 0
	v_cndmask_b32_e64 v29, v28, v29, s[12:13]
	v_fma_f32 v28, -v30, v28, v26
	v_cmp_lt_f32_e64 s[12:13], 0, v28
	s_nop 1
	v_cndmask_b32_e64 v28, v29, v30, s[12:13]
	v_mul_f32_e32 v29, 0x37800000, v28
	v_cndmask_b32_e32 v28, v28, v29, vcc
	v_cmp_class_f32_e32 vcc, v26, v108
	v_cndmask_b32_e64 v29, v11, v15, s[10:11]
	s_nop 0
	v_cndmask_b32_e32 v30, v28, v26, vcc
	v_div_scale_f32 v31, s[12:13], v30, v30, 1.0
	v_rcp_f32_e32 v32, v31
	v_cndmask_b32_e64 v26, v8, v12, s[10:11]
	v_cndmask_b32_e64 v28, v10, v14, s[10:11]
	v_fma_f32 v33, -v31, v32, 1.0
	v_fmac_f32_e32 v32, v33, v32
	v_div_scale_f32 v33, vcc, 1.0, v30, 1.0
	v_mul_f32_e32 v34, v33, v32
	v_fma_f32 v35, -v31, v34, v33
	v_fmac_f32_e32 v34, v35, v32
	v_fma_f32 v31, -v31, v34, v33
	v_div_fmas_f32 v31, v31, v32, v34
	v_div_fixup_f32 v32, v31, v30, 1.0
	v_pk_mul_f32 v[30:31], v[32:33], v[44:45] op_sel_hi:[0,1]
	v_pk_mul_f32 v[24:25], v[32:33], v[24:25] op_sel_hi:[0,1]
	v_pk_mul_f32 v[30:31], v[26:27], v[30:31]
	v_pk_mul_f32 v[28:29], v[28:29], v[24:25]
	v_pk_mul_f32 v[24:25], v[32:33], v[48:49] op_sel_hi:[0,1]
	v_cndmask_b32_e64 v27, v1, v5, s[10:11]
	v_cndmask_b32_e64 v26, v0, v4, s[10:11]
	v_pk_mul_f32 v[24:25], v[26:27], v[24:25]
	v_pk_mul_f32 v[26:27], v[32:33], v[38:39] op_sel_hi:[0,1]
	v_cndmask_b32_e64 v33, v3, v7, s[10:11]
	v_cndmask_b32_e64 v32, v2, v6, s[10:11]
	v_pk_mul_f32 v[26:27], v[32:33], v[26:27] op_sel:[0,1] op_sel_hi:[1,0]
	ds_swizzle_b32 v32, v30 offset:swizzle(SWAP,1)
	ds_swizzle_b32 v33, v31 offset:swizzle(SWAP,1)
	ds_swizzle_b32 v34, v28 offset:swizzle(SWAP,1)
	ds_swizzle_b32 v35, v29 offset:swizzle(SWAP,1)
	ds_swizzle_b32 v38, v24 offset:swizzle(SWAP,1)
	ds_swizzle_b32 v39, v25 offset:swizzle(SWAP,1)
	ds_swizzle_b32 v36, v26 offset:swizzle(SWAP,1)
	ds_swizzle_b32 v37, v27 offset:swizzle(SWAP,1)
	v_lshl_add_u64 v[44:45], v[46:47], 0, v[50:51]
	v_lshl_add_u64 v[44:45], v[74:75], 1, v[44:45]
	v_lshl_add_u64 v[44:45], v[44:45], 0, v[64:65]
	global_store_dwordx4 v[44:45], v[40:43], off nt
	s_and_saveexec_b64 s[12:13], s[2:3]
	s_cbranch_execz .LBB0_1602
	v_lshl_add_u32 v48, v128, 6, s60
	ds_read2_b32 v[40:41], v48 offset0:8 offset1:9
	ds_read2_b32 v[42:43], v48 offset0:10 offset1:11
	ds_read2_b32 v[44:45], v48 offset0:12 offset1:13
	ds_read2_b32 v[46:47], v48 offset0:14 offset1:15
	s_waitcnt lgkmcnt(3)
	v_pk_mul_f32 v[32:33], v[40:41], v[32:33]
	s_waitcnt lgkmcnt(2)
	v_pk_mul_f32 v[34:35], v[42:43], v[34:35]
	s_waitcnt lgkmcnt(1)
	v_pk_mul_f32 v[38:39], v[44:45], v[38:39]
	ds_read2_b32 v[40:41], v48 offset1:1
	ds_read2_b32 v[42:43], v48 offset0:2 offset1:3
	ds_read2_b32 v[44:45], v48 offset0:4 offset1:5
	ds_read2_b32 v[48:49], v48 offset0:6 offset1:7
	s_waitcnt lgkmcnt(4)
	v_pk_mul_f32 v[36:37], v[46:47], v[36:37]
	v_cndmask_b32_e64 v33, v33, -v33, s[4:5]
	v_cndmask_b32_e64 v32, v32, -v32, s[4:5]
	v_cndmask_b32_e64 v35, v35, -v35, s[4:5]
	v_cndmask_b32_e64 v34, v34, -v34, s[4:5]
	v_cndmask_b32_e64 v38, v38, -v38, s[4:5]
	v_cndmask_b32_e64 v39, v39, -v39, s[4:5]
	v_cndmask_b32_e64 v36, v36, -v36, s[4:5]
	v_cndmask_b32_e64 v37, v37, -v37, s[4:5]
	s_waitcnt lgkmcnt(0)
	v_pk_fma_f32 v[26:27], v[26:27], v[48:49], v[36:37]
	v_pk_fma_f32 v[24:25], v[24:25], v[44:45], v[38:39]
	v_pk_fma_f32 v[28:29], v[28:29], v[42:43], v[34:35]
	v_pk_fma_f32 v[30:31], v[30:31], v[40:41], v[32:33]
.LBB0_1602:
	s_or_b64 exec, exec, s[12:13]
	s_waitcnt vmcnt(10)
	v_lshlrev_b32_e32 v40, 16, v20
	v_and_b32_e32 v41, 0xffff0000, v20
	s_waitcnt lgkmcnt(2)
	v_pk_mul_f32 v[38:39], v[40:41], v[40:41]
	v_lshlrev_b32_e32 v42, 16, v21
	v_and_b32_e32 v43, 0xffff0000, v21
	v_pk_mul_f32 v[20:21], v[42:43], v[42:43]
	v_add_f32_e32 v33, v38, v39
	v_lshlrev_b32_e32 v44, 16, v22
	v_and_b32_e32 v45, 0xffff0000, v22
	v_add_f32_e32 v20, v20, v33
	v_and_b32_e32 v34, 0xffff0000, v23
	v_lshlrev_b32_e32 v35, 16, v23
	v_pk_mul_f32 v[22:23], v[44:45], v[44:45]
	v_add_f32_e32 v20, v21, v20
	v_add_f32_e32 v20, v22, v20
	s_waitcnt lgkmcnt(0)
	v_pk_mul_f32 v[36:37], v[34:35], v[34:35]
	v_add_f32_e32 v20, v23, v20
	v_add_f32_e32 v20, v37, v20
	v_add_f32_e32 v22, v36, v20
	ds_swizzle_b32 v23, v22 offset:swizzle(SWAP,1)
	v_cndmask_b32_e64 v32, v119, 1.0, s[10:11]
	v_pk_mul_f32 v[20:21], v[32:33], v[30:31] op_sel_hi:[0,1]
	v_cvt_pk_bf16_f32 v36, v20, v21
	v_pk_mul_f32 v[20:21], v[32:33], v[28:29] op_sel_hi:[0,1]
	s_waitcnt lgkmcnt(0)
	v_add_f32_e32 v22, v22, v23
	ds_swizzle_b32 v23, v22 offset:swizzle(SWAP,2)
	v_cvt_pk_bf16_f32 v37, v20, v21
	v_pk_mul_f32 v[20:21], v[32:33], v[24:25] op_sel_hi:[0,1]
	v_cvt_pk_bf16_f32 v38, v20, v21
	v_pk_mul_f32 v[20:21], v[32:33], v[26:27] op_sel_hi:[0,1]
	s_waitcnt lgkmcnt(0)
	v_add_f32_e32 v22, v22, v23
	ds_swizzle_b32 v23, v22 offset:swizzle(SWAP,4)
	v_cvt_pk_bf16_f32 v39, v20, v21
	v_add_u32_e32 v24, s97, v128
	v_mov_b64_e32 v[20:21], s[38:39]
	v_mad_i64_i32 v[46:47], s[12:13], v24, s83, v[20:21]
	s_waitcnt lgkmcnt(0)
	v_add_f32_e32 v20, v22, v23
	v_fmamk_f32 v20, v20, 0x3c800000, v107
	v_mul_f32_e32 v21, 0x4f800000, v20
	v_cmp_gt_f32_e32 vcc, s84, v20
	v_cndmask_b32_e64 v48, 0, v120, s[10:11]
	v_mov_b32_e32 v49, v65
	v_cndmask_b32_e32 v20, v20, v21, vcc
	v_sqrt_f32_e32 v22, v20
	v_cndmask_b32_e64 v21, v9, v13, s[8:9]
	v_add_u32_e32 v23, -1, v22
	v_fma_f32 v24, -v23, v22, v20
	v_cmp_ge_f32_e64 s[10:11], 0, v24
	v_add_u32_e32 v24, 1, v22
	s_nop 0
	v_cndmask_b32_e64 v23, v22, v23, s[10:11]
	v_fma_f32 v22, -v24, v22, v20
	v_cmp_lt_f32_e64 s[10:11], 0, v22
	s_nop 1
	v_cndmask_b32_e64 v22, v23, v24, s[10:11]
	v_mul_f32_e32 v23, 0x37800000, v22
	v_cndmask_b32_e32 v22, v22, v23, vcc
	v_cmp_class_f32_e32 vcc, v20, v108
	v_cndmask_b32_e64 v23, v11, v15, s[8:9]
	s_nop 0
	v_cndmask_b32_e32 v24, v22, v20, vcc
	v_div_scale_f32 v25, s[10:11], v24, v24, 1.0
	v_rcp_f32_e32 v26, v25
	v_cndmask_b32_e64 v20, v8, v12, s[8:9]
	v_cndmask_b32_e64 v22, v10, v14, s[8:9]
	v_fma_f32 v27, -v25, v26, 1.0
	v_fmac_f32_e32 v26, v27, v26
	v_div_scale_f32 v27, vcc, 1.0, v24, 1.0
	v_mul_f32_e32 v28, v27, v26
	v_fma_f32 v29, -v25, v28, v27
	v_fmac_f32_e32 v28, v29, v26
	v_fma_f32 v25, -v25, v28, v27
	v_div_fmas_f32 v25, v25, v26, v28
	v_div_fixup_f32 v24, v25, v24, 1.0
	v_pk_mul_f32 v[26:27], v[24:25], v[40:41] op_sel_hi:[0,1]
	v_pk_mul_f32 v[20:21], v[20:21], v[26:27]
	v_pk_mul_f32 v[26:27], v[24:25], v[42:43] op_sel_hi:[0,1]
	v_pk_mul_f32 v[22:23], v[22:23], v[26:27]
	v_pk_mul_f32 v[26:27], v[24:25], v[44:45] op_sel_hi:[0,1]
	v_cndmask_b32_e64 v29, v1, v5, s[8:9]
	v_cndmask_b32_e64 v28, v0, v4, s[8:9]
	v_pk_mul_f32 v[26:27], v[28:29], v[26:27]
	v_pk_mul_f32 v[24:25], v[24:25], v[34:35] op_sel_hi:[0,1]
	v_cndmask_b32_e64 v29, v3, v7, s[8:9]
	v_cndmask_b32_e64 v28, v2, v6, s[8:9]
	v_pk_mul_f32 v[24:25], v[28:29], v[24:25] op_sel:[0,1] op_sel_hi:[1,0]
	ds_swizzle_b32 v28, v20 offset:swizzle(SWAP,1)
	ds_swizzle_b32 v29, v21 offset:swizzle(SWAP,1)
	ds_swizzle_b32 v30, v22 offset:swizzle(SWAP,1)
	ds_swizzle_b32 v31, v23 offset:swizzle(SWAP,1)
	ds_swizzle_b32 v34, v26 offset:swizzle(SWAP,1)
	ds_swizzle_b32 v35, v27 offset:swizzle(SWAP,1)
	ds_swizzle_b32 v32, v24 offset:swizzle(SWAP,1)
	ds_swizzle_b32 v33, v25 offset:swizzle(SWAP,1)
	v_lshl_add_u64 v[40:41], v[46:47], 0, v[48:49]
	v_lshl_add_u64 v[40:41], v[72:73], 1, v[40:41]
	v_lshl_add_u64 v[40:41], v[40:41], 0, v[64:65]
	global_store_dwordx4 v[40:41], v[36:39], off nt
	s_and_saveexec_b64 s[10:11], s[2:3]
	s_cbranch_execz .LBB0_1604
	v_lshl_add_u32 v44, v127, 6, s60
	ds_read2_b32 v[36:37], v44 offset0:8 offset1:9
	ds_read2_b32 v[38:39], v44 offset0:10 offset1:11
	ds_read2_b32 v[40:41], v44 offset0:12 offset1:13
	ds_read2_b32 v[42:43], v44 offset0:14 offset1:15
	s_waitcnt lgkmcnt(3)
	v_pk_mul_f32 v[28:29], v[36:37], v[28:29]
	s_waitcnt lgkmcnt(2)
	v_pk_mul_f32 v[30:31], v[38:39], v[30:31]
	s_waitcnt lgkmcnt(1)
	v_pk_mul_f32 v[34:35], v[40:41], v[34:35]
	ds_read2_b32 v[36:37], v44 offset1:1
	ds_read2_b32 v[38:39], v44 offset0:2 offset1:3
	ds_read2_b32 v[40:41], v44 offset0:4 offset1:5
	ds_read2_b32 v[44:45], v44 offset0:6 offset1:7
	s_waitcnt lgkmcnt(4)
	v_pk_mul_f32 v[32:33], v[42:43], v[32:33]
	v_cndmask_b32_e64 v29, v29, -v29, s[4:5]
	v_cndmask_b32_e64 v28, v28, -v28, s[4:5]
	v_cndmask_b32_e64 v31, v31, -v31, s[4:5]
	v_cndmask_b32_e64 v30, v30, -v30, s[4:5]
	v_cndmask_b32_e64 v34, v34, -v34, s[4:5]
	v_cndmask_b32_e64 v35, v35, -v35, s[4:5]
	v_cndmask_b32_e64 v32, v32, -v32, s[4:5]
	v_cndmask_b32_e64 v33, v33, -v33, s[4:5]
	s_waitcnt lgkmcnt(0)
	v_pk_fma_f32 v[24:25], v[24:25], v[44:45], v[32:33]
	v_pk_fma_f32 v[26:27], v[26:27], v[40:41], v[34:35]
	v_pk_fma_f32 v[22:23], v[22:23], v[38:39], v[30:31]
	v_pk_fma_f32 v[20:21], v[20:21], v[36:37], v[28:29]
.LBB0_1604:
	s_or_b64 exec, exec, s[10:11]
	s_waitcnt lgkmcnt(7)
	v_cndmask_b32_e64 v28, v119, 1.0, s[8:9]
	s_waitcnt vmcnt(10) lgkmcnt(3)
	v_lshlrev_b32_e32 v34, 16, v16
	s_waitcnt lgkmcnt(2)
	v_and_b32_e32 v35, 0xffff0000, v16
	v_pk_mul_f32 v[20:21], v[28:29], v[20:21] op_sel_hi:[0,1]
	v_pk_mul_f32 v[36:37], v[34:35], v[34:35]
	v_lshlrev_b32_e32 v16, 16, v17
	v_and_b32_e32 v17, 0xffff0000, v17
	v_cvt_pk_bf16_f32 v20, v20, v21
	v_pk_mul_f32 v[38:39], v[16:17], v[16:17]
	v_add_f32_e32 v21, v36, v37
	v_lshlrev_b32_e32 v40, 16, v18
	v_and_b32_e32 v41, 0xffff0000, v18
	v_add_f32_e32 v21, v38, v21
	v_and_b32_e32 v30, 0xffff0000, v19
	v_lshlrev_b32_e32 v31, 16, v19
	v_pk_mul_f32 v[18:19], v[40:41], v[40:41]
	v_add_f32_e32 v21, v39, v21
	v_add_f32_e32 v18, v18, v21
	s_waitcnt lgkmcnt(0)
	v_pk_mul_f32 v[32:33], v[30:31], v[30:31]
	v_add_f32_e32 v18, v19, v18
	v_add_f32_e32 v18, v33, v18
	v_add_f32_e32 v29, v32, v18
	ds_swizzle_b32 v32, v29 offset:swizzle(SWAP,1)
	v_pk_mul_f32 v[18:19], v[28:29], v[22:23] op_sel_hi:[0,1]
	v_cvt_pk_bf16_f32 v21, v18, v19
	v_pk_mul_f32 v[18:19], v[28:29], v[26:27] op_sel_hi:[0,1]
	v_cvt_pk_bf16_f32 v22, v18, v19
	s_waitcnt lgkmcnt(0)
	v_add_f32_e32 v26, v29, v32
	ds_swizzle_b32 v27, v26 offset:swizzle(SWAP,2)
	v_pk_mul_f32 v[18:19], v[28:29], v[24:25] op_sel_hi:[0,1]
	v_cvt_pk_bf16_f32 v23, v18, v19
	v_add_u32_e32 v24, s97, v127
	v_mov_b64_e32 v[18:19], s[38:39]
	s_waitcnt lgkmcnt(0)
	v_add_f32_e32 v25, v26, v27
	ds_swizzle_b32 v26, v25 offset:swizzle(SWAP,4)
	v_mad_i64_i32 v[36:37], s[10:11], v24, s83, v[18:19]
	v_cndmask_b32_e64 v38, 0, v120, s[8:9]
	v_cndmask_b32_e64 v29, v1, v5, s[6:7]
	s_waitcnt lgkmcnt(0)
	v_add_f32_e32 v18, v25, v26
	v_fmamk_f32 v18, v18, 0x3c800000, v107
	v_mul_f32_e32 v19, 0x4f800000, v18
	v_cmp_gt_f32_e32 vcc, s84, v18
	v_cndmask_b32_e64 v25, v11, v15, s[6:7]
	v_mov_b32_e32 v39, v65
	v_cndmask_b32_e32 v24, v18, v19, vcc
	v_sqrt_f32_e32 v26, v24
	v_cndmask_b32_e64 v19, v9, v13, s[6:7]
	v_cndmask_b32_e64 v18, v8, v12, s[6:7]
	v_lshl_add_u64 v[36:37], v[36:37], 0, v[38:39]
	v_add_u32_e32 v27, -1, v26
	v_fma_f32 v28, -v27, v26, v24
	v_cmp_ge_f32_e64 s[8:9], 0, v28
	v_add_u32_e32 v28, 1, v26
	v_lshl_add_u64 v[36:37], v[70:71], 1, v[36:37]
	v_cndmask_b32_e64 v27, v26, v27, s[8:9]
	v_fma_f32 v26, -v28, v26, v24
	v_cmp_lt_f32_e64 s[8:9], 0, v26
	v_lshl_add_u64 v[36:37], v[36:37], 0, v[64:65]
	global_store_dwordx4 v[36:37], v[20:23], off nt
	v_cndmask_b32_e64 v26, v27, v28, s[8:9]
	v_mul_f32_e32 v27, 0x37800000, v26
	v_cndmask_b32_e32 v26, v26, v27, vcc
	v_cmp_class_f32_e32 vcc, v24, v108
	v_cndmask_b32_e64 v28, v0, v4, s[6:7]
	s_nop 0
	v_cndmask_b32_e32 v26, v26, v24, vcc
	v_div_scale_f32 v27, s[8:9], v26, v26, 1.0
	v_rcp_f32_e32 v32, v27
	v_cndmask_b32_e64 v24, v10, v14, s[6:7]
	v_fma_f32 v33, -v27, v32, 1.0
	v_fmac_f32_e32 v32, v33, v32
	v_div_scale_f32 v33, vcc, 1.0, v26, 1.0
	v_mul_f32_e32 v42, v33, v32
	v_fma_f32 v43, -v27, v42, v33
	v_fmac_f32_e32 v42, v43, v32
	v_fma_f32 v27, -v27, v42, v33
	v_div_fmas_f32 v27, v27, v32, v42
	v_div_fixup_f32 v32, v27, v26, 1.0
	v_pk_mul_f32 v[16:17], v[32:33], v[16:17] op_sel_hi:[0,1]
	v_pk_mul_f32 v[26:27], v[32:33], v[34:35] op_sel_hi:[0,1]
	v_pk_mul_f32 v[24:25], v[24:25], v[16:17]
	v_pk_mul_f32 v[16:17], v[32:33], v[40:41] op_sel_hi:[0,1]
	v_pk_mul_f32 v[26:27], v[18:19], v[26:27]
	v_pk_mul_f32 v[16:17], v[28:29], v[16:17]
	v_cndmask_b32_e64 v19, v3, v7, s[6:7]
	v_cndmask_b32_e64 v18, v2, v6, s[6:7]
	v_pk_mul_f32 v[28:29], v[32:33], v[30:31] op_sel_hi:[0,1]
	v_pk_mul_f32 v[18:19], v[18:19], v[28:29] op_sel:[0,1] op_sel_hi:[1,0]
	ds_swizzle_b32 v28, v26 offset:swizzle(SWAP,1)
	ds_swizzle_b32 v29, v27 offset:swizzle(SWAP,1)
	ds_swizzle_b32 v30, v24 offset:swizzle(SWAP,1)
	ds_swizzle_b32 v31, v25 offset:swizzle(SWAP,1)
	ds_swizzle_b32 v34, v16 offset:swizzle(SWAP,1)
	ds_swizzle_b32 v35, v17 offset:swizzle(SWAP,1)
	ds_swizzle_b32 v32, v18 offset:swizzle(SWAP,1)
	ds_swizzle_b32 v33, v19 offset:swizzle(SWAP,1)
	s_and_saveexec_b64 s[8:9], s[2:3]
	s_cbranch_execz .LBB0_1581
	v_lshl_add_u32 v40, v126, 6, s60
	ds_read2_b32 v[20:21], v40 offset0:8 offset1:9
	ds_read2_b32 v[22:23], v40 offset0:10 offset1:11
	ds_read2_b32 v[36:37], v40 offset0:12 offset1:13
	ds_read2_b32 v[38:39], v40 offset0:14 offset1:15
	s_waitcnt lgkmcnt(3)
	v_pk_mul_f32 v[20:21], v[20:21], v[28:29]
	s_waitcnt lgkmcnt(2)
	v_pk_mul_f32 v[22:23], v[22:23], v[30:31]
	s_waitcnt lgkmcnt(1)
	v_pk_mul_f32 v[28:29], v[36:37], v[34:35]
	ds_read2_b32 v[30:31], v40 offset1:1
	ds_read2_b32 v[34:35], v40 offset0:2 offset1:3
	ds_read2_b32 v[36:37], v40 offset0:4 offset1:5
	ds_read2_b32 v[40:41], v40 offset0:6 offset1:7
	s_waitcnt lgkmcnt(4)
	v_pk_mul_f32 v[32:33], v[38:39], v[32:33]
	v_cndmask_b32_e64 v21, v21, -v21, s[4:5]
	v_cndmask_b32_e64 v20, v20, -v20, s[4:5]
	v_cndmask_b32_e64 v23, v23, -v23, s[4:5]
	v_cndmask_b32_e64 v22, v22, -v22, s[4:5]
	v_cndmask_b32_e64 v28, v28, -v28, s[4:5]
	v_cndmask_b32_e64 v29, v29, -v29, s[4:5]
	v_cndmask_b32_e64 v32, v32, -v32, s[4:5]
	v_cndmask_b32_e64 v33, v33, -v33, s[4:5]
	s_waitcnt lgkmcnt(0)
	v_pk_fma_f32 v[18:19], v[18:19], v[40:41], v[32:33]
	v_pk_fma_f32 v[16:17], v[16:17], v[36:37], v[28:29]
	v_pk_fma_f32 v[24:25], v[24:25], v[34:35], v[22:23]
	v_pk_fma_f32 v[26:27], v[26:27], v[30:31], v[20:21]
	s_branch .LBB0_1581

.LBB0_1607:
	s_waitcnt lgkmcnt(0)
	s_barrier
	s_lshl_b32 s6, s22, 2
	v_lshrrev_b32_e32 v2, 3, v67
	v_and_b32_e32 v102, 4, v2
	v_and_b32_e32 v2, 2, v2
	v_bfe_u32 v3, v67, 1, 1
	v_bfe_u32 v64, v67, 2, 2
	v_or3_b32 v123, v2, s6, v3
	v_lshlrev_b32_e32 v2, 3, v67
	v_or_b32_e32 v103, v102, v64
	v_and_b32_e32 v132, 8, v2
	v_bitop3_b32 v2, v102, 63, v64 bitop3:0x36
	v_cndmask_b32_e64 v2, v2, v103, s[2:3]
	v_bitop3_b32 v3, v102, 55, v64 bitop3:0x36
	v_or_b32_e32 v4, 8, v103
	v_lshlrev_b32_e32 v5, 2, v2
	v_cndmask_b32_e64 v3, v3, v4, s[2:3]
	v_lshl_add_u32 v4, v2, 8, s64
	v_and_b32_e32 v5, 12, v5
	v_bfe_u32 v2, v2, 2, 2
	v_bitop3_b32 v2, v5, v123, v2 bitop3:0x36
	v_lshlrev_b32_e32 v2, 4, v2
	v_add3_u32 v8, v4, v2, v132
	v_lshlrev_b32_e32 v2, 2, v3
	v_add3_u32 v12, v0, v1, s10
	v_lshl_add_u32 v4, v3, 8, s64
	v_and_b32_e32 v2, 12, v2
	v_bfe_u32 v3, v3, 2, 2
	v_add_u32_e32 v13, 0x2000, v12
	v_bitop3_b32 v5, v2, v123, v3 bitop3:0x36
	ds_read2_b64 v[0:3], v13 offset0:128 offset1:130
	v_lshlrev_b32_e32 v5, 4, v5
	v_add3_u32 v9, v4, v5, v132
	ds_read_b64_tr_b16 v[4:5], v8 offset:32768
	ds_read_b64_tr_b16 v[6:7], v9 offset:32768
	ds_read_b64_tr_b16 v[10:11], v9
	ds_read_b64_tr_b16 v[8:9], v8
	v_add_u32_e32 v133, 0x4800, v12
	s_waitcnt lgkmcnt(2)
	v_mfma_f32_32x32x16_bf16 v[48:63], v[0:3], v[4:7], 0
	ds_read2_b64 v[0:3], v133 offset1:2
	v_add_u32_e32 v134, 0x3000, v12
	v_or_b32_e32 v124, 16, v103
	v_bitop3_b32 v125, v102, 47, v64 bitop3:0x36
	v_cndmask_b32_e64 v124, v125, v124, s[2:3]
	v_bitop3_b32 v125, v103, 55, 16 bitop3:0x36
	v_or_b32_e32 v126, 24, v103
	s_waitcnt lgkmcnt(0)
	v_mfma_f32_32x32x16_bf16 v[32:47], v[8:11], v[0:3], 0
	ds_read2_b64 v[0:3], v134 offset0:192 offset1:194
	v_lshlrev_b32_e32 v127, 2, v124
	v_cndmask_b32_e64 v125, v125, v126, s[2:3]
	v_lshl_add_u32 v126, v124, 8, s64
	v_and_b32_e32 v127, 12, v127
	v_bfe_u32 v124, v124, 2, 2
	v_bitop3_b32 v124, v127, v123, v124 bitop3:0x36
	v_lshlrev_b32_e32 v124, 4, v124
	v_add3_u32 v128, v126, v124, v132
	v_lshlrev_b32_e32 v126, 2, v125
	v_lshl_add_u32 v124, v125, 8, s64
	v_and_b32_e32 v126, 12, v126
	v_bfe_u32 v125, v125, 2, 2
	v_add_u32_e32 v135, 0x5800, v12
	v_bitop3_b32 v125, v126, v123, v125 bitop3:0x36
	s_waitcnt lgkmcnt(0)
	v_mfma_f32_32x32x16_bf16 v[16:31], v[0:3], v[4:7], 0
	ds_read2_b64 v[0:3], v135 offset0:64 offset1:66
	ds_read2_b64 v[98:101], v13 offset0:132 offset1:134
	v_lshlrev_b32_e32 v125, 4, v125
	v_add3_u32 v129, v124, v125, v132
	ds_read_b64_tr_b16 v[124:125], v128 offset:32768
	ds_read_b64_tr_b16 v[126:127], v129 offset:32768
	ds_read_b64_tr_b16 v[130:131], v129
	ds_read_b64_tr_b16 v[128:129], v128
	s_mov_b32 s48, s21
	s_waitcnt lgkmcnt(2)
	v_mfma_f32_32x32x16_bf16 v[48:63], v[98:101], v[124:127], v[48:63]
	ds_read2_b64 v[98:101], v133 offset0:4 offset1:6
	s_waitcnt lgkmcnt(0)
	v_mfma_f32_32x32x16_bf16 v[32:47], v[128:131], v[98:101], v[32:47]
	ds_read2_b64 v[98:101], v134 offset0:196 offset1:198
	s_nop 7
	v_cvt_pk_bf16_f32 v48, v48, v49
	v_cvt_pk_bf16_f32 v49, v50, v51
	v_cvt_pk_bf16_f32 v50, v52, v53
	v_cvt_pk_bf16_f32 v51, v54, v55
	v_cvt_pk_bf16_f32 v52, v56, v57
	v_cvt_pk_bf16_f32 v53, v58, v59
	v_mfma_f32_32x32x16_bf16 v[0:15], v[8:11], v[0:3], 0
	v_xor_b32_e32 v34, 0x80000000, v34
	v_xor_b32_e32 v35, 0x80000000, v35
	v_xor_b32_e32 v36, 0x80000000, v36
	v_xor_b32_e32 v37, 0x80000000, v37
	v_xor_b32_e32 v33, 0x80000000, v33
	v_xor_b32_e32 v32, 0x80000000, v32
	v_xor_b32_e32 v38, 0x80000000, v38
	s_waitcnt lgkmcnt(0)
	v_mfma_f32_32x32x16_bf16 v[16:31], v[98:101], v[124:127], v[16:31]
	ds_read2_b64 v[98:101], v135 offset0:68 offset1:70
	v_xor_b32_e32 v39, 0x80000000, v39
	v_cvt_pk_bf16_f32 v32, v32, v33
	v_cvt_pk_bf16_f32 v33, v34, v35
	v_cvt_pk_bf16_f32 v34, v36, v37
	v_xor_b32_e32 v40, 0x80000000, v40
	v_xor_b32_e32 v41, 0x80000000, v41
	s_waitcnt lgkmcnt(0)
	v_mfma_f32_32x32x16_bf16 v[0:15], v[128:131], v[98:101], v[0:15]
	v_or_b32_e32 v98, 32, v103
	v_bitop3_b32 v99, v102, 31, v64 bitop3:0x36
	v_cndmask_b32_e64 v98, v99, v98, s[2:3]
	v_bitop3_b32 v99, v103, 55, 32 bitop3:0x36
	v_or_b32_e32 v100, 40, v103
	v_lshlrev_b32_e32 v101, 2, v98
	v_cndmask_b32_e64 v99, v99, v100, s[2:3]
	v_lshl_add_u32 v100, v98, 8, s64
	v_and_b32_e32 v101, 12, v101
	v_bfe_u32 v98, v98, 2, 2
	v_bitop3_b32 v98, v101, v123, v98 bitop3:0x36
	v_lshlrev_b32_e32 v98, 4, v98
	v_add3_u32 v128, v100, v98, v132
	v_lshlrev_b32_e32 v98, 2, v99
	v_lshl_add_u32 v124, v99, 8, s64
	v_and_b32_e32 v98, 12, v98
	v_bfe_u32 v99, v99, 2, 2
	v_bitop3_b32 v125, v98, v123, v99 bitop3:0x36
	ds_read2_b64 v[98:101], v134 offset0:200 offset1:202
	v_lshlrev_b32_e32 v125, 4, v125
	v_add3_u32 v129, v124, v125, v132
	ds_read_b64_tr_b16 v[124:125], v128 offset:32768
	ds_read_b64_tr_b16 v[126:127], v129 offset:32768
	ds_read_b64_tr_b16 v[130:131], v129
	ds_read_b64_tr_b16 v[128:129], v128
	s_waitcnt lgkmcnt(2)
	v_mfma_f32_32x32x16_bf16 v[16:31], v[98:101], v[124:127], v[16:31]
	ds_read2_b64 v[98:101], v135 offset0:72 offset1:74
	v_bitop3_b32 v64, v102, 15, v64 bitop3:0x36
	v_xor_b32_e32 v42, 0x80000000, v42
	v_xor_b32_e32 v43, 0x80000000, v43
	v_xor_b32_e32 v44, 0x80000000, v44
	v_xor_b32_e32 v45, 0x80000000, v45
	v_xor_b32_e32 v46, 0x80000000, v46
	s_waitcnt lgkmcnt(0)
	v_mfma_f32_32x32x16_bf16 v[0:15], v[128:131], v[98:101], v[0:15]
	v_or_b32_e32 v98, 48, v103
	v_cndmask_b32_e64 v64, v64, v98, s[2:3]
	v_bitop3_b32 v98, v103, 55, 48 bitop3:0x36
	v_or_b32_e32 v99, 56, v103
	v_lshlrev_b32_e32 v100, 2, v64
	v_cndmask_b32_e64 v98, v98, v99, s[2:3]
	v_lshl_add_u32 v99, v64, 8, s64
	v_and_b32_e32 v100, 12, v100
	v_bfe_u32 v64, v64, 2, 2
	v_bitop3_b32 v64, v100, v123, v64 bitop3:0x36
	v_lshlrev_b32_e32 v64, 4, v64
	v_add3_u32 v64, v99, v64, v132
	v_lshlrev_b32_e32 v99, 2, v98
	v_lshl_add_u32 v102, v98, 8, s64
	v_and_b32_e32 v99, 12, v99
	v_bfe_u32 v98, v98, 2, 2
	v_bitop3_b32 v103, v99, v123, v98 bitop3:0x36
	ds_read2_b64 v[98:101], v134 offset0:204 offset1:206
	v_lshlrev_b32_e32 v103, 4, v103
	v_add3_u32 v102, v102, v103, v132
	ds_read_b64_tr_b16 v[124:125], v64 offset:32768
	ds_read_b64_tr_b16 v[126:127], v102 offset:32768
	ds_read_b64_tr_b16 v[130:131], v102
	ds_read_b64_tr_b16 v[128:129], v64
	s_waitcnt lgkmcnt(2)
	v_mfma_f32_32x32x16_bf16 v[16:31], v[98:101], v[124:127], v[16:31]
	ds_read2_b64 v[98:101], v135 offset0:76 offset1:78
	v_and_b32_e32 v64, 63, v67
	s_add_u32 s2, s4, 0xe000
	s_addc_u32 s3, s5, 0
	s_lshl_b32 s6, s22, 1
	v_xor_b32_e32 v47, 0x80000000, v47
	v_cvt_pk_bf16_f32 v35, v38, v39
	s_waitcnt lgkmcnt(0)
	v_mfma_f32_32x32x16_bf16 v[0:15], v[128:131], v[98:101], v[0:15]
	v_lshlrev_b32_e32 v99, 4, v64
	v_lshlrev_b32_e32 v98, 5, v64
	v_lshl_or_b32 v64, s22, 11, v99
	v_lshl_add_u64 v[36:37], s[4:5], 0, v[64:65]
	v_lshl_or_b32 v56, s22, 12, v98
	s_or_b32 s6, s6, 1
	v_cvt_pk_bf16_f32 v54, v60, v61
	s_nop 4
	v_xor_b32_e32 v2, 0x80000000, v2
	v_xor_b32_e32 v3, 0x80000000, v3
	v_xor_b32_e32 v4, 0x80000000, v4
	v_xor_b32_e32 v5, 0x80000000, v5
	v_xor_b32_e32 v1, 0x80000000, v1
	v_xor_b32_e32 v0, 0x80000000, v0
	v_xor_b32_e32 v6, 0x80000000, v6
	v_xor_b32_e32 v7, 0x80000000, v7
	v_cvt_pk_bf16_f32 v0, v0, v1
	v_cvt_pk_bf16_f32 v1, v2, v3
	v_cvt_pk_bf16_f32 v2, v4, v5
	v_add_co_u32_e32 v4, vcc, s93, v36
	v_cvt_pk_bf16_f32 v55, v62, v63
	global_store_dwordx4 v56, v[48:51], s[2:3] nt
	global_store_dwordx4 v56, v[52:55], s[2:3] offset:16 nt
	global_store_dwordx4 v64, v[32:35], s[4:5] nt
	v_lshl_or_b32 v38, s6, 10, v99
	v_cvt_pk_bf16_f32 v16, v16, v17
	v_cvt_pk_bf16_f32 v32, v40, v41
	v_cvt_pk_bf16_f32 v33, v42, v43
	v_cvt_pk_bf16_f32 v34, v44, v45
	v_cvt_pk_bf16_f32 v35, v46, v47
	v_cvt_pk_bf16_f32 v17, v18, v19
	v_cvt_pk_bf16_f32 v18, v20, v21
	v_cvt_pk_bf16_f32 v19, v22, v23
	v_cvt_pk_bf16_f32 v20, v24, v25
	v_lshl_or_b32 v24, s6, 11, v98
	v_xor_b32_e32 v8, 0x80000000, v8
	v_xor_b32_e32 v9, 0x80000000, v9
	v_xor_b32_e32 v10, 0x80000000, v10
	v_xor_b32_e32 v11, 0x80000000, v11
	v_xor_b32_e32 v12, 0x80000000, v12
	v_xor_b32_e32 v13, 0x80000000, v13
	v_xor_b32_e32 v14, 0x80000000, v14
	v_xor_b32_e32 v15, 0x80000000, v15
	v_cvt_pk_bf16_f32 v3, v6, v7
	v_addc_co_u32_e32 v5, vcc, 0, v37, vcc
	s_add_i32 s20, s20, 2
	global_store_dwordx4 v38, v[32:35], s[4:5] nt
	v_cvt_pk_bf16_f32 v21, v26, v27
	v_cvt_pk_bf16_f32 v22, v28, v29
	v_cvt_pk_bf16_f32 v23, v30, v31
	global_store_dwordx4 v24, v[16:19], s[2:3] nt
	global_store_dwordx4 v24, v[20:23], s[2:3] offset:16 nt
	global_store_dwordx4 v[4:5], v[0:3], off nt
	s_cmp_eq_u32 s21, 6
	v_mov_b32_e32 v123, v67
	v_cvt_pk_bf16_f32 v0, v8, v9
	v_cvt_pk_bf16_f32 v1, v10, v11
	v_cvt_pk_bf16_f32 v2, v12, v13
	v_cvt_pk_bf16_f32 v3, v14, v15
	global_store_dwordx4 v[4:5], v[0:3], off offset:1024 nt
	s_cbranch_scc1 .LBB0_1573

.LBB0_1683:
	s_or_b64 exec, exec, s[14:15]
	s_and_b64 s[12:13], s[12:13], exec
	s_cselect_b32 s14, 0, 0x1000
	s_and_b64 s[12:13], s[10:11], exec
	s_cselect_b32 s12, 0x800, 0
	s_or_b32 s12, s14, s12
	v_lshl_or_b32 v64, v17, 4, s12
	v_cvt_pk_bf16_f32 v18, v20, v0
	v_cvt_pk_bf16_f32 v20, v1, v4
	v_lshl_add_u64 v[0:1], s[4:5], 0, v[64:65]
	v_lshl_add_u64 v[14:15], v[0:1], 0, s[50:51]
	v_add_co_u32_e32 v0, vcc, s91, v0
	v_cvt_pk_bf16_f32 v19, v19, v2
	s_waitcnt lgkmcnt(0)
	v_cvt_pk_bf16_f32 v21, v3, v6
	v_addc_co_u32_e32 v1, vcc, 0, v1, vcc
	global_store_dwordx4 v[0:1], v[18:21], off nt
	v_cvt_pk_bf16_f32 v0, v5, v8
	v_cvt_pk_bf16_f32 v1, v7, v10
	v_cvt_pk_bf16_f32 v2, v9, v12
	v_cvt_pk_bf16_f32 v3, v11, v13
	global_store_dwordx4 v[14:15], v[0:3], off offset:1024 nt
